# more nt hints: bf16 weight-copy stores, residual loads of the router norm, final-phase loads and output stores
# speedup vs baseline: 1.0157x; 1.0040x over previous
; template <bool BF> __device__ __forceinline__ unsigned pk16(float lo, float hi) { return BF ? pkb(lo, hi) : pkh(lo, hi); }
;     static __device__ __forceinline__ void store(const CvItem& d, int tid, const f32x4 (&v)[2][8]) {
;         const int lane = tid & 63, wave = tid >> 6, kg = lane >> 3, ng = lane & 7; const int nblk = d.N / 128, kb = d.r / nblk, nb = d.r % nblk;
; #pragma unroll
;         for (int t = 0; t < 2; ++t) { const int sb = 2 * wave + t, k0 = 256 * kb + 64 * (sb >> 2) + 8 * kg, n0 = 128 * nb + 32 * (sb & 3) + 4 * ng;
; #pragma unroll
;             for (int j = 0; j < 4; ++j) { u32x4 w; w.x = pk16<MOE_BF16>(v[t][0][j], v[t][1][j]); w.y = pk16<MOE_BF16>(v[t][2][j], v[t][3][j]); w.z = pk16<MOE_BF16>(v[t][4][j], v[t][5][j]); w.w = pk16<MOE_BF16>(v[t][6][j], v[t][7][j]);
;                 const int n = n0 + j, row = d.add >= 0 ? (n >> 7) * 256 + (n & 127) + d.add : n;
;                 *(u32x4*)(d.WT + (size_t)row * d.K + k0) = w; } } }
.LBB0_606:
	s_lshl_b32 s18, s25, 8
	s_add_i32 s1, s18, s1
	s_waitcnt vmcnt(13)
	v_cvt_pk_bf16_f32 v136, v100, v104
	v_add_u32_e32 v100, s1, v214
	v_cndmask_b32_e64 v100, v100, v132, s[8:9]
	v_ashrrev_i32_e32 v104, 31, v100
	s_waitcnt vmcnt(9)
	v_cvt_pk_bf16_f32 v137, v108, v112
	v_mul_lo_u32 v104, s10, v104
	v_mul_lo_u32 v108, s11, v100
	v_mad_u64_u32 v[140:141], s[18:19], s10, v100, 0
	v_add3_u32 v141, v141, v104, v108
	v_lshl_add_u64 v[140:141], v[140:141], 1, s[6:7]
	v_lshlrev_b64 v[142:143], 1, v[134:135]
	s_waitcnt vmcnt(5)
	v_cvt_pk_bf16_f32 v138, v116, v120
	s_waitcnt vmcnt(1)
	v_cvt_pk_bf16_f32 v139, v124, v128
	v_lshl_add_u64 v[134:135], v[140:141], 0, v[142:143]
	global_store_dwordx4 v[134:135], v[136:139], off nt
	v_cvt_pk_bf16_f32 v134, v101, v105
	v_bitop3_b32 v101, v132, s79, 1 bitop3:0xc8
	v_or_b32_e32 v100, 1, v132
	v_add_u32_e32 v101, s1, v101
	v_cndmask_b32_e64 v100, v101, v100, s[8:9]
	v_ashrrev_i32_e32 v101, 31, v100
	v_mul_lo_u32 v104, s10, v101
	v_mul_lo_u32 v105, s11, v100
	v_mad_u64_u32 v[100:101], s[18:19], s10, v100, 0
	v_add3_u32 v101, v101, v104, v105
	v_lshl_add_u64 v[100:101], v[100:101], 1, s[6:7]
	v_cvt_pk_bf16_f32 v135, v109, v113
	v_cvt_pk_bf16_f32 v136, v117, v121
	v_cvt_pk_bf16_f32 v137, v125, v129
	v_lshl_add_u64 v[100:101], v[100:101], 0, v[142:143]
	s_movk_i32 s18, 0x5e
	global_store_dwordx4 v[100:101], v[134:137], off nt
	v_bitop3_b32 v101, v132, s18, 2 bitop3:0xc8
	v_or_b32_e32 v100, 2, v132
	v_add_u32_e32 v101, s1, v101
	v_cndmask_b32_e64 v100, v101, v100, s[8:9]
	v_ashrrev_i32_e32 v101, 31, v100
	v_cvt_pk_bf16_f32 v134, v102, v106
	v_mul_lo_u32 v102, s10, v101
	v_mul_lo_u32 v104, s11, v100
	v_mad_u64_u32 v[100:101], s[18:19], s10, v100, 0
	s_movk_i32 s18, 0x5f
	s_nop 0
	v_bitop3_b32 v105, v132, s18, 3 bitop3:0xc8
	v_add3_u32 v101, v101, v102, v104
	v_or_b32_e32 v104, 3, v132
	v_add_u32_e32 v105, s1, v105
	v_lshl_add_u64 v[100:101], v[100:101], 1, s[6:7]
	v_cndmask_b32_e64 v104, v105, v104, s[8:9]
	v_cvt_pk_bf16_f32 v135, v110, v114
	v_cvt_pk_bf16_f32 v136, v118, v122
	v_cvt_pk_bf16_f32 v137, v126, v130
	v_lshl_add_u64 v[100:101], v[100:101], 0, v[142:143]
	v_ashrrev_i32_e32 v105, 31, v104
	global_store_dwordx4 v[100:101], v[134:137], off nt
	v_cvt_pk_bf16_f32 v100, v103, v107
	v_mul_lo_u32 v106, s10, v105
	v_mul_lo_u32 v107, s11, v104
	v_mad_u64_u32 v[104:105], s[18:19], s10, v104, 0
	v_add3_u32 v105, v105, v106, v107
	v_lshl_add_u64 v[104:105], v[104:105], 1, s[6:7]
	v_cvt_pk_bf16_f32 v101, v111, v115
	v_cvt_pk_bf16_f32 v102, v119, v123
	v_cvt_pk_bf16_f32 v103, v127, v131
	v_lshl_add_u64 v[104:105], v[104:105], 0, v[142:143]
	s_movk_i32 s18, 0x7c
	global_store_dwordx4 v[104:105], v[100:103], off nt
	v_or_b32_e32 v133, 32, v132
	s_and_b64 vcc, exec, s[4:5]
	v_cvt_pk_bf16_f32 v100, v68, v72
	v_bitop3_b32 v68, v132, s18, 32 bitop3:0xc8
	v_add_u32_e32 v68, s1, v68
	v_cndmask_b32_e64 v68, v68, v133, s[8:9]
	v_ashrrev_i32_e32 v72, 31, v68
	v_cvt_pk_bf16_f32 v101, v76, v80
	v_mul_lo_u32 v72, s10, v72
	v_mul_lo_u32 v76, s11, v68
	v_mad_u64_u32 v[104:105], s[18:19], s10, v68, 0
	v_add3_u32 v105, v105, v72, v76
	v_lshl_add_u64 v[104:105], v[104:105], 1, s[6:7]
	v_cvt_pk_bf16_f32 v102, v84, v88
	s_waitcnt vmcnt(4)
	v_cvt_pk_bf16_f32 v103, v92, v96
	v_lshl_add_u64 v[104:105], v[104:105], 0, v[142:143]
	s_movk_i32 s18, 0x7d
	global_store_dwordx4 v[104:105], v[100:103], off nt
	v_or_b32_e32 v68, 33, v132
	s_nop 0
	v_cvt_pk_bf16_f32 v100, v69, v73
	v_bitop3_b32 v69, v132, s18, 33 bitop3:0xc8
	v_add_u32_e32 v69, s1, v69
	v_cndmask_b32_e64 v68, v69, v68, s[8:9]
	v_ashrrev_i32_e32 v69, 31, v68
	v_mul_lo_u32 v72, s10, v69
	v_mul_lo_u32 v73, s11, v68
	v_mad_u64_u32 v[68:69], s[18:19], s10, v68, 0
	v_add3_u32 v69, v69, v72, v73
	v_lshl_add_u64 v[68:69], v[68:69], 1, s[6:7]
	v_cvt_pk_bf16_f32 v101, v77, v81
	v_cvt_pk_bf16_f32 v102, v85, v89
	v_cvt_pk_bf16_f32 v103, v93, v97
	v_lshl_add_u64 v[68:69], v[68:69], 0, v[142:143]
	s_movk_i32 s18, 0x7e
	global_store_dwordx4 v[68:69], v[100:103], off nt
	v_bitop3_b32 v69, v132, s18, 34 bitop3:0xc8
	v_or_b32_e32 v68, 34, v132
	v_add_u32_e32 v69, s1, v69
	v_cndmask_b32_e64 v68, v69, v68, s[8:9]
	v_ashrrev_i32_e32 v69, 31, v68
	v_cvt_pk_bf16_f32 v100, v70, v74
	v_mul_lo_u32 v70, s10, v69
	v_mul_lo_u32 v72, s11, v68
	v_mad_u64_u32 v[68:69], s[18:19], s10, v68, 0
	s_movk_i32 s18, 0x7f
	s_nop 0
	v_bitop3_b32 v73, v132, s18, 35 bitop3:0xc8
	v_add3_u32 v69, v69, v70, v72
	v_or_b32_e32 v72, 35, v132
	v_add_u32_e32 v73, s1, v73
	v_lshl_add_u64 v[68:69], v[68:69], 1, s[6:7]
	v_cndmask_b32_e64 v72, v73, v72, s[8:9]
	v_cvt_pk_bf16_f32 v101, v78, v82
	v_cvt_pk_bf16_f32 v102, v86, v90
	v_cvt_pk_bf16_f32 v103, v94, v98
	v_lshl_add_u64 v[68:69], v[68:69], 0, v[142:143]
	v_ashrrev_i32_e32 v73, 31, v72
	global_store_dwordx4 v[68:69], v[100:103], off nt
	v_cvt_pk_bf16_f32 v68, v71, v75
	v_mul_lo_u32 v74, s10, v73
	v_mul_lo_u32 v75, s11, v72
	v_mad_u64_u32 v[72:73], s[8:9], s10, v72, 0
	v_add3_u32 v73, v73, v74, v75
	v_lshl_add_u64 v[72:73], v[72:73], 1, s[6:7]
	v_cvt_pk_bf16_f32 v69, v79, v83
	v_cvt_pk_bf16_f32 v70, v87, v91
	v_cvt_pk_bf16_f32 v71, v95, v99
	v_lshl_add_u64 v[72:73], v[72:73], 0, v[142:143]
	global_store_dwordx4 v[72:73], v[68:71], off nt
	s_cbranch_vccnz .LBB0_589
; template <bool BF> __device__ __forceinline__ unsigned pk16(float lo, float hi) { return BF ? pkb(lo, hi) : pkh(lo, hi); }
;     static __device__ __forceinline__ void store(const CvItem& d, int tid, const f32x4 (&v)[2][8]) {
;         const int lane = tid & 63, wave = tid >> 6, kg = lane >> 3, ng = lane & 7; const int nblk = d.N / 128, kb = d.r / nblk, nb = d.r % nblk;
; #pragma unroll
;         for (int t = 0; t < 2; ++t) { const int sb = 2 * wave + t, k0 = 256 * kb + 64 * (sb >> 2) + 8 * kg, n0 = 128 * nb + 32 * (sb & 3) + 4 * ng;
; #pragma unroll
;             for (int j = 0; j < 4; ++j) { u32x4 w; w.x = pk16<MOE_BF16>(v[t][0][j], v[t][1][j]); w.y = pk16<MOE_BF16>(v[t][2][j], v[t][3][j]); w.z = pk16<MOE_BF16>(v[t][4][j], v[t][5][j]); w.w = pk16<MOE_BF16>(v[t][6][j], v[t][7][j]);
;                 const int n = n0 + j, row = d.add >= 0 ? (n >> 7) * 256 + (n & 127) + d.add : n;
;                 *(u32x4*)(d.WT + (size_t)row * d.K + k0) = w; } } }
;     __device__ __forceinline__ void run_all(int tid) const {
;     ...
;             if (two) store(d1, tid, vb); }
	s_lshr_b32 s1, s24, 7
	v_cvt_f32_i32_e32 v68, s1
	s_ashr_i32 s4, s20, 30
	s_or_b32 s6, s4, 1
	v_cvt_pk_bf16_f32 v70, v48, v52
	v_rcp_iflag_f32_e32 v69, v68
	v_cvt_pk_bf16_f32 v71, v60, v64
	v_mul_f32_e32 v69, v2, v69
	v_trunc_f32_e32 v69, v69
	v_fma_f32 v2, -v69, v68, v2
	v_cvt_i32_f32_e32 v69, v69
	v_cmp_ge_f32_e64 s[4:5], |v2|, v68
	s_and_b64 s[4:5], s[4:5], exec
	s_cselect_b32 s4, s6, 0
	v_add_u32_e32 v2, s4, v69
	v_bfe_i32 v68, v2, 0, 16
	v_mul_lo_u32 v2, v2, s1
	v_sub_u32_e32 v2, s3, v2
	v_bfe_i32 v2, v2, 0, 16
	v_lshl_or_b32 v76, v2, 7, v214
	v_lshlrev_b32_e32 v2, 8, v2
	v_add_u32_e32 v2, s23, v2
	v_add_u32_e32 v74, v2, v214
	v_cndmask_b32_e64 v74, v74, v76, s[14:15]
	v_ashrrev_i32_e32 v75, 31, v74
	v_lshl_or_b32 v72, v68, 8, v213
	v_mul_lo_u32 v77, s16, v75
	v_mul_lo_u32 v78, s17, v74
	v_mad_u64_u32 v[74:75], s[4:5], s16, v74, 0
	v_ashrrev_i32_e32 v73, 31, v72
	v_add3_u32 v75, v75, v77, v78
	v_lshl_add_u64 v[74:75], v[74:75], 1, s[12:13]
	v_lshlrev_b64 v[72:73], 1, v[72:73]
	v_cvt_pk_bf16_f32 v68, v16, v36
	v_cvt_pk_bf16_f32 v69, v44, v56
	v_lshl_add_u64 v[74:75], v[74:75], 0, v[72:73]
	global_store_dwordx4 v[74:75], v[68:71], off nt
	v_bitop3_b32 v75, v76, s79, 1 bitop3:0xc8
	v_or_b32_e32 v74, 1, v76
	v_add_u32_e32 v75, v75, v2
	v_cndmask_b32_e64 v74, v75, v74, s[14:15]
	v_ashrrev_i32_e32 v75, 31, v74
	v_mul_lo_u32 v77, s16, v75
	v_mul_lo_u32 v78, s17, v74
	v_mad_u64_u32 v[74:75], s[4:5], s16, v74, 0
	v_add3_u32 v75, v75, v77, v78
	v_lshl_add_u64 v[74:75], v[74:75], 1, s[12:13]
	v_cvt_pk_bf16_f32 v68, v17, v37
	v_cvt_pk_bf16_f32 v69, v45, v57
	v_cvt_pk_bf16_f32 v70, v49, v53
	v_cvt_pk_bf16_f32 v71, v61, v65
	v_lshl_add_u64 v[74:75], v[74:75], 0, v[72:73]
	s_movk_i32 s1, 0x5e
	global_store_dwordx4 v[74:75], v[68:71], off nt
	v_bitop3_b32 v75, v76, s1, 2 bitop3:0xc8
	v_or_b32_e32 v74, 2, v76
	v_add_u32_e32 v75, v75, v2
	v_cndmask_b32_e64 v74, v75, v74, s[14:15]
	v_ashrrev_i32_e32 v75, 31, v74
	v_mul_lo_u32 v77, s16, v75
	v_mul_lo_u32 v78, s17, v74
	v_mad_u64_u32 v[74:75], s[4:5], s16, v74, 0
	v_add3_u32 v75, v75, v77, v78
	v_lshl_add_u64 v[74:75], v[74:75], 1, s[12:13]
	v_cvt_pk_bf16_f32 v68, v18, v38
	v_cvt_pk_bf16_f32 v69, v46, v58
	v_cvt_pk_bf16_f32 v70, v50, v54
	v_cvt_pk_bf16_f32 v71, v62, v66
	v_lshl_add_u64 v[74:75], v[74:75], 0, v[72:73]
	s_movk_i32 s1, 0x5f
	global_store_dwordx4 v[74:75], v[68:71], off nt
	v_bitop3_b32 v75, v76, s1, 3 bitop3:0xc8
	v_or_b32_e32 v74, 3, v76
	v_add_u32_e32 v75, v75, v2
	v_cndmask_b32_e64 v74, v75, v74, s[14:15]
	v_ashrrev_i32_e32 v75, 31, v74
	v_mul_lo_u32 v77, s16, v75
	v_mul_lo_u32 v78, s17, v74
	v_mad_u64_u32 v[74:75], s[4:5], s16, v74, 0
	v_add3_u32 v75, v75, v77, v78
	v_lshl_add_u64 v[74:75], v[74:75], 1, s[12:13]
	v_cvt_pk_bf16_f32 v68, v19, v39
	v_cvt_pk_bf16_f32 v69, v47, v59
	v_cvt_pk_bf16_f32 v70, v51, v55
	v_cvt_pk_bf16_f32 v71, v63, v67
	v_lshl_add_u64 v[74:75], v[74:75], 0, v[72:73]
	s_movk_i32 s1, 0x7c
	global_store_dwordx4 v[74:75], v[68:71], off nt
	v_bitop3_b32 v75, v76, s1, 32 bitop3:0xc8
	v_or_b32_e32 v74, 32, v76
	v_add_u32_e32 v75, v75, v2
	v_cndmask_b32_e64 v74, v75, v74, s[14:15]
	v_ashrrev_i32_e32 v75, 31, v74
	v_mul_lo_u32 v77, s16, v75
	v_mul_lo_u32 v78, s17, v74
	v_mad_u64_u32 v[74:75], s[4:5], s16, v74, 0
	v_add3_u32 v75, v75, v77, v78
	v_lshl_add_u64 v[74:75], v[74:75], 1, s[12:13]
	v_cvt_pk_bf16_f32 v68, v4, v8
	v_cvt_pk_bf16_f32 v69, v12, v20
	v_cvt_pk_bf16_f32 v70, v24, v28
	v_cvt_pk_bf16_f32 v71, v32, v40
	v_lshl_add_u64 v[74:75], v[74:75], 0, v[72:73]
	s_movk_i32 s1, 0x7d
	global_store_dwordx4 v[74:75], v[68:71], off nt
	v_bitop3_b32 v75, v76, s1, 33 bitop3:0xc8
	v_or_b32_e32 v74, 33, v76
	v_add_u32_e32 v75, v75, v2
	v_cndmask_b32_e64 v74, v75, v74, s[14:15]
	v_ashrrev_i32_e32 v75, 31, v74
	v_mul_lo_u32 v77, s16, v75
	v_mul_lo_u32 v78, s17, v74
	v_mad_u64_u32 v[74:75], s[4:5], s16, v74, 0
	v_add3_u32 v75, v75, v77, v78
	v_lshl_add_u64 v[74:75], v[74:75], 1, s[12:13]
	v_cvt_pk_bf16_f32 v68, v5, v9
	v_cvt_pk_bf16_f32 v69, v13, v21
	v_cvt_pk_bf16_f32 v70, v25, v29
	v_cvt_pk_bf16_f32 v71, v33, v41
	v_lshl_add_u64 v[74:75], v[74:75], 0, v[72:73]
	s_movk_i32 s1, 0x7e
	global_store_dwordx4 v[74:75], v[68:71], off nt
	v_bitop3_b32 v75, v76, s1, 34 bitop3:0xc8
	v_or_b32_e32 v74, 34, v76
	v_add_u32_e32 v75, v75, v2
	v_cndmask_b32_e64 v74, v75, v74, s[14:15]
	v_ashrrev_i32_e32 v75, 31, v74
	v_mul_lo_u32 v77, s16, v75
	v_mul_lo_u32 v78, s17, v74
	v_mad_u64_u32 v[74:75], s[4:5], s16, v74, 0
	v_add3_u32 v75, v75, v77, v78
	v_lshl_add_u64 v[74:75], v[74:75], 1, s[12:13]
	v_cvt_pk_bf16_f32 v68, v6, v10
	v_cvt_pk_bf16_f32 v69, v14, v22
	v_cvt_pk_bf16_f32 v70, v26, v30
	v_cvt_pk_bf16_f32 v71, v34, v42
	v_lshl_add_u64 v[74:75], v[74:75], 0, v[72:73]
	s_movk_i32 s1, 0x7f
	global_store_dwordx4 v[74:75], v[68:71], off nt
	v_bitop3_b32 v75, v76, s1, 35 bitop3:0xc8
	v_or_b32_e32 v74, 35, v76
	v_add_u32_e32 v2, v75, v2
	v_cndmask_b32_e64 v2, v2, v74, s[14:15]
	v_ashrrev_i32_e32 v74, 31, v2
	v_mul_lo_u32 v76, s16, v74
	v_mul_lo_u32 v77, s17, v2
	v_mad_u64_u32 v[74:75], s[4:5], s16, v2, 0
	v_add3_u32 v75, v75, v76, v77
	v_lshl_add_u64 v[74:75], v[74:75], 1, s[12:13]
	v_cvt_pk_bf16_f32 v68, v7, v11
	v_cvt_pk_bf16_f32 v69, v15, v23
	v_cvt_pk_bf16_f32 v70, v27, v31
	v_cvt_pk_bf16_f32 v71, v35, v43
	v_lshl_add_u64 v[72:73], v[74:75], 0, v[72:73]
	global_store_dwordx4 v[72:73], v[68:71], off nt
	s_branch .LBB0_589

; #define LAS __attribute__((address_space(3)))
; template <int R, bool RT = false>
; __device__ __forceinline__ void norm_phase(const NormArgs& a, LAS unsigned char* lds, bool ctx_rows, const float* ctx_src, const float* ctx_shift, const float* ctx_scale) {
;     ...
;         for (int j = 0; j < 4; ++j) { const int c = 4 * lane + 256 * j; const f32x4 g = *(const f32x4*)(a.gain + c);
;             if (a.shift) { const f32x4 sc = *(const f32x4*)(a.scale + (size_t)b * a.mstride + c); A[j] = g * (sc + 1.f); Sh[j] = *(const f32x4*)(a.shift + (size_t)b * a.mstride + c); }
;     ...
;             for (int q = 0; q < R; ++q) { const int row = row0 + rr + q;
;                 if (a.src16) { const f16* xr = a.src16 + (size_t)row * DM;
; #pragma unroll
;                     for (int j = 0; j < 4; ++j) { const f16x4 t = *(const f16x4*)(xr + 4 * lane + 256 * j); v[q][j] = (f32x4){(float)t[0], (float)t[1], (float)t[2], (float)t[3]};
;                         if constexpr (RT) { if (j == 0) *(LAS u32x2*)(hs + (rr + q) * 528 + 8 * lane) = __builtin_bit_cast(u32x2, t);
;                             else xp[rr / 4][q][j - 1] = __builtin_bit_cast(u32x2, t); } } }
;                 else { const float* xr = a.src + (size_t)row * DM;
; #pragma unroll
;                     for (int j = 0; j < 4; ++j) v[q][j] = *(const f32x4*)(xr + 4 * lane + 256 * j); } }
;             if (a.y2) {
;                 unsigned long long mask[R]; int ee[R][4]; float wgt[R][4]; f16x4 ld[R][4][4];
;                 int cnt[R];
; #pragma unroll
;                 for (int q = 0; q < R; ++q) { mask[q] = __ballot(sl[q] >= 0); cnt[q] = __builtin_popcountll(mask[q]);
; #pragma unroll
;                     for (int i = 0; i < 4; ++i) { if (mask[q]) { ee[q][i] = __builtin_ctzll(mask[q]); mask[q] &= mask[q] - 1; wgt[q][i] = 1.f; } else { ee[q][i] = i ? ee[q][0] : 0; wgt[q][i] = 0.f; } }
; #pragma unroll
;                     for (int i = 0; i < 4; ++i) {
;                         if (i < cnt[q]) { int slot = __shfl(sl[q], ee[q][i]); slot = slot < 0 ? 0 : slot; const f16* yr = a.y2 + ((size_t)ee[q][i] * EROWS + b * CAP + slot) * DM + 4 * lane;
; #pragma unroll
;                             for (int j = 0; j < 4; ++j) ld[q][i][j] = *(const f16x4*)(yr + 256 * j); } } }
; #pragma unroll
;                 for (int q = 0; q < R; ++q) { const int row = row0 + rr + q;
;                     f32x4 cs[4];
; #pragma unroll
.LBB0_808:
	s_ashr_i32 s0, s34, 31
	s_lshr_b32 s0, s0, 25
	s_add_i32 s0, s34, s0
	s_ashr_i32 s22, s0, 7
	v_mad_i64_i32 v[32:33], s[2:3], s22, v209, v[28:29]
	global_load_dwordx4 v[6:9], v[32:33], off
	global_load_dwordx4 v[2:5], v[20:21], off
	v_mad_i64_i32 v[38:39], s[2:3], s22, v209, v[30:31]
	s_add_i32 s24, s14, 1
	s_ashr_i32 s15, s14, 31
	s_ashr_i32 s25, s24, 31
	s_lshl_b64 s[2:3], s[14:15], 11
	s_lshl_b64 s[24:25], s[24:25], 11
	v_lshl_add_u64 v[60:61], v[22:23], 0, s[24:25]
	s_add_i32 s28, s14, 3
	s_add_i32 s26, s14, 2
	s_ashr_i32 s29, s28, 31
	s_ashr_i32 s27, s26, 31
	s_lshl_b64 s[28:29], s[28:29], 11
	s_lshl_b64 s[26:27], s[26:27], 11
	v_lshl_add_u64 v[130:131], v[22:23], 0, s[28:29]
	v_cmp_lt_i32_e32 vcc, v222, v221
	s_ashr_i32 s23, s22, 31
	s_waitcnt vmcnt(0)
	v_pk_add_f32 v[8:9], v[8:9], 1.0 op_sel_hi:[1,0]
	v_pk_add_f32 v[6:7], v[6:7], 1.0 op_sel_hi:[1,0]
	v_pk_mul_f32 v[34:35], v[4:5], v[8:9]
	v_pk_mul_f32 v[36:37], v[2:3], v[6:7]
	global_load_dwordx4 v[2:5], v[38:39], off
	global_load_dwordx4 v[6:9], v[20:21], off offset:1024
	global_load_dwordx4 v[10:13], v[32:33], off offset:1024
	s_waitcnt vmcnt(0)
	v_pk_add_f32 v[12:13], v[12:13], 1.0 op_sel_hi:[1,0]
	v_pk_add_f32 v[10:11], v[10:11], 1.0 op_sel_hi:[1,0]
	v_pk_mul_f32 v[40:41], v[8:9], v[12:13]
	v_pk_mul_f32 v[42:43], v[6:7], v[10:11]
	global_load_dwordx4 v[6:9], v[38:39], off offset:1024
	global_load_dwordx4 v[10:13], v[20:21], off offset:2048
	global_load_dwordx4 v[14:17], v[32:33], off offset:2048
	s_waitcnt vmcnt(0)
	v_pk_add_f32 v[16:17], v[16:17], 1.0 op_sel_hi:[1,0]
	v_pk_add_f32 v[14:15], v[14:15], 1.0 op_sel_hi:[1,0]
	v_pk_mul_f32 v[44:45], v[12:13], v[16:17]
	v_pk_mul_f32 v[46:47], v[10:11], v[14:15]
	global_load_dwordx4 v[10:13], v[38:39], off offset:2048
	global_load_dwordx4 v[14:17], v[20:21], off offset:3072
	global_load_dwordx4 v[48:51], v[32:33], off offset:3072
	s_waitcnt vmcnt(0)
	v_pk_add_f32 v[32:33], v[50:51], 1.0 op_sel_hi:[1,0]
	v_pk_add_f32 v[48:49], v[48:49], 1.0 op_sel_hi:[1,0]
	v_pk_mul_f32 v[52:53], v[16:17], v[32:33]
	v_pk_mul_f32 v[54:55], v[14:15], v[48:49]
	global_load_dwordx4 v[14:17], v[38:39], off offset:3072
	v_lshl_add_u64 v[32:33], v[22:23], 0, s[2:3]
	global_load_dwordx2 v[50:51], v[32:33], off nt
	global_load_dwordx2 v[48:49], v[32:33], off offset:512 nt
	global_load_dwordx2 v[38:39], v[32:33], off offset:1024 nt
	global_load_dwordx2 v[56:57], v[60:61], off nt
	global_load_dwordx2 v[58:59], v[60:61], off offset:512 nt
	global_load_dwordx2 v[68:69], v[130:131], off nt
	global_load_dwordx2 v[70:71], v[130:131], off offset:512 nt
	s_waitcnt vmcnt(6)
	v_cvt_f32_f16_e32 v72, v50
	v_cvt_f32_f16_sdwa v73, v50 dst_sel:DWORD dst_unused:UNUSED_PAD src0_sel:WORD_1
	v_cvt_f32_f16_e32 v76, v51
	v_cvt_f32_f16_sdwa v77, v51 dst_sel:DWORD dst_unused:UNUSED_PAD src0_sel:WORD_1
	s_waitcnt vmcnt(3)
	v_cvt_f32_f16_e32 v88, v56
	v_cvt_f32_f16_sdwa v89, v56 dst_sel:DWORD dst_unused:UNUSED_PAD src0_sel:WORD_1
	v_cvt_f32_f16_e32 v90, v57
	v_cvt_f32_f16_sdwa v91, v57 dst_sel:DWORD dst_unused:UNUSED_PAD src0_sel:WORD_1
	ds_write2_b64 v211, v[50:51], v[56:57] offset1:66
	global_load_dwordx2 v[56:57], v[60:61], off offset:1024 nt
	global_load_dwordx2 v[50:51], v[60:61], off offset:1536 nt
	v_lshl_add_u64 v[60:61], v[22:23], 0, s[26:27]
	global_load_dwordx2 v[32:33], v[32:33], off offset:1536 nt
	v_cvt_f32_f16_e32 v74, v48
	global_load_dwordx2 v[66:67], v[60:61], off nt
	global_load_dwordx2 v[64:65], v[60:61], off offset:512 nt
	global_load_dwordx2 v[62:63], v[60:61], off offset:1024 nt
	v_cvt_f32_f16_sdwa v75, v48 dst_sel:DWORD dst_unused:UNUSED_PAD src0_sel:WORD_1
	global_load_dwordx2 v[60:61], v[60:61], off offset:1536 nt
	v_cvt_f32_f16_e32 v80, v49
	v_cvt_f32_f16_sdwa v81, v49 dst_sel:DWORD dst_unused:UNUSED_PAD src0_sel:WORD_1
	v_cvt_f32_f16_e32 v78, v38
	v_cvt_f32_f16_sdwa v79, v38 dst_sel:DWORD dst_unused:UNUSED_PAD src0_sel:WORD_1
	v_cvt_f32_f16_e32 v84, v39
	v_cvt_f32_f16_sdwa v85, v39 dst_sel:DWORD dst_unused:UNUSED_PAD src0_sel:WORD_1
	v_pk_mul_f32 v[136:137], v[72:73], v[72:73]
	v_pk_mul_f32 v[138:139], v[76:77], v[76:77]
	v_pk_mul_f32 v[140:141], v[74:75], v[74:75]
	v_pk_mul_f32 v[142:143], v[80:81], v[80:81]
	v_pk_mul_f32 v[144:145], v[78:79], v[78:79]
	v_pk_mul_f32 v[146:147], v[84:85], v[84:85]
	v_add_f32_e32 v142, v142, v143
	v_add_f32_e32 v140, v140, v141
	v_add_f32_e32 v138, v138, v139
	v_add_f32_e32 v136, v136, v137
	v_add_f32_e32 v140, v140, v142
	v_add_f32_e32 v136, v136, v138
	v_add_f32_e32 v137, v146, v147
	v_add_f32_e32 v138, v144, v145
	v_add_f32_e32 v136, v136, v140
	v_add_f32_e32 v137, v138, v137
	v_add_f32_e32 v136, v136, v137
	s_waitcnt vmcnt(9)
	v_cvt_f32_f16_e32 v92, v58
	v_cvt_f32_f16_sdwa v93, v58 dst_sel:DWORD dst_unused:UNUSED_PAD src0_sel:WORD_1
	v_cvt_f32_f16_e32 v96, v59
	v_cvt_f32_f16_sdwa v97, v59 dst_sel:DWORD dst_unused:UNUSED_PAD src0_sel:WORD_1
	v_pk_mul_f32 v[140:141], v[90:91], v[90:91]
	v_pk_mul_f32 v[142:143], v[92:93], v[92:93]
	v_add_f32_e32 v140, v140, v141
	v_pk_mul_f32 v[144:145], v[96:97], v[96:97]
	v_add_f32_e32 v142, v142, v143
	s_waitcnt vmcnt(8)
	v_cvt_f32_f16_e32 v120, v68
	v_cvt_f32_f16_sdwa v121, v68 dst_sel:DWORD dst_unused:UNUSED_PAD src0_sel:WORD_1
	v_cvt_f32_f16_e32 v122, v69
	v_cvt_f32_f16_sdwa v123, v69 dst_sel:DWORD dst_unused:UNUSED_PAD src0_sel:WORD_1
	s_waitcnt vmcnt(6)
	v_cvt_f32_f16_e32 v94, v56
	v_cvt_f32_f16_sdwa v95, v56 dst_sel:DWORD dst_unused:UNUSED_PAD src0_sel:WORD_1
	v_cvt_f32_f16_e32 v100, v57
	s_waitcnt vmcnt(4)
	v_cvt_f32_f16_e32 v82, v32
	v_cvt_f32_f16_sdwa v83, v32 dst_sel:DWORD dst_unused:UNUSED_PAD src0_sel:WORD_1
	s_waitcnt vmcnt(3)
; #define LAS __attribute__((address_space(3)))
; template <int R, bool RT = false>
; __device__ __forceinline__ void norm_phase(const NormArgs& a, LAS unsigned char* lds, bool ctx_rows, const float* ctx_src, const float* ctx_shift, const float* ctx_scale) {
;     ...
;             for (int q = 0; q < R; ++q) { const int row = row0 + rr + q;
;                 if (a.src16) { const f16* xr = a.src16 + (size_t)row * DM;
; #pragma unroll
;                     for (int j = 0; j < 4; ++j) { const f16x4 t = *(const f16x4*)(xr + 4 * lane + 256 * j); v[q][j] = (f32x4){(float)t[0], (float)t[1], (float)t[2], (float)t[3]};
;                         if constexpr (RT) { if (j == 0) *(LAS u32x2*)(hs + (rr + q) * 528 + 8 * lane) = __builtin_bit_cast(u32x2, t);
;                             else xp[rr / 4][q][j - 1] = __builtin_bit_cast(u32x2, t); } } }
;                 else { const float* xr = a.src + (size_t)row * DM;
; #pragma unroll
;                     for (int j = 0; j < 4; ++j) v[q][j] = *(const f32x4*)(xr + 4 * lane + 256 * j); } }
;             if (a.y2) {
;                 unsigned long long mask[R]; int ee[R][4]; float wgt[R][4]; f16x4 ld[R][4][4];
;                 int cnt[R];
; #pragma unroll
;                 for (int q = 0; q < R; ++q) { mask[q] = __ballot(sl[q] >= 0); cnt[q] = __builtin_popcountll(mask[q]);
; #pragma unroll
;                     for (int i = 0; i < 4; ++i) { if (mask[q]) { ee[q][i] = __builtin_ctzll(mask[q]); mask[q] &= mask[q] - 1; wgt[q][i] = 1.f; } else { ee[q][i] = i ? ee[q][0] : 0; wgt[q][i] = 0.f; } }
; #pragma unroll
;                     for (int i = 0; i < 4; ++i) {
;                         if (i < cnt[q]) { int slot = __shfl(sl[q], ee[q][i]); slot = slot < 0 ? 0 : slot; const f16* yr = a.y2 + ((size_t)ee[q][i] * EROWS + b * CAP + slot) * DM + 4 * lane;
; #pragma unroll
;                             for (int j = 0; j < 4; ++j) ld[q][i][j] = *(const f16x4*)(yr + 256 * j); } } }
; #pragma unroll
;                 for (int q = 0; q < R; ++q) { const int row = row0 + rr + q;
;                     f32x4 cs[4];
; #pragma unroll
;                     for (int j = 0; j < 4; ++j) cs[j] = (f32x4){0.f, 0.f, 0.f, 0.f};
; #pragma unroll
;                     for (int i = 0; i < 4; ++i) if (i < cnt[q]) {
; #pragma unroll
	ds_write2_b64 v211, v[66:67], v[68:69] offset0:132 offset1:198
	global_load_dwordx2 v[68:69], v[130:131], off offset:1024 nt
	v_cvt_f32_f16_e32 v104, v66
	v_cvt_f32_f16_sdwa v105, v66 dst_sel:DWORD dst_unused:UNUSED_PAD src0_sel:WORD_1
	v_cvt_f32_f16_e32 v108, v67
	v_cvt_f32_f16_sdwa v109, v67 dst_sel:DWORD dst_unused:UNUSED_PAD src0_sel:WORD_1
	global_load_dwordx2 v[66:67], v[130:131], off offset:1536 nt
	v_cvt_f32_f16_e32 v86, v33
	v_cvt_f32_f16_sdwa v87, v33 dst_sel:DWORD dst_unused:UNUSED_PAD src0_sel:WORD_1
	v_pk_mul_f32 v[148:149], v[82:83], v[82:83]
	v_cvt_f32_f16_sdwa v101, v57 dst_sel:DWORD dst_unused:UNUSED_PAD src0_sel:WORD_1
	v_add_f32_e32 v138, v148, v149
	v_pk_mul_f32 v[150:151], v[86:87], v[86:87]
	v_cvt_f32_f16_e32 v98, v50
	v_add_f32_e32 v137, v150, v151
	v_add_f32_e32 v137, v138, v137
	v_add_f32_e32 v136, v136, v137
	v_mov_b32_e32 v137, 0
	v_cvt_f32_f16_sdwa v99, v50 dst_sel:DWORD dst_unused:UNUSED_PAD src0_sel:WORD_1
	v_add_f32_dpp v136, v136, v136 quad_perm:[1,0,3,2] row_mask:0xf bank_mask:0xf bound_ctrl:1
	v_cvt_f32_f16_e32 v102, v51
	v_cvt_f32_f16_sdwa v103, v51 dst_sel:DWORD dst_unused:UNUSED_PAD src0_sel:WORD_1
	v_add_f32_dpp v136, v136, v136 quad_perm:[2,3,0,1] row_mask:0xf bank_mask:0xf bound_ctrl:1
	v_pk_mul_f32 v[138:139], v[88:89], v[88:89]
	v_pk_mul_f32 v[146:147], v[94:95], v[94:95]
	v_add_f32_dpp v136, v136, v136 row_half_mirror row_mask:0xf bank_mask:0xf bound_ctrl:1
	v_add_f32_e32 v138, v138, v139
	v_pk_mul_f32 v[148:149], v[100:101], v[100:101]
	v_add_f32_dpp v136, v136, v136 row_mirror row_mask:0xf bank_mask:0xf bound_ctrl:1
	v_add_f32_e32 v138, v138, v140
	v_add_f32_e32 v139, v146, v147
	v_mov_b32_dpp v137, v136 row_bcast:15 row_mask:0xa bank_mask:0xf
	v_add_f32_e32 v136, v136, v137
	v_mov_b32_e32 v137, 0
	v_pk_mul_f32 v[150:151], v[98:99], v[98:99]
	v_pk_mul_f32 v[152:153], v[102:103], v[102:103]
	v_mov_b32_dpp v137, v136 row_bcast:31 row_mask:0xc bank_mask:0xf
	v_add_f32_e32 v136, v136, v137
	v_add_f32_e32 v137, v144, v145
	v_add_f32_e32 v137, v142, v137
	v_add_f32_e32 v137, v138, v137
	v_add_f32_e32 v138, v148, v149
	v_add_f32_e32 v138, v139, v138
	v_add_f32_e32 v137, v137, v138
	v_add_f32_e32 v138, v152, v153
	v_add_f32_e32 v139, v150, v151
	v_add_f32_e32 v138, v139, v138
	v_add_f32_e32 v137, v137, v138
	v_mov_b32_e32 v138, 0
	s_waitcnt vmcnt(4)
	v_cvt_f32_f16_e32 v106, v64
	v_add_f32_dpp v137, v137, v137 quad_perm:[1,0,3,2] row_mask:0xf bank_mask:0xf bound_ctrl:1
	v_cvt_f32_f16_sdwa v107, v64 dst_sel:DWORD dst_unused:UNUSED_PAD src0_sel:WORD_1
	v_cvt_f32_f16_e32 v112, v65
	v_add_f32_dpp v137, v137, v137 quad_perm:[2,3,0,1] row_mask:0xf bank_mask:0xf bound_ctrl:1
	v_cvt_f32_f16_sdwa v113, v65 dst_sel:DWORD dst_unused:UNUSED_PAD src0_sel:WORD_1
	v_readlane_b32 s0, v136, 63
	v_add_f32_dpp v137, v137, v137 row_half_mirror row_mask:0xf bank_mask:0xf bound_ctrl:1
	s_waitcnt vmcnt(3)
	v_cvt_f32_f16_e32 v110, v62
	v_cvt_f32_f16_sdwa v111, v62 dst_sel:DWORD dst_unused:UNUSED_PAD src0_sel:WORD_1
	v_add_f32_dpp v137, v137, v137 row_mirror row_mask:0xf bank_mask:0xf bound_ctrl:1
	v_cvt_f32_f16_e32 v116, v63
	v_cvt_f32_f16_sdwa v117, v63 dst_sel:DWORD dst_unused:UNUSED_PAD src0_sel:WORD_1
	v_mov_b32_dpp v138, v137 row_bcast:15 row_mask:0xa bank_mask:0xf
	v_add_f32_e32 v137, v137, v138
	v_mov_b32_e32 v138, 0
	v_fma_f32 v136, s0, v214, v213
	v_pk_mul_f32 v[144:145], v[106:107], v[106:107]
	v_mov_b32_dpp v138, v137 row_bcast:31 row_mask:0xc bank_mask:0xf
	v_add_f32_e32 v137, v137, v138
	v_pk_mul_f32 v[146:147], v[112:113], v[112:113]
	v_readlane_b32 s0, v137, 63
	s_waitcnt vmcnt(2)
	v_cvt_f32_f16_e32 v114, v60
	v_cvt_f32_f16_sdwa v115, v60 dst_sel:DWORD dst_unused:UNUSED_PAD src0_sel:WORD_1
	v_fma_f32 v137, s0, v214, v213
	v_cvt_f32_f16_e32 v118, v61
	v_cvt_f32_f16_sdwa v119, v61 dst_sel:DWORD dst_unused:UNUSED_PAD src0_sel:WORD_1
	v_rsq_f32_e32 v138, v137
	v_pk_mul_f32 v[140:141], v[104:105], v[104:105]
	v_pk_mul_f32 v[142:143], v[108:109], v[108:109]
	v_add_f32_e32 v137, v146, v147
	v_add_f32_e32 v139, v144, v145
	v_add_f32_e32 v137, v139, v137
	v_add_f32_e32 v139, v142, v143
	v_add_f32_e32 v140, v140, v141
	v_pk_mul_f32 v[148:149], v[110:111], v[110:111]
	v_pk_mul_f32 v[150:151], v[116:117], v[116:117]
	v_add_f32_e32 v139, v140, v139
	v_add_f32_e32 v137, v139, v137
	v_add_f32_e32 v139, v150, v151
	v_add_f32_e32 v140, v148, v149
	v_pk_mul_f32 v[152:153], v[114:115], v[114:115]
	v_pk_mul_f32 v[154:155], v[118:119], v[118:119]
	v_add_f32_e32 v139, v140, v139
	v_add_f32_e32 v137, v137, v139
	v_add_f32_e32 v139, v154, v155
	v_add_f32_e32 v140, v152, v153
	v_add_f32_e32 v139, v140, v139
	v_add_f32_e32 v137, v137, v139
	v_mov_b32_e32 v139, 0
	v_cvt_f32_f16_e32 v124, v70
	v_add_f32_dpp v137, v137, v137 quad_perm:[1,0,3,2] row_mask:0xf bank_mask:0xf bound_ctrl:1
	v_cvt_f32_f16_sdwa v125, v70 dst_sel:DWORD dst_unused:UNUSED_PAD src0_sel:WORD_1
	v_cvt_f32_f16_e32 v128, v71
	v_add_f32_dpp v137, v137, v137 quad_perm:[2,3,0,1] row_mask:0xf bank_mask:0xf bound_ctrl:1
	v_cvt_f32_f16_sdwa v129, v71 dst_sel:DWORD dst_unused:UNUSED_PAD src0_sel:WORD_1
	s_waitcnt vmcnt(1)
	v_cvt_f32_f16_e32 v126, v68
	v_add_f32_dpp v137, v137, v137 row_half_mirror row_mask:0xf bank_mask:0xf bound_ctrl:1
	v_cvt_f32_f16_sdwa v127, v68 dst_sel:DWORD dst_unused:UNUSED_PAD src0_sel:WORD_1
	v_cvt_f32_f16_e32 v132, v69
	v_add_f32_dpp v137, v137, v137 row_mirror row_mask:0xf bank_mask:0xf bound_ctrl:1
	v_cvt_f32_f16_sdwa v133, v69 dst_sel:DWORD dst_unused:UNUSED_PAD src0_sel:WORD_1
	v_pk_mul_f32 v[142:143], v[120:121], v[120:121]
	v_mov_b32_dpp v139, v137 row_bcast:15 row_mask:0xa bank_mask:0xf
	v_add_f32_e32 v137, v137, v139
	v_mov_b32_e32 v139, 0
	v_pk_mul_f32 v[144:145], v[122:123], v[122:123]
	s_waitcnt vmcnt(0)
; __device__ __forceinline__ unsigned pkb(float lo, float hi) { f32x2 v = {lo, hi}; bf16x2_t b = __builtin_convertvector(v, bf16x2_t); return __builtin_bit_cast(unsigned, b); }
; template <int R, bool RT = false>
; __device__ __forceinline__ void norm_phase(const NormArgs& a, LAS unsigned char* lds, bool ctx_rows, const float* ctx_src, const float* ctx_shift, const float* ctx_scale) {
;     ...
;             for (int q = 0; q < R; ++q) { float ss = 0.f;
; #pragma unroll
;                 for (int j = 0; j < 4; ++j) ss += (v[q][j][0] * v[q][j][0] + v[q][j][1] * v[q][j][1]) + (v[q][j][2] * v[q][j][2] + v[q][j][3] * v[q][j][3]);
;                 rstd[q] = __builtin_amdgcn_rsqf(wave_sum(ss) * (1.f / DM) + EPS);
;                 if constexpr (RT) rsel[q] = ((lane >> 4) == rr / 4) ? rstd[q] : rsel[q]; }
; #pragma unroll
;             for (int q = 0; q < R; ++q) { const int row = row0 + rr + q;
; #pragma unroll
;                 for (int j = 0; j < 4; ++j) v[q][j] = (v[q][j] * rstd[q]) * A[j] + Sh[j];
;                 if (a.fout) {
; #pragma unroll
;                     for (int j = 0; j < 4; ++j) *(f32x4*)(a.fout + (size_t)row * DM + 4 * lane + 256 * j) = v[q][j];
;                 }
;                 if (a.hout) {
; #pragma unroll
;                     for (int j = 0; j < 4; ++j) { u32x2 w; if (a.hbf) { w.x = pkb(v[q][j][0], v[q][j][1]); w.y = pkb(v[q][j][2], v[q][j][3]); } else { w.x = pkh(v[q][j][0], v[q][j][1]); w.y = pkh(v[q][j][2], v[q][j][3]); } *(u32x2*)(a.hout + (size_t)row * DM + 4 * lane + 256 * j) = w; }
;                 }
	v_cvt_f32_f16_e32 v130, v66
	v_mov_b32_dpp v139, v137 row_bcast:31 row_mask:0xc bank_mask:0xf
	v_add_f32_e32 v137, v137, v139
	v_cvt_f32_f16_sdwa v131, v66 dst_sel:DWORD dst_unused:UNUSED_PAD src0_sel:WORD_1
	v_readlane_b32 s0, v137, 63
	v_cvt_f32_f16_e32 v134, v67
	v_cvt_f32_f16_sdwa v135, v67 dst_sel:DWORD dst_unused:UNUSED_PAD src0_sel:WORD_1
	v_fma_f32 v137, s0, v214, v213
	v_rsq_f32_e32 v140, v137
	v_pk_mul_f32 v[146:147], v[124:125], v[124:125]
	v_pk_mul_f32 v[148:149], v[128:129], v[128:129]
	v_add_f32_e32 v137, v144, v145
	v_add_f32_e32 v139, v142, v143
	v_add_f32_e32 v137, v139, v137
	v_add_f32_e32 v139, v148, v149
	v_add_f32_e32 v141, v146, v147
	v_pk_mul_f32 v[150:151], v[126:127], v[126:127]
	v_pk_mul_f32 v[152:153], v[132:133], v[132:133]
	v_add_f32_e32 v139, v141, v139
	v_add_f32_e32 v137, v137, v139
	v_add_f32_e32 v139, v152, v153
	v_add_f32_e32 v141, v150, v151
	v_pk_mul_f32 v[154:155], v[130:131], v[130:131]
	v_pk_mul_f32 v[156:157], v[134:135], v[134:135]
	v_add_f32_e32 v139, v141, v139
	v_add_f32_e32 v137, v137, v139
	v_add_f32_e32 v139, v156, v157
	v_add_f32_e32 v141, v154, v155
	v_add_f32_e32 v139, v141, v139
	v_add_f32_e32 v137, v137, v139
	v_mov_b32_e32 v139, 0
	v_rsq_f32_e32 v136, v136
	v_add_f32_dpp v137, v137, v137 quad_perm:[1,0,3,2] row_mask:0xf bank_mask:0xf bound_ctrl:1
	v_cndmask_b32_e64 v164, 0, v140, s[4:5]
	v_cndmask_b32_e64 v163, 0, v138, s[4:5]
	v_add_f32_dpp v137, v137, v137 quad_perm:[2,3,0,1] row_mask:0xf bank_mask:0xf bound_ctrl:1
	v_cndmask_b32_e64 v161, 0, v136, s[4:5]
	s_nop 0
	v_add_f32_dpp v137, v137, v137 row_half_mirror row_mask:0xf bank_mask:0xf bound_ctrl:1
	s_nop 1
	v_add_f32_dpp v137, v137, v137 row_mirror row_mask:0xf bank_mask:0xf bound_ctrl:1
	s_nop 1
	v_mov_b32_dpp v139, v137 row_bcast:15 row_mask:0xa bank_mask:0xf
	v_add_f32_e32 v137, v137, v139
	v_mov_b32_e32 v139, 0
	s_nop 1
	v_mov_b32_dpp v139, v137 row_bcast:31 row_mask:0xc bank_mask:0xf
	v_add_f32_e32 v137, v137, v139
	s_nop 0
	v_readlane_b32 s0, v137, 63
	s_nop 1
	v_fma_f32 v137, s0, v214, v213
	v_pk_mul_f32 v[72:73], v[72:73], v[136:137] op_sel_hi:[1,0]
	v_pk_mul_f32 v[76:77], v[76:77], v[136:137] op_sel_hi:[1,0]
	v_pk_fma_f32 v[72:73], v[36:37], v[72:73], v[2:3]
	v_pk_fma_f32 v[76:77], v[34:35], v[76:77], v[4:5]
	v_pk_mul_f32 v[74:75], v[74:75], v[136:137] op_sel_hi:[1,0]
	v_pk_mul_f32 v[80:81], v[80:81], v[136:137] op_sel_hi:[1,0]
	v_pk_fma_f32 v[74:75], v[42:43], v[74:75], v[6:7]
	v_pk_fma_f32 v[80:81], v[40:41], v[80:81], v[8:9]
	v_pk_mul_f32 v[78:79], v[78:79], v[136:137] op_sel_hi:[1,0]
	v_pk_mul_f32 v[84:85], v[84:85], v[136:137] op_sel_hi:[1,0]
	v_cvt_pk_bf16_f32 v72, v72, v73
	v_cvt_pk_bf16_f32 v73, v76, v77
	v_lshl_add_u64 v[76:77], v[24:25], 0, s[2:3]
	v_pk_fma_f32 v[84:85], v[44:45], v[84:85], v[12:13]
	v_pk_fma_f32 v[78:79], v[46:47], v[78:79], v[10:11]
	v_pk_mul_f32 v[82:83], v[82:83], v[136:137] op_sel_hi:[1,0]
	v_pk_mul_f32 v[86:87], v[86:87], v[136:137] op_sel_hi:[1,0]
	global_store_dwordx2 v[76:77], v[72:73], off
	v_cvt_pk_bf16_f32 v72, v74, v75
	v_cvt_pk_bf16_f32 v73, v80, v81
	v_pk_fma_f32 v[86:87], v[52:53], v[86:87], v[16:17]
	v_pk_fma_f32 v[82:83], v[54:55], v[82:83], v[14:15]
	global_store_dwordx2 v[76:77], v[72:73], off offset:512
	v_cvt_pk_bf16_f32 v72, v78, v79
	v_cvt_pk_bf16_f32 v73, v84, v85
	global_store_dwordx2 v[76:77], v[72:73], off offset:1024
	v_cvt_pk_bf16_f32 v72, v82, v83
	v_cvt_pk_bf16_f32 v73, v86, v87
	global_store_dwordx2 v[76:77], v[72:73], off offset:1536
	v_pk_mul_f32 v[72:73], v[88:89], v[138:139] op_sel_hi:[1,0]
	v_pk_mul_f32 v[74:75], v[90:91], v[138:139] op_sel_hi:[1,0]
	v_pk_fma_f32 v[72:73], v[36:37], v[72:73], v[2:3]
	v_pk_fma_f32 v[74:75], v[34:35], v[74:75], v[4:5]
	v_pk_mul_f32 v[76:77], v[92:93], v[138:139] op_sel_hi:[1,0]
	v_pk_mul_f32 v[78:79], v[96:97], v[138:139] op_sel_hi:[1,0]
	v_pk_fma_f32 v[76:77], v[42:43], v[76:77], v[6:7]
	v_pk_fma_f32 v[78:79], v[40:41], v[78:79], v[8:9]
	v_pk_mul_f32 v[80:81], v[94:95], v[138:139] op_sel_hi:[1,0]
	v_pk_mul_f32 v[82:83], v[100:101], v[138:139] op_sel_hi:[1,0]
	v_cvt_pk_bf16_f32 v72, v72, v73
	v_cvt_pk_bf16_f32 v73, v74, v75
	v_lshl_add_u64 v[74:75], v[24:25], 0, s[24:25]
	v_pk_fma_f32 v[82:83], v[44:45], v[82:83], v[12:13]
	v_pk_fma_f32 v[80:81], v[46:47], v[80:81], v[10:11]
	v_pk_mul_f32 v[84:85], v[98:99], v[138:139] op_sel_hi:[1,0]
	v_pk_mul_f32 v[86:87], v[102:103], v[138:139] op_sel_hi:[1,0]
	global_store_dwordx2 v[74:75], v[72:73], off
	v_cvt_pk_bf16_f32 v72, v76, v77
	v_cvt_pk_bf16_f32 v73, v78, v79
	v_pk_fma_f32 v[86:87], v[52:53], v[86:87], v[16:17]
	v_pk_fma_f32 v[84:85], v[54:55], v[84:85], v[14:15]
	global_store_dwordx2 v[74:75], v[72:73], off offset:512
	v_cvt_pk_bf16_f32 v72, v80, v81
	v_cvt_pk_bf16_f32 v73, v82, v83
	global_store_dwordx2 v[74:75], v[72:73], off offset:1024
	v_cvt_pk_bf16_f32 v72, v84, v85
	v_cvt_pk_bf16_f32 v73, v86, v87
	global_store_dwordx2 v[74:75], v[72:73], off offset:1536
	v_pk_mul_f32 v[72:73], v[104:105], v[140:141] op_sel_hi:[1,0]
	v_pk_mul_f32 v[74:75], v[108:109], v[140:141] op_sel_hi:[1,0]
	v_pk_fma_f32 v[72:73], v[36:37], v[72:73], v[2:3]
	v_pk_fma_f32 v[74:75], v[34:35], v[74:75], v[4:5]
	v_pk_mul_f32 v[76:77], v[106:107], v[140:141] op_sel_hi:[1,0]
	v_pk_mul_f32 v[78:79], v[112:113], v[140:141] op_sel_hi:[1,0]
	v_rsq_f32_e32 v142, v137
	v_pk_fma_f32 v[78:79], v[40:41], v[78:79], v[8:9]
	v_pk_fma_f32 v[76:77], v[42:43], v[76:77], v[6:7]
	v_pk_mul_f32 v[80:81], v[110:111], v[140:141] op_sel_hi:[1,0]
	v_pk_mul_f32 v[82:83], v[116:117], v[140:141] op_sel_hi:[1,0]
	v_cvt_pk_bf16_f32 v72, v72, v73
	v_cvt_pk_bf16_f32 v73, v74, v75
	v_lshl_add_u64 v[74:75], v[24:25], 0, s[26:27]
; #define LAS __attribute__((address_space(3)))
; __device__ __forceinline__ unsigned pkb(float lo, float hi) { f32x2 v = {lo, hi}; bf16x2_t b = __builtin_convertvector(v, bf16x2_t); return __builtin_bit_cast(unsigned, b); }
; template <int R, bool RT = false>
; __device__ __forceinline__ void norm_phase(const NormArgs& a, LAS unsigned char* lds, bool ctx_rows, const float* ctx_src, const float* ctx_shift, const float* ctx_scale) {
;     ...
;             for (int q = 0; q < R; ++q) { const int row = row0 + rr + q;
;                 if (a.src16) { const f16* xr = a.src16 + (size_t)row * DM;
; #pragma unroll
;                     for (int j = 0; j < 4; ++j) { const f16x4 t = *(const f16x4*)(xr + 4 * lane + 256 * j); v[q][j] = (f32x4){(float)t[0], (float)t[1], (float)t[2], (float)t[3]};
;                         if constexpr (RT) { if (j == 0) *(LAS u32x2*)(hs + (rr + q) * 528 + 8 * lane) = __builtin_bit_cast(u32x2, t);
;                             else xp[rr / 4][q][j - 1] = __builtin_bit_cast(u32x2, t); } } }
;     ...
;             for (int q = 0; q < R; ++q) { const int row = row0 + rr + q;
; #pragma unroll
;                 for (int j = 0; j < 4; ++j) v[q][j] = (v[q][j] * rstd[q]) * A[j] + Sh[j];
;                 if (a.fout) {
; #pragma unroll
;                     for (int j = 0; j < 4; ++j) *(f32x4*)(a.fout + (size_t)row * DM + 4 * lane + 256 * j) = v[q][j];
;                 }
;                 if (a.hout) {
; #pragma unroll
;                     for (int j = 0; j < 4; ++j) { u32x2 w; if (a.hbf) { w.x = pkb(v[q][j][0], v[q][j][1]); w.y = pkb(v[q][j][2], v[q][j][3]); } else { w.x = pkh(v[q][j][0], v[q][j][1]); w.y = pkh(v[q][j][2], v[q][j][3]); } *(u32x2*)(a.hout + (size_t)row * DM + 4 * lane + 256 * j) = w; }
;                 }
	v_pk_fma_f32 v[82:83], v[44:45], v[82:83], v[12:13]
	v_pk_fma_f32 v[80:81], v[46:47], v[80:81], v[10:11]
	v_pk_mul_f32 v[84:85], v[114:115], v[140:141] op_sel_hi:[1,0]
	v_pk_mul_f32 v[86:87], v[118:119], v[140:141] op_sel_hi:[1,0]
	global_store_dwordx2 v[74:75], v[72:73], off
	v_cvt_pk_bf16_f32 v72, v76, v77
	v_cvt_pk_bf16_f32 v73, v78, v79
	v_pk_fma_f32 v[86:87], v[52:53], v[86:87], v[16:17]
	v_pk_fma_f32 v[84:85], v[54:55], v[84:85], v[14:15]
	global_store_dwordx2 v[74:75], v[72:73], off offset:512
	v_cvt_pk_bf16_f32 v72, v80, v81
	v_cvt_pk_bf16_f32 v73, v82, v83
	global_store_dwordx2 v[74:75], v[72:73], off offset:1024
	v_cvt_pk_bf16_f32 v72, v84, v85
	v_cvt_pk_bf16_f32 v73, v86, v87
	global_store_dwordx2 v[74:75], v[72:73], off offset:1536
	v_pk_mul_f32 v[72:73], v[120:121], v[142:143] op_sel_hi:[1,0]
	v_pk_mul_f32 v[74:75], v[122:123], v[142:143] op_sel_hi:[1,0]
	v_pk_fma_f32 v[72:73], v[36:37], v[72:73], v[2:3]
	v_pk_fma_f32 v[74:75], v[34:35], v[74:75], v[4:5]
	v_pk_mul_f32 v[76:77], v[124:125], v[142:143] op_sel_hi:[1,0]
	v_pk_mul_f32 v[78:79], v[128:129], v[142:143] op_sel_hi:[1,0]
	v_pk_fma_f32 v[76:77], v[42:43], v[76:77], v[6:7]
	v_pk_fma_f32 v[78:79], v[40:41], v[78:79], v[8:9]
	v_pk_mul_f32 v[80:81], v[126:127], v[142:143] op_sel_hi:[1,0]
	v_pk_mul_f32 v[82:83], v[132:133], v[142:143] op_sel_hi:[1,0]
	v_cvt_pk_bf16_f32 v72, v72, v73
	v_cvt_pk_bf16_f32 v73, v74, v75
	v_lshl_add_u64 v[74:75], v[24:25], 0, s[28:29]
	v_pk_fma_f32 v[82:83], v[44:45], v[82:83], v[12:13]
	v_pk_fma_f32 v[80:81], v[46:47], v[80:81], v[10:11]
	v_pk_mul_f32 v[84:85], v[130:131], v[142:143] op_sel_hi:[1,0]
	v_pk_mul_f32 v[86:87], v[134:135], v[142:143] op_sel_hi:[1,0]
	global_store_dwordx2 v[74:75], v[72:73], off
	v_cvt_pk_bf16_f32 v72, v76, v77
	v_cvt_pk_bf16_f32 v73, v78, v79
	v_pk_fma_f32 v[86:87], v[52:53], v[86:87], v[16:17]
	v_pk_fma_f32 v[84:85], v[54:55], v[84:85], v[14:15]
	global_store_dwordx2 v[74:75], v[72:73], off offset:512
	v_cvt_pk_bf16_f32 v72, v80, v81
	v_cvt_pk_bf16_f32 v73, v82, v83
	s_add_i32 s2, s14, 4
	s_add_i32 s24, s14, 5
	global_store_dwordx2 v[74:75], v[72:73], off offset:1024
	v_cvt_pk_bf16_f32 v72, v84, v85
	v_cvt_pk_bf16_f32 v73, v86, v87
	s_ashr_i32 s3, s2, 31
	s_ashr_i32 s25, s24, 31
	global_store_dwordx2 v[74:75], v[72:73], off offset:1536
	s_lshl_b64 s[2:3], s[2:3], 11
	s_lshl_b64 s[24:25], s[24:25], 11
	v_lshl_add_u64 v[72:73], v[22:23], 0, s[2:3]
	v_lshl_add_u64 v[84:85], v[22:23], 0, s[24:25]
	global_load_dwordx2 v[78:79], v[72:73], off nt
	global_load_dwordx2 v[76:77], v[72:73], off offset:512 nt
	global_load_dwordx2 v[74:75], v[72:73], off offset:1024 nt
	global_load_dwordx2 v[80:81], v[84:85], off nt
	s_add_i32 s28, s14, 7
	s_add_i32 s26, s14, 6
	s_ashr_i32 s29, s28, 31
	s_ashr_i32 s27, s26, 31
	s_lshl_b64 s[28:29], s[28:29], 11
	s_lshl_b64 s[26:27], s[26:27], 11
	v_lshl_add_u64 v[154:155], v[22:23], 0, s[28:29]
	global_load_dwordx2 v[82:83], v[84:85], off offset:512 nt
	global_load_dwordx2 v[92:93], v[154:155], off nt
	global_load_dwordx2 v[94:95], v[154:155], off offset:512 nt
	v_cndmask_b32_e64 v165, 0, v142, s[4:5]
	global_load_dwordx2 v[72:73], v[72:73], off offset:1536 nt
	s_waitcnt vmcnt(7)
	v_cvt_f32_f16_e32 v96, v78
	v_cvt_f32_f16_sdwa v97, v78 dst_sel:DWORD dst_unused:UNUSED_PAD src0_sel:WORD_1
	v_cvt_f32_f16_e32 v100, v79
	v_cvt_f32_f16_sdwa v101, v79 dst_sel:DWORD dst_unused:UNUSED_PAD src0_sel:WORD_1
	s_waitcnt vmcnt(4)
	v_cvt_f32_f16_e32 v112, v80
	v_cvt_f32_f16_sdwa v113, v80 dst_sel:DWORD dst_unused:UNUSED_PAD src0_sel:WORD_1
	v_cvt_f32_f16_e32 v114, v81
	v_cvt_f32_f16_sdwa v115, v81 dst_sel:DWORD dst_unused:UNUSED_PAD src0_sel:WORD_1
	ds_write2_b64 v225, v[78:79], v[80:81] offset0:8 offset1:74
	global_load_dwordx2 v[80:81], v[84:85], off offset:1024 nt
	global_load_dwordx2 v[78:79], v[84:85], off offset:1536 nt
	v_lshl_add_u64 v[84:85], v[22:23], 0, s[26:27]
	global_load_dwordx2 v[90:91], v[84:85], off nt
	global_load_dwordx2 v[88:89], v[84:85], off offset:512 nt
	global_load_dwordx2 v[86:87], v[84:85], off offset:1024 nt
	s_waitcnt vmcnt(7)
	v_cvt_f32_f16_e32 v144, v92
	global_load_dwordx2 v[84:85], v[84:85], off offset:1536 nt
	v_cvt_f32_f16_sdwa v145, v92 dst_sel:DWORD dst_unused:UNUSED_PAD src0_sel:WORD_1
	v_cvt_f32_f16_e32 v146, v93
	v_cvt_f32_f16_sdwa v147, v93 dst_sel:DWORD dst_unused:UNUSED_PAD src0_sel:WORD_1
	v_cvt_f32_f16_e32 v98, v76
	v_cvt_f32_f16_sdwa v99, v76 dst_sel:DWORD dst_unused:UNUSED_PAD src0_sel:WORD_1
	v_cvt_f32_f16_e32 v104, v77
	v_cvt_f32_f16_sdwa v105, v77 dst_sel:DWORD dst_unused:UNUSED_PAD src0_sel:WORD_1
	v_cvt_f32_f16_e32 v102, v74
	v_cvt_f32_f16_sdwa v103, v74 dst_sel:DWORD dst_unused:UNUSED_PAD src0_sel:WORD_1
	v_cvt_f32_f16_e32 v108, v75
	v_cvt_f32_f16_sdwa v109, v75 dst_sel:DWORD dst_unused:UNUSED_PAD src0_sel:WORD_1
	v_pk_mul_f32 v[170:171], v[98:99], v[98:99]
	v_pk_mul_f32 v[172:173], v[104:105], v[104:105]
	s_waitcnt vmcnt(6)
; #define LAS __attribute__((address_space(3)))
; template <int R, bool RT = false>
; __device__ __forceinline__ void norm_phase(const NormArgs& a, LAS unsigned char* lds, bool ctx_rows, const float* ctx_src, const float* ctx_shift, const float* ctx_scale) {
;     ...
;             for (int q = 0; q < R; ++q) { const int row = row0 + rr + q;
;                 if (a.src16) { const f16* xr = a.src16 + (size_t)row * DM;
; #pragma unroll
;                     for (int j = 0; j < 4; ++j) { const f16x4 t = *(const f16x4*)(xr + 4 * lane + 256 * j); v[q][j] = (f32x4){(float)t[0], (float)t[1], (float)t[2], (float)t[3]};
;                         if constexpr (RT) { if (j == 0) *(LAS u32x2*)(hs + (rr + q) * 528 + 8 * lane) = __builtin_bit_cast(u32x2, t);
;                             else xp[rr / 4][q][j - 1] = __builtin_bit_cast(u32x2, t); } } }
;                 else { const float* xr = a.src + (size_t)row * DM;
; #pragma unroll
;                     for (int j = 0; j < 4; ++j) v[q][j] = *(const f32x4*)(xr + 4 * lane + 256 * j); } }
;             if (a.y2) {
;                 unsigned long long mask[R]; int ee[R][4]; float wgt[R][4]; f16x4 ld[R][4][4];
;                 int cnt[R];
; #pragma unroll
;                 for (int q = 0; q < R; ++q) { mask[q] = __ballot(sl[q] >= 0); cnt[q] = __builtin_popcountll(mask[q]);
; #pragma unroll
;                     for (int i = 0; i < 4; ++i) { if (mask[q]) { ee[q][i] = __builtin_ctzll(mask[q]); mask[q] &= mask[q] - 1; wgt[q][i] = 1.f; } else { ee[q][i] = i ? ee[q][0] : 0; wgt[q][i] = 0.f; } }
; #pragma unroll
;                     for (int i = 0; i < 4; ++i) {
;                         if (i < cnt[q]) { int slot = __shfl(sl[q], ee[q][i]); slot = slot < 0 ? 0 : slot; const f16* yr = a.y2 + ((size_t)ee[q][i] * EROWS + b * CAP + slot) * DM + 4 * lane;
; #pragma unroll
;                             for (int j = 0; j < 4; ++j) ld[q][i][j] = *(const f16x4*)(yr + 256 * j); } } }
; #pragma unroll
;                 for (int q = 0; q < R; ++q) { const int row = row0 + rr + q;
;                     f32x4 cs[4];
; #pragma unroll
;                     for (int j = 0; j < 4; ++j) cs[j] = (f32x4){0.f, 0.f, 0.f, 0.f};
; #pragma unroll
;                     for (int i = 0; i < 4; ++i) if (i < cnt[q]) {
; #pragma unroll
	v_cvt_f32_f16_e32 v106, v72
	v_cvt_f32_f16_sdwa v107, v72 dst_sel:DWORD dst_unused:UNUSED_PAD src0_sel:WORD_1
	v_cvt_f32_f16_e32 v110, v73
	v_cvt_f32_f16_sdwa v111, v73 dst_sel:DWORD dst_unused:UNUSED_PAD src0_sel:WORD_1
	v_pk_mul_f32 v[166:167], v[96:97], v[96:97]
	v_pk_mul_f32 v[168:169], v[100:101], v[100:101]
	v_add_f32_e32 v160, v172, v173
	v_add_f32_e32 v162, v170, v171
	v_add_f32_e32 v160, v162, v160
	v_add_f32_e32 v162, v168, v169
	v_add_f32_e32 v166, v166, v167
	v_pk_mul_f32 v[174:175], v[102:103], v[102:103]
	v_pk_mul_f32 v[176:177], v[108:109], v[108:109]
	v_add_f32_e32 v162, v166, v162
	v_add_f32_e32 v160, v162, v160
	v_add_f32_e32 v162, v176, v177
	v_add_f32_e32 v166, v174, v175
	v_pk_mul_f32 v[178:179], v[106:107], v[106:107]
	v_pk_mul_f32 v[180:181], v[110:111], v[110:111]
	v_add_f32_e32 v162, v166, v162
	v_add_f32_e32 v160, v160, v162
	v_add_f32_e32 v162, v180, v181
	v_add_f32_e32 v166, v178, v179
	v_add_f32_e32 v162, v166, v162
	v_add_f32_e32 v160, v160, v162
	v_mov_b32_e32 v162, 0
	v_cvt_f32_f16_e32 v116, v82
	v_add_f32_dpp v160, v160, v160 quad_perm:[1,0,3,2] row_mask:0xf bank_mask:0xf bound_ctrl:1
	v_cvt_f32_f16_sdwa v117, v82 dst_sel:DWORD dst_unused:UNUSED_PAD src0_sel:WORD_1
	v_cvt_f32_f16_e32 v120, v83
	v_add_f32_dpp v160, v160, v160 quad_perm:[2,3,0,1] row_mask:0xf bank_mask:0xf bound_ctrl:1
	v_cvt_f32_f16_sdwa v121, v83 dst_sel:DWORD dst_unused:UNUSED_PAD src0_sel:WORD_1
	v_pk_mul_f32 v[170:171], v[116:117], v[116:117]
	v_add_f32_dpp v160, v160, v160 row_half_mirror row_mask:0xf bank_mask:0xf bound_ctrl:1
	v_pk_mul_f32 v[166:167], v[112:113], v[112:113]
	v_pk_mul_f32 v[172:173], v[120:121], v[120:121]
	v_add_f32_dpp v160, v160, v160 row_mirror row_mask:0xf bank_mask:0xf bound_ctrl:1
	v_pk_mul_f32 v[168:169], v[114:115], v[114:115]
	v_add_f32_e32 v166, v166, v167
	v_mov_b32_dpp v162, v160 row_bcast:15 row_mask:0xa bank_mask:0xf
	v_add_f32_e32 v160, v160, v162
	v_mov_b32_e32 v162, 0
	s_waitcnt vmcnt(5)
	v_cvt_f32_f16_e32 v118, v80
	v_mov_b32_dpp v162, v160 row_bcast:31 row_mask:0xc bank_mask:0xf
	v_add_f32_e32 v160, v160, v162
	s_waitcnt vmcnt(3)
	ds_write2_b64 v225, v[90:91], v[92:93] offset0:140 offset1:206
	global_load_dwordx2 v[92:93], v[154:155], off offset:1024 nt
	v_cvt_f32_f16_e32 v128, v90
	v_cvt_f32_f16_sdwa v129, v90 dst_sel:DWORD dst_unused:UNUSED_PAD src0_sel:WORD_1
	v_cvt_f32_f16_e32 v132, v91
	v_cvt_f32_f16_sdwa v133, v91 dst_sel:DWORD dst_unused:UNUSED_PAD src0_sel:WORD_1
	global_load_dwordx2 v[90:91], v[154:155], off offset:1536 nt
	v_readlane_b32 s0, v160, 63
	v_cvt_f32_f16_sdwa v119, v80 dst_sel:DWORD dst_unused:UNUSED_PAD src0_sel:WORD_1
	v_cvt_f32_f16_e32 v124, v81
	v_fma_f32 v160, s0, v214, v213
	v_rsq_f32_e32 v160, v160
	v_cvt_f32_f16_sdwa v125, v81 dst_sel:DWORD dst_unused:UNUSED_PAD src0_sel:WORD_1
	v_cvt_f32_f16_e32 v122, v78
	v_cvt_f32_f16_sdwa v123, v78 dst_sel:DWORD dst_unused:UNUSED_PAD src0_sel:WORD_1
	v_cvt_f32_f16_e32 v126, v79
	v_cvt_f32_f16_sdwa v127, v79 dst_sel:DWORD dst_unused:UNUSED_PAD src0_sel:WORD_1
	v_cndmask_b32_e64 v186, v161, v160, s[6:7]
	v_add_f32_e32 v161, v172, v173
	v_add_f32_e32 v162, v170, v171
	v_add_f32_e32 v161, v162, v161
	v_add_f32_e32 v162, v168, v169
	v_pk_mul_f32 v[174:175], v[118:119], v[118:119]
	v_pk_mul_f32 v[176:177], v[124:125], v[124:125]
	v_add_f32_e32 v162, v166, v162
	v_add_f32_e32 v161, v162, v161
	v_add_f32_e32 v162, v176, v177
	v_add_f32_e32 v166, v174, v175
	v_pk_mul_f32 v[178:179], v[122:123], v[122:123]
	v_pk_mul_f32 v[180:181], v[126:127], v[126:127]
	v_add_f32_e32 v162, v166, v162
	v_add_f32_e32 v161, v161, v162
	v_add_f32_e32 v162, v180, v181
	v_add_f32_e32 v166, v178, v179
	v_add_f32_e32 v162, v166, v162
	v_add_f32_e32 v161, v161, v162
	v_mov_b32_e32 v162, 0
	s_waitcnt vmcnt(4)
	v_cvt_f32_f16_e32 v130, v88
	v_add_f32_dpp v161, v161, v161 quad_perm:[1,0,3,2] row_mask:0xf bank_mask:0xf bound_ctrl:1
	v_cvt_f32_f16_sdwa v131, v88 dst_sel:DWORD dst_unused:UNUSED_PAD src0_sel:WORD_1
	v_cvt_f32_f16_e32 v136, v89
	v_add_f32_dpp v161, v161, v161 quad_perm:[2,3,0,1] row_mask:0xf bank_mask:0xf bound_ctrl:1
	v_cvt_f32_f16_sdwa v137, v89 dst_sel:DWORD dst_unused:UNUSED_PAD src0_sel:WORD_1
	s_waitcnt vmcnt(3)
	v_cvt_f32_f16_e32 v134, v86
	v_add_f32_dpp v161, v161, v161 row_half_mirror row_mask:0xf bank_mask:0xf bound_ctrl:1
	v_cvt_f32_f16_sdwa v135, v86 dst_sel:DWORD dst_unused:UNUSED_PAD src0_sel:WORD_1
	v_cvt_f32_f16_e32 v140, v87
	v_add_f32_dpp v161, v161, v161 row_mirror row_mask:0xf bank_mask:0xf bound_ctrl:1
	v_cvt_f32_f16_sdwa v141, v87 dst_sel:DWORD dst_unused:UNUSED_PAD src0_sel:WORD_1
	v_pk_mul_f32 v[170:171], v[130:131], v[130:131]
	v_mov_b32_dpp v162, v161 row_bcast:15 row_mask:0xa bank_mask:0xf
	v_add_f32_e32 v161, v161, v162
	v_mov_b32_e32 v162, 0
	v_pk_mul_f32 v[172:173], v[136:137], v[136:137]
	s_waitcnt vmcnt(2)
; __device__ __forceinline__ unsigned pkb(float lo, float hi) { f32x2 v = {lo, hi}; bf16x2_t b = __builtin_convertvector(v, bf16x2_t); return __builtin_bit_cast(unsigned, b); }
; template <int R, bool RT = false>
; __device__ __forceinline__ void norm_phase(const NormArgs& a, LAS unsigned char* lds, bool ctx_rows, const float* ctx_src, const float* ctx_shift, const float* ctx_scale) {
;     ...
;             for (int q = 0; q < R; ++q) { float ss = 0.f;
; #pragma unroll
;                 for (int j = 0; j < 4; ++j) ss += (v[q][j][0] * v[q][j][0] + v[q][j][1] * v[q][j][1]) + (v[q][j][2] * v[q][j][2] + v[q][j][3] * v[q][j][3]);
;                 rstd[q] = __builtin_amdgcn_rsqf(wave_sum(ss) * (1.f / DM) + EPS);
;                 if constexpr (RT) rsel[q] = ((lane >> 4) == rr / 4) ? rstd[q] : rsel[q]; }
; #pragma unroll
;             for (int q = 0; q < R; ++q) { const int row = row0 + rr + q;
; #pragma unroll
;                 for (int j = 0; j < 4; ++j) v[q][j] = (v[q][j] * rstd[q]) * A[j] + Sh[j];
;                 if (a.fout) {
; #pragma unroll
;                     for (int j = 0; j < 4; ++j) *(f32x4*)(a.fout + (size_t)row * DM + 4 * lane + 256 * j) = v[q][j];
;                 }
;                 if (a.hout) {
; #pragma unroll
;                     for (int j = 0; j < 4; ++j) { u32x2 w; if (a.hbf) { w.x = pkb(v[q][j][0], v[q][j][1]); w.y = pkb(v[q][j][2], v[q][j][3]); } else { w.x = pkh(v[q][j][0], v[q][j][1]); w.y = pkh(v[q][j][2], v[q][j][3]); } *(u32x2*)(a.hout + (size_t)row * DM + 4 * lane + 256 * j) = w; }
;                 }
	v_cvt_f32_f16_e32 v138, v84
	v_mov_b32_dpp v162, v161 row_bcast:31 row_mask:0xc bank_mask:0xf
	v_add_f32_e32 v161, v161, v162
	v_cvt_f32_f16_sdwa v139, v84 dst_sel:DWORD dst_unused:UNUSED_PAD src0_sel:WORD_1
	v_readlane_b32 s0, v161, 63
	v_cvt_f32_f16_e32 v142, v85
	v_cvt_f32_f16_sdwa v143, v85 dst_sel:DWORD dst_unused:UNUSED_PAD src0_sel:WORD_1
	v_fma_f32 v161, s0, v214, v213
	v_rsq_f32_e32 v162, v161
	v_pk_mul_f32 v[166:167], v[128:129], v[128:129]
	v_pk_mul_f32 v[168:169], v[132:133], v[132:133]
	v_add_f32_e32 v161, v172, v173
	v_cndmask_b32_e64 v187, v163, v162, s[6:7]
	v_add_f32_e32 v163, v170, v171
	v_add_f32_e32 v161, v163, v161
	v_add_f32_e32 v163, v168, v169
	v_add_f32_e32 v166, v166, v167
	v_pk_mul_f32 v[174:175], v[134:135], v[134:135]
	v_pk_mul_f32 v[176:177], v[140:141], v[140:141]
	v_add_f32_e32 v163, v166, v163
	v_add_f32_e32 v161, v163, v161
	v_add_f32_e32 v163, v176, v177
	v_add_f32_e32 v166, v174, v175
	v_pk_mul_f32 v[178:179], v[138:139], v[138:139]
	v_pk_mul_f32 v[180:181], v[142:143], v[142:143]
	v_add_f32_e32 v163, v166, v163
	v_add_f32_e32 v161, v161, v163
	v_add_f32_e32 v163, v180, v181
	v_add_f32_e32 v166, v178, v179
	v_add_f32_e32 v163, v166, v163
	v_add_f32_e32 v161, v161, v163
	v_mov_b32_e32 v163, 0
	v_cvt_f32_f16_e32 v148, v94
	v_add_f32_dpp v161, v161, v161 quad_perm:[1,0,3,2] row_mask:0xf bank_mask:0xf bound_ctrl:1
	v_cvt_f32_f16_sdwa v149, v94 dst_sel:DWORD dst_unused:UNUSED_PAD src0_sel:WORD_1
	v_cvt_f32_f16_e32 v152, v95
	v_add_f32_dpp v161, v161, v161 quad_perm:[2,3,0,1] row_mask:0xf bank_mask:0xf bound_ctrl:1
	v_cvt_f32_f16_sdwa v153, v95 dst_sel:DWORD dst_unused:UNUSED_PAD src0_sel:WORD_1
	s_waitcnt vmcnt(1)
	v_cvt_f32_f16_e32 v150, v92
	v_add_f32_dpp v161, v161, v161 row_half_mirror row_mask:0xf bank_mask:0xf bound_ctrl:1
	v_cvt_f32_f16_sdwa v151, v92 dst_sel:DWORD dst_unused:UNUSED_PAD src0_sel:WORD_1
	v_cvt_f32_f16_e32 v156, v93
	v_add_f32_dpp v161, v161, v161 row_mirror row_mask:0xf bank_mask:0xf bound_ctrl:1
	v_cvt_f32_f16_sdwa v157, v93 dst_sel:DWORD dst_unused:UNUSED_PAD src0_sel:WORD_1
	v_pk_mul_f32 v[168:169], v[144:145], v[144:145]
	v_mov_b32_dpp v163, v161 row_bcast:15 row_mask:0xa bank_mask:0xf
	v_add_f32_e32 v161, v161, v163
	v_mov_b32_e32 v163, 0
	v_pk_mul_f32 v[170:171], v[146:147], v[146:147]
	s_waitcnt vmcnt(0)
	v_cvt_f32_f16_e32 v154, v90
	v_mov_b32_dpp v163, v161 row_bcast:31 row_mask:0xc bank_mask:0xf
	v_add_f32_e32 v161, v161, v163
	v_cvt_f32_f16_sdwa v155, v90 dst_sel:DWORD dst_unused:UNUSED_PAD src0_sel:WORD_1
	v_readlane_b32 s0, v161, 63
	v_cvt_f32_f16_e32 v158, v91
	v_cvt_f32_f16_sdwa v159, v91 dst_sel:DWORD dst_unused:UNUSED_PAD src0_sel:WORD_1
	v_fma_f32 v161, s0, v214, v213
	v_rsq_f32_e32 v166, v161
	v_pk_mul_f32 v[172:173], v[148:149], v[148:149]
	v_pk_mul_f32 v[174:175], v[152:153], v[152:153]
	v_add_f32_e32 v161, v170, v171
	v_add_f32_e32 v163, v168, v169
	v_cndmask_b32_e64 v189, v164, v166, s[6:7]
	v_add_f32_e32 v161, v163, v161
	v_add_f32_e32 v163, v174, v175
	v_add_f32_e32 v164, v172, v173
	v_pk_mul_f32 v[176:177], v[150:151], v[150:151]
	v_pk_mul_f32 v[178:179], v[156:157], v[156:157]
	v_add_f32_e32 v163, v164, v163
	v_add_f32_e32 v161, v161, v163
	v_add_f32_e32 v163, v178, v179
	v_add_f32_e32 v164, v176, v177
	v_pk_mul_f32 v[180:181], v[154:155], v[154:155]
	v_pk_mul_f32 v[182:183], v[158:159], v[158:159]
	v_add_f32_e32 v163, v164, v163
	v_add_f32_e32 v161, v161, v163
	v_add_f32_e32 v163, v182, v183
	v_add_f32_e32 v164, v180, v181
	v_add_f32_e32 v163, v164, v163
	v_add_f32_e32 v161, v161, v163
	v_mov_b32_e32 v163, 0
	s_nop 0
	v_add_f32_dpp v161, v161, v161 quad_perm:[1,0,3,2] row_mask:0xf bank_mask:0xf bound_ctrl:1
	s_nop 1
	v_add_f32_dpp v161, v161, v161 quad_perm:[2,3,0,1] row_mask:0xf bank_mask:0xf bound_ctrl:1
	s_nop 1
	v_add_f32_dpp v161, v161, v161 row_half_mirror row_mask:0xf bank_mask:0xf bound_ctrl:1
	s_nop 1
	v_add_f32_dpp v161, v161, v161 row_mirror row_mask:0xf bank_mask:0xf bound_ctrl:1
	s_nop 1
	v_mov_b32_dpp v163, v161 row_bcast:15 row_mask:0xa bank_mask:0xf
	v_add_f32_e32 v161, v161, v163
	v_mov_b32_e32 v163, 0
	s_nop 1
	v_mov_b32_dpp v163, v161 row_bcast:31 row_mask:0xc bank_mask:0xf
	v_add_f32_e32 v161, v161, v163
	s_nop 0
	v_readlane_b32 s0, v161, 63
	s_nop 1
	v_fma_f32 v161, s0, v214, v213
	v_pk_mul_f32 v[96:97], v[96:97], v[160:161] op_sel_hi:[1,0]
	v_pk_mul_f32 v[100:101], v[100:101], v[160:161] op_sel_hi:[1,0]
	v_pk_fma_f32 v[96:97], v[36:37], v[96:97], v[2:3]
	v_pk_fma_f32 v[100:101], v[34:35], v[100:101], v[4:5]
	v_pk_mul_f32 v[98:99], v[98:99], v[160:161] op_sel_hi:[1,0]
	v_pk_mul_f32 v[104:105], v[104:105], v[160:161] op_sel_hi:[1,0]
	v_pk_fma_f32 v[98:99], v[42:43], v[98:99], v[6:7]
	v_pk_fma_f32 v[104:105], v[40:41], v[104:105], v[8:9]
	v_pk_mul_f32 v[102:103], v[102:103], v[160:161] op_sel_hi:[1,0]
	v_pk_mul_f32 v[108:109], v[108:109], v[160:161] op_sel_hi:[1,0]
	v_cvt_pk_bf16_f32 v96, v96, v97
	v_cvt_pk_bf16_f32 v97, v100, v101
	v_lshl_add_u64 v[100:101], v[24:25], 0, s[2:3]
	v_pk_fma_f32 v[108:109], v[44:45], v[108:109], v[12:13]
	v_pk_fma_f32 v[102:103], v[46:47], v[102:103], v[10:11]
	v_pk_mul_f32 v[106:107], v[106:107], v[160:161] op_sel_hi:[1,0]
	v_pk_mul_f32 v[110:111], v[110:111], v[160:161] op_sel_hi:[1,0]
	global_store_dwordx2 v[100:101], v[96:97], off
	v_cvt_pk_bf16_f32 v96, v98, v99
	v_cvt_pk_bf16_f32 v97, v104, v105
	v_pk_fma_f32 v[110:111], v[52:53], v[110:111], v[16:17]
	v_pk_fma_f32 v[106:107], v[54:55], v[106:107], v[14:15]
	global_store_dwordx2 v[100:101], v[96:97], off offset:512
	v_cvt_pk_bf16_f32 v96, v102, v103
	v_cvt_pk_bf16_f32 v97, v108, v109
	global_store_dwordx2 v[100:101], v[96:97], off offset:1024
; #define LAS __attribute__((address_space(3)))
; __device__ __forceinline__ unsigned pkb(float lo, float hi) { f32x2 v = {lo, hi}; bf16x2_t b = __builtin_convertvector(v, bf16x2_t); return __builtin_bit_cast(unsigned, b); }
; template <int R, bool RT = false>
; __device__ __forceinline__ void norm_phase(const NormArgs& a, LAS unsigned char* lds, bool ctx_rows, const float* ctx_src, const float* ctx_shift, const float* ctx_scale) {
;     ...
;             for (int q = 0; q < R; ++q) { const int row = row0 + rr + q;
;                 if (a.src16) { const f16* xr = a.src16 + (size_t)row * DM;
; #pragma unroll
;                     for (int j = 0; j < 4; ++j) { const f16x4 t = *(const f16x4*)(xr + 4 * lane + 256 * j); v[q][j] = (f32x4){(float)t[0], (float)t[1], (float)t[2], (float)t[3]};
;                         if constexpr (RT) { if (j == 0) *(LAS u32x2*)(hs + (rr + q) * 528 + 8 * lane) = __builtin_bit_cast(u32x2, t);
;                             else xp[rr / 4][q][j - 1] = __builtin_bit_cast(u32x2, t); } } }
;     ...
;             for (int q = 0; q < R; ++q) { const int row = row0 + rr + q;
; #pragma unroll
;                 for (int j = 0; j < 4; ++j) v[q][j] = (v[q][j] * rstd[q]) * A[j] + Sh[j];
;                 if (a.fout) {
; #pragma unroll
;                     for (int j = 0; j < 4; ++j) *(f32x4*)(a.fout + (size_t)row * DM + 4 * lane + 256 * j) = v[q][j];
;                 }
;                 if (a.hout) {
; #pragma unroll
;                     for (int j = 0; j < 4; ++j) { u32x2 w; if (a.hbf) { w.x = pkb(v[q][j][0], v[q][j][1]); w.y = pkb(v[q][j][2], v[q][j][3]); } else { w.x = pkh(v[q][j][0], v[q][j][1]); w.y = pkh(v[q][j][2], v[q][j][3]); } *(u32x2*)(a.hout + (size_t)row * DM + 4 * lane + 256 * j) = w; }
;                 }
	v_cvt_pk_bf16_f32 v96, v106, v107
	v_cvt_pk_bf16_f32 v97, v110, v111
	global_store_dwordx2 v[100:101], v[96:97], off offset:1536
	v_pk_mul_f32 v[96:97], v[112:113], v[162:163] op_sel_hi:[1,0]
	v_pk_mul_f32 v[98:99], v[114:115], v[162:163] op_sel_hi:[1,0]
	v_pk_fma_f32 v[96:97], v[36:37], v[96:97], v[2:3]
	v_pk_fma_f32 v[98:99], v[34:35], v[98:99], v[4:5]
	v_pk_mul_f32 v[100:101], v[116:117], v[162:163] op_sel_hi:[1,0]
	v_pk_mul_f32 v[102:103], v[120:121], v[162:163] op_sel_hi:[1,0]
	v_pk_fma_f32 v[100:101], v[42:43], v[100:101], v[6:7]
	v_pk_fma_f32 v[102:103], v[40:41], v[102:103], v[8:9]
	v_pk_mul_f32 v[104:105], v[118:119], v[162:163] op_sel_hi:[1,0]
	v_pk_mul_f32 v[106:107], v[124:125], v[162:163] op_sel_hi:[1,0]
	v_cvt_pk_bf16_f32 v96, v96, v97
	v_cvt_pk_bf16_f32 v97, v98, v99
	v_lshl_add_u64 v[98:99], v[24:25], 0, s[24:25]
	v_pk_fma_f32 v[106:107], v[44:45], v[106:107], v[12:13]
	v_pk_fma_f32 v[104:105], v[46:47], v[104:105], v[10:11]
	v_pk_mul_f32 v[108:109], v[122:123], v[162:163] op_sel_hi:[1,0]
	v_pk_mul_f32 v[110:111], v[126:127], v[162:163] op_sel_hi:[1,0]
	global_store_dwordx2 v[98:99], v[96:97], off
	v_cvt_pk_bf16_f32 v96, v100, v101
	v_cvt_pk_bf16_f32 v97, v102, v103
	v_pk_fma_f32 v[110:111], v[52:53], v[110:111], v[16:17]
	v_pk_fma_f32 v[108:109], v[54:55], v[108:109], v[14:15]
	global_store_dwordx2 v[98:99], v[96:97], off offset:512
	v_cvt_pk_bf16_f32 v96, v104, v105
	v_cvt_pk_bf16_f32 v97, v106, v107
	global_store_dwordx2 v[98:99], v[96:97], off offset:1024
	v_cvt_pk_bf16_f32 v96, v108, v109
	v_cvt_pk_bf16_f32 v97, v110, v111
	global_store_dwordx2 v[98:99], v[96:97], off offset:1536
	v_pk_mul_f32 v[96:97], v[128:129], v[166:167] op_sel_hi:[1,0]
	v_pk_mul_f32 v[98:99], v[132:133], v[166:167] op_sel_hi:[1,0]
	v_pk_fma_f32 v[96:97], v[36:37], v[96:97], v[2:3]
	v_pk_fma_f32 v[98:99], v[34:35], v[98:99], v[4:5]
	v_pk_mul_f32 v[100:101], v[130:131], v[166:167] op_sel_hi:[1,0]
	v_pk_mul_f32 v[102:103], v[136:137], v[166:167] op_sel_hi:[1,0]
	v_rsq_f32_e32 v164, v161
	v_pk_fma_f32 v[102:103], v[40:41], v[102:103], v[8:9]
	v_pk_fma_f32 v[100:101], v[42:43], v[100:101], v[6:7]
	v_pk_mul_f32 v[104:105], v[134:135], v[166:167] op_sel_hi:[1,0]
	v_pk_mul_f32 v[106:107], v[140:141], v[166:167] op_sel_hi:[1,0]
	v_cvt_pk_bf16_f32 v96, v96, v97
	v_cvt_pk_bf16_f32 v97, v98, v99
	v_lshl_add_u64 v[98:99], v[24:25], 0, s[26:27]
	v_pk_fma_f32 v[106:107], v[44:45], v[106:107], v[12:13]
	v_pk_fma_f32 v[104:105], v[46:47], v[104:105], v[10:11]
	v_pk_mul_f32 v[108:109], v[138:139], v[166:167] op_sel_hi:[1,0]
	v_pk_mul_f32 v[110:111], v[142:143], v[166:167] op_sel_hi:[1,0]
	global_store_dwordx2 v[98:99], v[96:97], off
	v_cvt_pk_bf16_f32 v96, v100, v101
	v_cvt_pk_bf16_f32 v97, v102, v103
	v_pk_fma_f32 v[110:111], v[52:53], v[110:111], v[16:17]
	v_pk_fma_f32 v[108:109], v[54:55], v[108:109], v[14:15]
	global_store_dwordx2 v[98:99], v[96:97], off offset:512
	v_cvt_pk_bf16_f32 v96, v104, v105
	v_cvt_pk_bf16_f32 v97, v106, v107
	global_store_dwordx2 v[98:99], v[96:97], off offset:1024
	v_cvt_pk_bf16_f32 v96, v108, v109
	v_cvt_pk_bf16_f32 v97, v110, v111
	global_store_dwordx2 v[98:99], v[96:97], off offset:1536
	v_pk_mul_f32 v[96:97], v[144:145], v[164:165] op_sel_hi:[1,0]
	v_pk_mul_f32 v[98:99], v[146:147], v[164:165] op_sel_hi:[1,0]
	v_pk_fma_f32 v[96:97], v[36:37], v[96:97], v[2:3]
	v_pk_fma_f32 v[98:99], v[34:35], v[98:99], v[4:5]
	v_pk_mul_f32 v[100:101], v[148:149], v[164:165] op_sel_hi:[1,0]
	v_pk_mul_f32 v[102:103], v[152:153], v[164:165] op_sel_hi:[1,0]
	v_pk_fma_f32 v[100:101], v[42:43], v[100:101], v[6:7]
	v_pk_fma_f32 v[102:103], v[40:41], v[102:103], v[8:9]
	v_pk_mul_f32 v[104:105], v[150:151], v[164:165] op_sel_hi:[1,0]
	v_pk_mul_f32 v[106:107], v[156:157], v[164:165] op_sel_hi:[1,0]
	v_cvt_pk_bf16_f32 v96, v96, v97
	v_cvt_pk_bf16_f32 v97, v98, v99
	v_lshl_add_u64 v[98:99], v[24:25], 0, s[28:29]
	s_add_i32 s2, s14, 8
	v_pk_fma_f32 v[106:107], v[44:45], v[106:107], v[12:13]
	v_pk_fma_f32 v[104:105], v[46:47], v[104:105], v[10:11]
	v_pk_mul_f32 v[108:109], v[154:155], v[164:165] op_sel_hi:[1,0]
	v_pk_mul_f32 v[110:111], v[158:159], v[164:165] op_sel_hi:[1,0]
	global_store_dwordx2 v[98:99], v[96:97], off
	v_cvt_pk_bf16_f32 v96, v100, v101
	v_cvt_pk_bf16_f32 v97, v102, v103
	s_ashr_i32 s3, s2, 31
	v_pk_fma_f32 v[110:111], v[52:53], v[110:111], v[16:17]
	v_pk_fma_f32 v[108:109], v[54:55], v[108:109], v[14:15]
	global_store_dwordx2 v[98:99], v[96:97], off offset:512
	v_cvt_pk_bf16_f32 v96, v104, v105
	v_cvt_pk_bf16_f32 v97, v106, v107
	s_lshl_b64 s[24:25], s[2:3], 11
	s_add_i32 s2, s14, 9
	global_store_dwordx2 v[98:99], v[96:97], off offset:1024
	v_cvt_pk_bf16_f32 v96, v108, v109
	v_cvt_pk_bf16_f32 v97, v110, v111
	s_ashr_i32 s3, s2, 31
	global_store_dwordx2 v[98:99], v[96:97], off offset:1536
	s_lshl_b64 s[26:27], s[2:3], 11
	v_lshl_add_u64 v[96:97], v[22:23], 0, s[24:25]
	v_lshl_add_u64 v[108:109], v[22:23], 0, s[26:27]
	global_load_dwordx2 v[102:103], v[96:97], off nt
	global_load_dwordx2 v[100:101], v[96:97], off offset:512 nt
	global_load_dwordx2 v[98:99], v[96:97], off offset:1024 nt
	global_load_dwordx2 v[104:105], v[108:109], off nt
	s_add_i32 s2, s14, 10
	s_ashr_i32 s3, s2, 31
	s_lshl_b64 s[28:29], s[2:3], 11
	s_add_i32 s2, s14, 11
	s_ashr_i32 s3, s2, 31
	s_lshl_b64 s[30:31], s[2:3], 11
	v_lshl_add_u64 v[178:179], v[22:23], 0, s[30:31]
	global_load_dwordx2 v[106:107], v[108:109], off offset:512 nt
	global_load_dwordx2 v[116:117], v[178:179], off nt
	global_load_dwordx2 v[118:119], v[178:179], off offset:512 nt
	v_cndmask_b32_e64 v185, v165, v164, s[6:7]
	global_load_dwordx2 v[96:97], v[96:97], off offset:1536 nt
	s_add_i32 s2, s14, 12
	s_ashr_i32 s3, s2, 31
	s_waitcnt vmcnt(7)
; #define LAS __attribute__((address_space(3)))
; template <int R, bool RT = false>
; __device__ __forceinline__ void norm_phase(const NormArgs& a, LAS unsigned char* lds, bool ctx_rows, const float* ctx_src, const float* ctx_shift, const float* ctx_scale) {
;     ...
;             for (int q = 0; q < R; ++q) { const int row = row0 + rr + q;
;                 if (a.src16) { const f16* xr = a.src16 + (size_t)row * DM;
; #pragma unroll
;                     for (int j = 0; j < 4; ++j) { const f16x4 t = *(const f16x4*)(xr + 4 * lane + 256 * j); v[q][j] = (f32x4){(float)t[0], (float)t[1], (float)t[2], (float)t[3]};
;                         if constexpr (RT) { if (j == 0) *(LAS u32x2*)(hs + (rr + q) * 528 + 8 * lane) = __builtin_bit_cast(u32x2, t);
;                             else xp[rr / 4][q][j - 1] = __builtin_bit_cast(u32x2, t); } } }
;                 else { const float* xr = a.src + (size_t)row * DM;
; #pragma unroll
;                     for (int j = 0; j < 4; ++j) v[q][j] = *(const f32x4*)(xr + 4 * lane + 256 * j); } }
;             if (a.y2) {
;                 unsigned long long mask[R]; int ee[R][4]; float wgt[R][4]; f16x4 ld[R][4][4];
;                 int cnt[R];
; #pragma unroll
;                 for (int q = 0; q < R; ++q) { mask[q] = __ballot(sl[q] >= 0); cnt[q] = __builtin_popcountll(mask[q]);
; #pragma unroll
;                     for (int i = 0; i < 4; ++i) { if (mask[q]) { ee[q][i] = __builtin_ctzll(mask[q]); mask[q] &= mask[q] - 1; wgt[q][i] = 1.f; } else { ee[q][i] = i ? ee[q][0] : 0; wgt[q][i] = 0.f; } }
; #pragma unroll
;                     for (int i = 0; i < 4; ++i) {
;                         if (i < cnt[q]) { int slot = __shfl(sl[q], ee[q][i]); slot = slot < 0 ? 0 : slot; const f16* yr = a.y2 + ((size_t)ee[q][i] * EROWS + b * CAP + slot) * DM + 4 * lane;
; #pragma unroll
;                             for (int j = 0; j < 4; ++j) ld[q][i][j] = *(const f16x4*)(yr + 256 * j); } } }
; #pragma unroll
;                 for (int q = 0; q < R; ++q) { const int row = row0 + rr + q;
;                     f32x4 cs[4];
; #pragma unroll
;                     for (int j = 0; j < 4; ++j) cs[j] = (f32x4){0.f, 0.f, 0.f, 0.f};
; #pragma unroll
;                     for (int i = 0; i < 4; ++i) if (i < cnt[q]) {
; #pragma unroll
	v_cvt_f32_f16_e32 v120, v102
	v_cvt_f32_f16_sdwa v121, v102 dst_sel:DWORD dst_unused:UNUSED_PAD src0_sel:WORD_1
	v_cvt_f32_f16_e32 v124, v103
	v_cvt_f32_f16_sdwa v125, v103 dst_sel:DWORD dst_unused:UNUSED_PAD src0_sel:WORD_1
	s_waitcnt vmcnt(4)
	v_cvt_f32_f16_e32 v136, v104
	v_cvt_f32_f16_sdwa v137, v104 dst_sel:DWORD dst_unused:UNUSED_PAD src0_sel:WORD_1
	v_cvt_f32_f16_e32 v138, v105
	v_cvt_f32_f16_sdwa v139, v105 dst_sel:DWORD dst_unused:UNUSED_PAD src0_sel:WORD_1
	ds_write2_b64 v226, v[102:103], v[104:105] offset0:16 offset1:82
	global_load_dwordx2 v[104:105], v[108:109], off offset:1024 nt
	global_load_dwordx2 v[102:103], v[108:109], off offset:1536 nt
	v_lshl_add_u64 v[108:109], v[22:23], 0, s[28:29]
	global_load_dwordx2 v[114:115], v[108:109], off nt
	global_load_dwordx2 v[112:113], v[108:109], off offset:512 nt
	global_load_dwordx2 v[110:111], v[108:109], off offset:1024 nt
	s_waitcnt vmcnt(7)
	v_cvt_f32_f16_e32 v168, v116
	global_load_dwordx2 v[108:109], v[108:109], off offset:1536 nt
	v_cvt_f32_f16_sdwa v169, v116 dst_sel:DWORD dst_unused:UNUSED_PAD src0_sel:WORD_1
	v_cvt_f32_f16_e32 v170, v117
	v_cvt_f32_f16_sdwa v171, v117 dst_sel:DWORD dst_unused:UNUSED_PAD src0_sel:WORD_1
	v_cvt_f32_f16_e32 v122, v100
	v_cvt_f32_f16_sdwa v123, v100 dst_sel:DWORD dst_unused:UNUSED_PAD src0_sel:WORD_1
	v_cvt_f32_f16_e32 v128, v101
	v_cvt_f32_f16_sdwa v129, v101 dst_sel:DWORD dst_unused:UNUSED_PAD src0_sel:WORD_1
	v_cvt_f32_f16_e32 v126, v98
	v_cvt_f32_f16_sdwa v127, v98 dst_sel:DWORD dst_unused:UNUSED_PAD src0_sel:WORD_1
	v_cvt_f32_f16_e32 v132, v99
	v_cvt_f32_f16_sdwa v133, v99 dst_sel:DWORD dst_unused:UNUSED_PAD src0_sel:WORD_1
	v_pk_mul_f32 v[194:195], v[122:123], v[122:123]
	v_pk_mul_f32 v[196:197], v[128:129], v[128:129]
	s_waitcnt vmcnt(6)
	v_cvt_f32_f16_e32 v130, v96
	v_cvt_f32_f16_sdwa v131, v96 dst_sel:DWORD dst_unused:UNUSED_PAD src0_sel:WORD_1
	v_cvt_f32_f16_e32 v134, v97
	v_cvt_f32_f16_sdwa v135, v97 dst_sel:DWORD dst_unused:UNUSED_PAD src0_sel:WORD_1
	v_pk_mul_f32 v[190:191], v[120:121], v[120:121]
	v_pk_mul_f32 v[192:193], v[124:125], v[124:125]
	v_add_f32_e32 v184, v196, v197
	v_add_f32_e32 v188, v194, v195
	v_add_f32_e32 v184, v188, v184
	v_add_f32_e32 v188, v192, v193
	v_add_f32_e32 v190, v190, v191
	v_pk_mul_f32 v[198:199], v[126:127], v[126:127]
	v_pk_mul_f32 v[200:201], v[132:133], v[132:133]
	v_add_f32_e32 v188, v190, v188
	v_add_f32_e32 v184, v188, v184
	v_add_f32_e32 v188, v200, v201
	v_add_f32_e32 v190, v198, v199
	v_pk_mul_f32 v[202:203], v[130:131], v[130:131]
	v_pk_mul_f32 v[204:205], v[134:135], v[134:135]
	v_add_f32_e32 v188, v190, v188
	v_add_f32_e32 v184, v184, v188
	v_add_f32_e32 v188, v204, v205
	v_add_f32_e32 v190, v202, v203
	v_add_f32_e32 v188, v190, v188
	v_add_f32_e32 v184, v184, v188
	v_mov_b32_e32 v188, 0
	v_cvt_f32_f16_e32 v140, v106
	v_add_f32_dpp v184, v184, v184 quad_perm:[1,0,3,2] row_mask:0xf bank_mask:0xf bound_ctrl:1
	v_cvt_f32_f16_sdwa v141, v106 dst_sel:DWORD dst_unused:UNUSED_PAD src0_sel:WORD_1
	v_cvt_f32_f16_e32 v144, v107
	v_add_f32_dpp v184, v184, v184 quad_perm:[2,3,0,1] row_mask:0xf bank_mask:0xf bound_ctrl:1
	v_cvt_f32_f16_sdwa v145, v107 dst_sel:DWORD dst_unused:UNUSED_PAD src0_sel:WORD_1
	v_pk_mul_f32 v[194:195], v[140:141], v[140:141]
	v_add_f32_dpp v184, v184, v184 row_half_mirror row_mask:0xf bank_mask:0xf bound_ctrl:1
	v_pk_mul_f32 v[190:191], v[136:137], v[136:137]
	v_pk_mul_f32 v[196:197], v[144:145], v[144:145]
	v_add_f32_dpp v184, v184, v184 row_mirror row_mask:0xf bank_mask:0xf bound_ctrl:1
	v_pk_mul_f32 v[192:193], v[138:139], v[138:139]
	v_add_f32_e32 v190, v190, v191
	v_mov_b32_dpp v188, v184 row_bcast:15 row_mask:0xa bank_mask:0xf
	v_add_f32_e32 v184, v184, v188
	v_mov_b32_e32 v188, 0
	s_waitcnt vmcnt(5)
	v_cvt_f32_f16_e32 v142, v104
	v_mov_b32_dpp v188, v184 row_bcast:31 row_mask:0xc bank_mask:0xf
	v_add_f32_e32 v184, v184, v188
	s_waitcnt vmcnt(3)
	ds_write2_b64 v226, v[114:115], v[116:117] offset0:148 offset1:214
	global_load_dwordx2 v[116:117], v[178:179], off offset:1024 nt
	v_cvt_f32_f16_e32 v152, v114
	v_cvt_f32_f16_sdwa v153, v114 dst_sel:DWORD dst_unused:UNUSED_PAD src0_sel:WORD_1
	v_cvt_f32_f16_e32 v156, v115
	v_cvt_f32_f16_sdwa v157, v115 dst_sel:DWORD dst_unused:UNUSED_PAD src0_sel:WORD_1
	global_load_dwordx2 v[114:115], v[178:179], off offset:1536 nt
	v_readlane_b32 s0, v184, 63
	v_cvt_f32_f16_sdwa v143, v104 dst_sel:DWORD dst_unused:UNUSED_PAD src0_sel:WORD_1
	v_cvt_f32_f16_e32 v148, v105
	v_fma_f32 v184, s0, v214, v213
	v_rsq_f32_e32 v184, v184
	v_cvt_f32_f16_sdwa v149, v105 dst_sel:DWORD dst_unused:UNUSED_PAD src0_sel:WORD_1
	v_cvt_f32_f16_e32 v146, v102
	v_cvt_f32_f16_sdwa v147, v102 dst_sel:DWORD dst_unused:UNUSED_PAD src0_sel:WORD_1
	v_cvt_f32_f16_e32 v150, v103
	v_cvt_f32_f16_sdwa v151, v103 dst_sel:DWORD dst_unused:UNUSED_PAD src0_sel:WORD_1
	v_cndmask_b32_e64 v210, v186, v184, s[8:9]
	v_add_f32_e32 v186, v196, v197
	v_add_f32_e32 v188, v194, v195
	v_add_f32_e32 v186, v188, v186
	v_add_f32_e32 v188, v192, v193
	v_pk_mul_f32 v[198:199], v[142:143], v[142:143]
	v_pk_mul_f32 v[200:201], v[148:149], v[148:149]
	v_add_f32_e32 v188, v190, v188
	v_add_f32_e32 v186, v188, v186
	v_add_f32_e32 v188, v200, v201
	v_add_f32_e32 v190, v198, v199
	v_pk_mul_f32 v[202:203], v[146:147], v[146:147]
	v_pk_mul_f32 v[204:205], v[150:151], v[150:151]
	v_add_f32_e32 v188, v190, v188
	v_add_f32_e32 v186, v186, v188
	v_add_f32_e32 v188, v204, v205
	v_add_f32_e32 v190, v202, v203
	v_add_f32_e32 v188, v190, v188
	v_add_f32_e32 v186, v186, v188
	v_mov_b32_e32 v188, 0
	s_waitcnt vmcnt(4)
; template <int R, bool RT = false>
; __device__ __forceinline__ void norm_phase(const NormArgs& a, LAS unsigned char* lds, bool ctx_rows, const float* ctx_src, const float* ctx_shift, const float* ctx_scale) {
;     ...
;             for (int q = 0; q < R; ++q) { float ss = 0.f;
; #pragma unroll
;                 for (int j = 0; j < 4; ++j) ss += (v[q][j][0] * v[q][j][0] + v[q][j][1] * v[q][j][1]) + (v[q][j][2] * v[q][j][2] + v[q][j][3] * v[q][j][3]);
;                 rstd[q] = __builtin_amdgcn_rsqf(wave_sum(ss) * (1.f / DM) + EPS);
;                 if constexpr (RT) rsel[q] = ((lane >> 4) == rr / 4) ? rstd[q] : rsel[q]; }
; #pragma unroll
;             for (int q = 0; q < R; ++q) { const int row = row0 + rr + q;
; #pragma unroll
;                 for (int j = 0; j < 4; ++j) v[q][j] = (v[q][j] * rstd[q]) * A[j] + Sh[j];
	v_cvt_f32_f16_e32 v154, v112
	v_add_f32_dpp v186, v186, v186 quad_perm:[1,0,3,2] row_mask:0xf bank_mask:0xf bound_ctrl:1
	v_cvt_f32_f16_sdwa v155, v112 dst_sel:DWORD dst_unused:UNUSED_PAD src0_sel:WORD_1
	v_cvt_f32_f16_e32 v160, v113
	v_add_f32_dpp v186, v186, v186 quad_perm:[2,3,0,1] row_mask:0xf bank_mask:0xf bound_ctrl:1
	v_cvt_f32_f16_sdwa v161, v113 dst_sel:DWORD dst_unused:UNUSED_PAD src0_sel:WORD_1
	s_waitcnt vmcnt(3)
	v_cvt_f32_f16_e32 v158, v110
	v_add_f32_dpp v186, v186, v186 row_half_mirror row_mask:0xf bank_mask:0xf bound_ctrl:1
	v_cvt_f32_f16_sdwa v159, v110 dst_sel:DWORD dst_unused:UNUSED_PAD src0_sel:WORD_1
	v_cvt_f32_f16_e32 v164, v111
	v_add_f32_dpp v186, v186, v186 row_mirror row_mask:0xf bank_mask:0xf bound_ctrl:1
	v_cvt_f32_f16_sdwa v165, v111 dst_sel:DWORD dst_unused:UNUSED_PAD src0_sel:WORD_1
	v_pk_mul_f32 v[194:195], v[154:155], v[154:155]
	v_mov_b32_dpp v188, v186 row_bcast:15 row_mask:0xa bank_mask:0xf
	v_add_f32_e32 v186, v186, v188
	v_mov_b32_e32 v188, 0
	v_pk_mul_f32 v[196:197], v[160:161], v[160:161]
	s_waitcnt vmcnt(2)
	v_cvt_f32_f16_e32 v162, v108
	v_mov_b32_dpp v188, v186 row_bcast:31 row_mask:0xc bank_mask:0xf
	v_add_f32_e32 v186, v186, v188
	v_cvt_f32_f16_sdwa v163, v108 dst_sel:DWORD dst_unused:UNUSED_PAD src0_sel:WORD_1
	v_readlane_b32 s0, v186, 63
	v_cvt_f32_f16_e32 v166, v109
	v_cvt_f32_f16_sdwa v167, v109 dst_sel:DWORD dst_unused:UNUSED_PAD src0_sel:WORD_1
	v_fma_f32 v186, s0, v214, v213
	v_rsq_f32_e32 v186, v186
	v_pk_mul_f32 v[190:191], v[152:153], v[152:153]
	v_pk_mul_f32 v[192:193], v[156:157], v[156:157]
	v_add_f32_e32 v188, v194, v195
	v_cndmask_b32_e64 v212, v187, v186, s[8:9]
	v_add_f32_e32 v187, v196, v197
	v_add_f32_e32 v187, v188, v187
	v_add_f32_e32 v188, v192, v193
	v_add_f32_e32 v190, v190, v191
	v_pk_mul_f32 v[198:199], v[158:159], v[158:159]
	v_pk_mul_f32 v[200:201], v[164:165], v[164:165]
	v_add_f32_e32 v188, v190, v188
	v_add_f32_e32 v187, v188, v187
	v_add_f32_e32 v188, v200, v201
	v_add_f32_e32 v190, v198, v199
	v_pk_mul_f32 v[202:203], v[162:163], v[162:163]
	v_pk_mul_f32 v[204:205], v[166:167], v[166:167]
	v_add_f32_e32 v188, v190, v188
	v_add_f32_e32 v187, v187, v188
	v_add_f32_e32 v188, v204, v205
	v_add_f32_e32 v190, v202, v203
	v_add_f32_e32 v188, v190, v188
	v_add_f32_e32 v187, v187, v188
	v_mov_b32_e32 v188, 0
	v_cvt_f32_f16_e32 v172, v118
	v_add_f32_dpp v187, v187, v187 quad_perm:[1,0,3,2] row_mask:0xf bank_mask:0xf bound_ctrl:1
	v_cvt_f32_f16_sdwa v173, v118 dst_sel:DWORD dst_unused:UNUSED_PAD src0_sel:WORD_1
	v_cvt_f32_f16_e32 v176, v119
	v_add_f32_dpp v187, v187, v187 quad_perm:[2,3,0,1] row_mask:0xf bank_mask:0xf bound_ctrl:1
	v_cvt_f32_f16_sdwa v177, v119 dst_sel:DWORD dst_unused:UNUSED_PAD src0_sel:WORD_1
	s_waitcnt vmcnt(1)
	v_cvt_f32_f16_e32 v174, v116
	v_add_f32_dpp v187, v187, v187 row_half_mirror row_mask:0xf bank_mask:0xf bound_ctrl:1
	v_cvt_f32_f16_sdwa v175, v116 dst_sel:DWORD dst_unused:UNUSED_PAD src0_sel:WORD_1
	v_cvt_f32_f16_e32 v180, v117
	v_add_f32_dpp v187, v187, v187 row_mirror row_mask:0xf bank_mask:0xf bound_ctrl:1
	v_cvt_f32_f16_sdwa v181, v117 dst_sel:DWORD dst_unused:UNUSED_PAD src0_sel:WORD_1
	v_pk_mul_f32 v[190:191], v[168:169], v[168:169]
	v_mov_b32_dpp v188, v187 row_bcast:15 row_mask:0xa bank_mask:0xf
	v_add_f32_e32 v187, v187, v188
	v_mov_b32_e32 v188, 0
	v_pk_mul_f32 v[192:193], v[170:171], v[170:171]
	s_waitcnt vmcnt(0)
	v_cvt_f32_f16_e32 v178, v114
	v_mov_b32_dpp v188, v187 row_bcast:31 row_mask:0xc bank_mask:0xf
	v_add_f32_e32 v187, v187, v188
	v_cvt_f32_f16_sdwa v179, v114 dst_sel:DWORD dst_unused:UNUSED_PAD src0_sel:WORD_1
	v_readlane_b32 s0, v187, 63
	v_cvt_f32_f16_e32 v182, v115
	v_cvt_f32_f16_sdwa v183, v115 dst_sel:DWORD dst_unused:UNUSED_PAD src0_sel:WORD_1
	v_fma_f32 v187, s0, v214, v213
	v_rsq_f32_e32 v188, v187
	v_pk_mul_f32 v[194:195], v[172:173], v[172:173]
	v_pk_mul_f32 v[196:197], v[176:177], v[176:177]
	v_add_f32_e32 v187, v192, v193
	v_cndmask_b32_e64 v230, v189, v188, s[8:9]
	v_add_f32_e32 v189, v190, v191
	v_add_f32_e32 v187, v189, v187
	v_add_f32_e32 v189, v196, v197
	v_add_f32_e32 v190, v194, v195
	v_pk_mul_f32 v[198:199], v[174:175], v[174:175]
	v_pk_mul_f32 v[200:201], v[180:181], v[180:181]
	v_add_f32_e32 v189, v190, v189
	v_add_f32_e32 v187, v187, v189
	v_add_f32_e32 v189, v200, v201
	v_add_f32_e32 v190, v198, v199
	v_pk_mul_f32 v[202:203], v[178:179], v[178:179]
	v_pk_mul_f32 v[204:205], v[182:183], v[182:183]
	v_add_f32_e32 v189, v190, v189
	v_add_f32_e32 v187, v187, v189
	v_add_f32_e32 v189, v204, v205
	v_add_f32_e32 v190, v202, v203
	v_add_f32_e32 v189, v190, v189
	v_add_f32_e32 v187, v187, v189
	v_mov_b32_e32 v189, 0
	v_pk_mul_f32 v[120:121], v[120:121], v[184:185] op_sel_hi:[1,0]
	v_add_f32_dpp v187, v187, v187 quad_perm:[1,0,3,2] row_mask:0xf bank_mask:0xf bound_ctrl:1
	v_pk_mul_f32 v[124:125], v[124:125], v[184:185] op_sel_hi:[1,0]
	v_pk_fma_f32 v[120:121], v[36:37], v[120:121], v[2:3]
	v_add_f32_dpp v187, v187, v187 quad_perm:[2,3,0,1] row_mask:0xf bank_mask:0xf bound_ctrl:1
	v_pk_fma_f32 v[124:125], v[34:35], v[124:125], v[4:5]
	v_pk_mul_f32 v[122:123], v[122:123], v[184:185] op_sel_hi:[1,0]
	v_add_f32_dpp v187, v187, v187 row_half_mirror row_mask:0xf bank_mask:0xf bound_ctrl:1
	v_pk_mul_f32 v[128:129], v[128:129], v[184:185] op_sel_hi:[1,0]
	v_pk_fma_f32 v[122:123], v[42:43], v[122:123], v[6:7]
	v_add_f32_dpp v187, v187, v187 row_mirror row_mask:0xf bank_mask:0xf bound_ctrl:1
	v_pk_fma_f32 v[128:129], v[40:41], v[128:129], v[8:9]
	v_pk_mul_f32 v[126:127], v[126:127], v[184:185] op_sel_hi:[1,0]
	v_mov_b32_dpp v189, v187 row_bcast:15 row_mask:0xa bank_mask:0xf
	v_add_f32_e32 v187, v187, v189
; #define LAS __attribute__((address_space(3)))
; __device__ __forceinline__ unsigned pkb(float lo, float hi) { f32x2 v = {lo, hi}; bf16x2_t b = __builtin_convertvector(v, bf16x2_t); return __builtin_bit_cast(unsigned, b); }
; template <int R, bool RT = false>
; __device__ __forceinline__ void norm_phase(const NormArgs& a, LAS unsigned char* lds, bool ctx_rows, const float* ctx_src, const float* ctx_shift, const float* ctx_scale) {
;     ...
;             for (int q = 0; q < R; ++q) { const int row = row0 + rr + q;
;                 if (a.src16) { const f16* xr = a.src16 + (size_t)row * DM;
; #pragma unroll
;                     for (int j = 0; j < 4; ++j) { const f16x4 t = *(const f16x4*)(xr + 4 * lane + 256 * j); v[q][j] = (f32x4){(float)t[0], (float)t[1], (float)t[2], (float)t[3]};
;                         if constexpr (RT) { if (j == 0) *(LAS u32x2*)(hs + (rr + q) * 528 + 8 * lane) = __builtin_bit_cast(u32x2, t);
;                             else xp[rr / 4][q][j - 1] = __builtin_bit_cast(u32x2, t); } } }
;     ...
;             for (int q = 0; q < R; ++q) { const int row = row0 + rr + q;
; #pragma unroll
;                 for (int j = 0; j < 4; ++j) v[q][j] = (v[q][j] * rstd[q]) * A[j] + Sh[j];
;                 if (a.fout) {
; #pragma unroll
;                     for (int j = 0; j < 4; ++j) *(f32x4*)(a.fout + (size_t)row * DM + 4 * lane + 256 * j) = v[q][j];
;                 }
;                 if (a.hout) {
; #pragma unroll
;                     for (int j = 0; j < 4; ++j) { u32x2 w; if (a.hbf) { w.x = pkb(v[q][j][0], v[q][j][1]); w.y = pkb(v[q][j][2], v[q][j][3]); } else { w.x = pkh(v[q][j][0], v[q][j][1]); w.y = pkh(v[q][j][2], v[q][j][3]); } *(u32x2*)(a.hout + (size_t)row * DM + 4 * lane + 256 * j) = w; }
;                 }
	v_mov_b32_e32 v189, 0
	v_pk_mul_f32 v[132:133], v[132:133], v[184:185] op_sel_hi:[1,0]
	v_cvt_pk_bf16_f32 v120, v120, v121
	v_mov_b32_dpp v189, v187 row_bcast:31 row_mask:0xc bank_mask:0xf
	v_cvt_pk_bf16_f32 v121, v124, v125
	v_lshl_add_u64 v[124:125], v[24:25], 0, s[24:25]
	v_add_f32_e32 v187, v187, v189
	v_pk_fma_f32 v[132:133], v[44:45], v[132:133], v[12:13]
	v_pk_fma_f32 v[126:127], v[46:47], v[126:127], v[10:11]
	v_pk_mul_f32 v[130:131], v[130:131], v[184:185] op_sel_hi:[1,0]
	v_pk_mul_f32 v[134:135], v[134:135], v[184:185] op_sel_hi:[1,0]
	global_store_dwordx2 v[124:125], v[120:121], off
	v_cvt_pk_bf16_f32 v120, v122, v123
	v_cvt_pk_bf16_f32 v121, v128, v129
	v_readlane_b32 s0, v187, 63
	v_pk_fma_f32 v[134:135], v[52:53], v[134:135], v[16:17]
	v_pk_fma_f32 v[130:131], v[54:55], v[130:131], v[14:15]
	global_store_dwordx2 v[124:125], v[120:121], off offset:512
	v_cvt_pk_bf16_f32 v120, v126, v127
	v_cvt_pk_bf16_f32 v121, v132, v133
	v_fma_f32 v187, s0, v214, v213
	global_store_dwordx2 v[124:125], v[120:121], off offset:1024
	v_cvt_pk_bf16_f32 v120, v130, v131
	v_cvt_pk_bf16_f32 v121, v134, v135
	global_store_dwordx2 v[124:125], v[120:121], off offset:1536
	v_pk_mul_f32 v[120:121], v[136:137], v[186:187] op_sel_hi:[1,0]
	v_pk_mul_f32 v[122:123], v[138:139], v[186:187] op_sel_hi:[1,0]
	v_pk_fma_f32 v[120:121], v[36:37], v[120:121], v[2:3]
	v_pk_fma_f32 v[122:123], v[34:35], v[122:123], v[4:5]
	v_pk_mul_f32 v[124:125], v[140:141], v[186:187] op_sel_hi:[1,0]
	v_pk_mul_f32 v[126:127], v[144:145], v[186:187] op_sel_hi:[1,0]
	v_pk_fma_f32 v[124:125], v[42:43], v[124:125], v[6:7]
	v_pk_fma_f32 v[126:127], v[40:41], v[126:127], v[8:9]
	v_pk_mul_f32 v[128:129], v[142:143], v[186:187] op_sel_hi:[1,0]
	v_pk_mul_f32 v[130:131], v[148:149], v[186:187] op_sel_hi:[1,0]
	v_cvt_pk_bf16_f32 v120, v120, v121
	v_cvt_pk_bf16_f32 v121, v122, v123
	v_lshl_add_u64 v[122:123], v[24:25], 0, s[26:27]
	v_pk_fma_f32 v[130:131], v[44:45], v[130:131], v[12:13]
	v_pk_fma_f32 v[128:129], v[46:47], v[128:129], v[10:11]
	v_pk_mul_f32 v[132:133], v[146:147], v[186:187] op_sel_hi:[1,0]
	v_pk_mul_f32 v[134:135], v[150:151], v[186:187] op_sel_hi:[1,0]
	global_store_dwordx2 v[122:123], v[120:121], off
	v_cvt_pk_bf16_f32 v120, v124, v125
	v_cvt_pk_bf16_f32 v121, v126, v127
	v_pk_fma_f32 v[134:135], v[52:53], v[134:135], v[16:17]
	v_pk_fma_f32 v[132:133], v[54:55], v[132:133], v[14:15]
	global_store_dwordx2 v[122:123], v[120:121], off offset:512
	v_cvt_pk_bf16_f32 v120, v128, v129
	v_cvt_pk_bf16_f32 v121, v130, v131
	global_store_dwordx2 v[122:123], v[120:121], off offset:1024
	v_cvt_pk_bf16_f32 v120, v132, v133
	v_cvt_pk_bf16_f32 v121, v134, v135
	global_store_dwordx2 v[122:123], v[120:121], off offset:1536
	v_pk_mul_f32 v[120:121], v[152:153], v[188:189] op_sel_hi:[1,0]
	v_pk_mul_f32 v[122:123], v[156:157], v[188:189] op_sel_hi:[1,0]
	v_pk_fma_f32 v[120:121], v[36:37], v[120:121], v[2:3]
	v_pk_fma_f32 v[122:123], v[34:35], v[122:123], v[4:5]
	v_pk_mul_f32 v[124:125], v[154:155], v[188:189] op_sel_hi:[1,0]
	v_pk_mul_f32 v[126:127], v[160:161], v[188:189] op_sel_hi:[1,0]
	v_rsq_f32_e32 v190, v187
	v_pk_fma_f32 v[126:127], v[40:41], v[126:127], v[8:9]
	v_pk_fma_f32 v[124:125], v[42:43], v[124:125], v[6:7]
	v_pk_mul_f32 v[128:129], v[158:159], v[188:189] op_sel_hi:[1,0]
	v_pk_mul_f32 v[130:131], v[164:165], v[188:189] op_sel_hi:[1,0]
	v_cvt_pk_bf16_f32 v120, v120, v121
	v_cvt_pk_bf16_f32 v121, v122, v123
	v_lshl_add_u64 v[122:123], v[24:25], 0, s[28:29]
	v_pk_fma_f32 v[130:131], v[44:45], v[130:131], v[12:13]
	v_pk_fma_f32 v[128:129], v[46:47], v[128:129], v[10:11]
	v_pk_mul_f32 v[132:133], v[162:163], v[188:189] op_sel_hi:[1,0]
	v_pk_mul_f32 v[134:135], v[166:167], v[188:189] op_sel_hi:[1,0]
	global_store_dwordx2 v[122:123], v[120:121], off
	v_cvt_pk_bf16_f32 v120, v124, v125
	v_cvt_pk_bf16_f32 v121, v126, v127
	v_pk_fma_f32 v[134:135], v[52:53], v[134:135], v[16:17]
	v_pk_fma_f32 v[132:133], v[54:55], v[132:133], v[14:15]
	global_store_dwordx2 v[122:123], v[120:121], off offset:512
	v_cvt_pk_bf16_f32 v120, v128, v129
	v_cvt_pk_bf16_f32 v121, v130, v131
	global_store_dwordx2 v[122:123], v[120:121], off offset:1024
	v_cvt_pk_bf16_f32 v120, v132, v133
	v_cvt_pk_bf16_f32 v121, v134, v135
	global_store_dwordx2 v[122:123], v[120:121], off offset:1536
	v_pk_mul_f32 v[120:121], v[168:169], v[190:191] op_sel_hi:[1,0]
	v_pk_mul_f32 v[122:123], v[170:171], v[190:191] op_sel_hi:[1,0]
	v_pk_fma_f32 v[120:121], v[36:37], v[120:121], v[2:3]
	v_pk_fma_f32 v[122:123], v[34:35], v[122:123], v[4:5]
	v_pk_mul_f32 v[124:125], v[172:173], v[190:191] op_sel_hi:[1,0]
	v_pk_mul_f32 v[126:127], v[176:177], v[190:191] op_sel_hi:[1,0]
	v_pk_fma_f32 v[124:125], v[42:43], v[124:125], v[6:7]
	v_pk_fma_f32 v[126:127], v[40:41], v[126:127], v[8:9]
	v_pk_mul_f32 v[128:129], v[174:175], v[190:191] op_sel_hi:[1,0]
	v_pk_mul_f32 v[130:131], v[180:181], v[190:191] op_sel_hi:[1,0]
	v_cvt_pk_bf16_f32 v120, v120, v121
	v_cvt_pk_bf16_f32 v121, v122, v123
	v_lshl_add_u64 v[122:123], v[24:25], 0, s[30:31]
	v_pk_fma_f32 v[130:131], v[44:45], v[130:131], v[12:13]
	v_pk_fma_f32 v[128:129], v[46:47], v[128:129], v[10:11]
	v_pk_mul_f32 v[132:133], v[178:179], v[190:191] op_sel_hi:[1,0]
	v_pk_mul_f32 v[134:135], v[182:183], v[190:191] op_sel_hi:[1,0]
	global_store_dwordx2 v[122:123], v[120:121], off
	v_cvt_pk_bf16_f32 v120, v124, v125
	v_cvt_pk_bf16_f32 v121, v126, v127
	v_pk_fma_f32 v[134:135], v[52:53], v[134:135], v[16:17]
	v_pk_fma_f32 v[132:133], v[54:55], v[132:133], v[14:15]
	global_store_dwordx2 v[122:123], v[120:121], off offset:512
	v_cvt_pk_bf16_f32 v120, v128, v129
	v_cvt_pk_bf16_f32 v121, v130, v131
	s_lshl_b64 s[24:25], s[2:3], 11
	s_add_i32 s2, s14, 13
	global_store_dwordx2 v[122:123], v[120:121], off offset:1024
	v_cvt_pk_bf16_f32 v120, v132, v133
	v_cvt_pk_bf16_f32 v121, v134, v135
	s_ashr_i32 s3, s2, 31
	global_store_dwordx2 v[122:123], v[120:121], off offset:1536
	s_lshl_b64 s[26:27], s[2:3], 11
	v_lshl_add_u64 v[120:121], v[22:23], 0, s[24:25]
	v_lshl_add_u64 v[132:133], v[22:23], 0, s[26:27]
	global_load_dwordx2 v[126:127], v[120:121], off nt
	global_load_dwordx2 v[124:125], v[120:121], off offset:512 nt
	global_load_dwordx2 v[122:123], v[120:121], off offset:1024 nt
	global_load_dwordx2 v[128:129], v[132:133], off nt
	s_add_i32 s2, s14, 14
	s_ashr_i32 s3, s2, 31
	s_lshl_b64 s[28:29], s[2:3], 11
	s_add_i32 s2, s14, 15
	s_ashr_i32 s3, s2, 31
	s_lshl_b64 s[30:31], s[2:3], 11
	v_lshl_add_u64 v[204:205], v[22:23], 0, s[30:31]
	global_load_dwordx2 v[130:131], v[132:133], off offset:512 nt
	global_load_dwordx2 v[188:189], v[204:205], off nt
	v_cndmask_b32_e64 v231, v185, v190, s[8:9]
	global_load_dwordx2 v[120:121], v[120:121], off offset:1536 nt
	s_waitcnt vmcnt(6)
; #define LAS __attribute__((address_space(3)))
; template <int R, bool RT = false>
; __device__ __forceinline__ void norm_phase(const NormArgs& a, LAS unsigned char* lds, bool ctx_rows, const float* ctx_src, const float* ctx_shift, const float* ctx_scale) {
;     ...
;             for (int q = 0; q < R; ++q) { const int row = row0 + rr + q;
;                 if (a.src16) { const f16* xr = a.src16 + (size_t)row * DM;
; #pragma unroll
;                     for (int j = 0; j < 4; ++j) { const f16x4 t = *(const f16x4*)(xr + 4 * lane + 256 * j); v[q][j] = (f32x4){(float)t[0], (float)t[1], (float)t[2], (float)t[3]};
;                         if constexpr (RT) { if (j == 0) *(LAS u32x2*)(hs + (rr + q) * 528 + 8 * lane) = __builtin_bit_cast(u32x2, t);
;                             else xp[rr / 4][q][j - 1] = __builtin_bit_cast(u32x2, t); } } }
;                 else { const float* xr = a.src + (size_t)row * DM;
; #pragma unroll
;                     for (int j = 0; j < 4; ++j) v[q][j] = *(const f32x4*)(xr + 4 * lane + 256 * j); } }
;             if (a.y2) {
;                 unsigned long long mask[R]; int ee[R][4]; float wgt[R][4]; f16x4 ld[R][4][4];
;                 int cnt[R];
; #pragma unroll
;                 for (int q = 0; q < R; ++q) { mask[q] = __ballot(sl[q] >= 0); cnt[q] = __builtin_popcountll(mask[q]);
; #pragma unroll
;                     for (int i = 0; i < 4; ++i) { if (mask[q]) { ee[q][i] = __builtin_ctzll(mask[q]); mask[q] &= mask[q] - 1; wgt[q][i] = 1.f; } else { ee[q][i] = i ? ee[q][0] : 0; wgt[q][i] = 0.f; } }
; #pragma unroll
;                     for (int i = 0; i < 4; ++i) {
;                         if (i < cnt[q]) { int slot = __shfl(sl[q], ee[q][i]); slot = slot < 0 ? 0 : slot; const f16* yr = a.y2 + ((size_t)ee[q][i] * EROWS + b * CAP + slot) * DM + 4 * lane;
; #pragma unroll
;                             for (int j = 0; j < 4; ++j) ld[q][i][j] = *(const f16x4*)(yr + 256 * j); } } }
; #pragma unroll
;                 for (int q = 0; q < R; ++q) { const int row = row0 + rr + q;
;                     f32x4 cs[4];
; #pragma unroll
;                     for (int j = 0; j < 4; ++j) cs[j] = (f32x4){0.f, 0.f, 0.f, 0.f};
; #pragma unroll
;                     for (int i = 0; i < 4; ++i) if (i < cnt[q]) {
; #pragma unroll
	v_cvt_f32_f16_e32 v134, v126
	v_cvt_f32_f16_sdwa v135, v126 dst_sel:DWORD dst_unused:UNUSED_PAD src0_sel:WORD_1
	v_cvt_f32_f16_e32 v138, v127
	v_cvt_f32_f16_sdwa v139, v127 dst_sel:DWORD dst_unused:UNUSED_PAD src0_sel:WORD_1
	s_waitcnt vmcnt(3)
	v_cvt_f32_f16_e32 v154, v128
	v_cvt_f32_f16_sdwa v155, v128 dst_sel:DWORD dst_unused:UNUSED_PAD src0_sel:WORD_1
	v_cvt_f32_f16_e32 v156, v129
	v_cvt_f32_f16_sdwa v157, v129 dst_sel:DWORD dst_unused:UNUSED_PAD src0_sel:WORD_1
	ds_write2_b64 v227, v[126:127], v[128:129] offset0:24 offset1:90
	global_load_dwordx2 v[128:129], v[132:133], off offset:1024 nt
	global_load_dwordx2 v[126:127], v[132:133], off offset:1536 nt
	v_lshl_add_u64 v[132:133], v[22:23], 0, s[28:29]
	global_load_dwordx2 v[186:187], v[132:133], off nt
	global_load_dwordx2 v[152:153], v[132:133], off offset:512 nt
	global_load_dwordx2 v[150:151], v[132:133], off offset:1024 nt
	s_waitcnt vmcnt(6)
	v_cvt_f32_f16_e32 v192, v188
	global_load_dwordx2 v[132:133], v[132:133], off offset:1536 nt
	v_cvt_f32_f16_sdwa v193, v188 dst_sel:DWORD dst_unused:UNUSED_PAD src0_sel:WORD_1
	v_cvt_f32_f16_e32 v194, v189
	v_cvt_f32_f16_sdwa v195, v189 dst_sel:DWORD dst_unused:UNUSED_PAD src0_sel:WORD_1
	global_load_dwordx2 v[190:191], v[204:205], off offset:1024 nt
	v_cvt_f32_f16_e32 v136, v124
	v_cvt_f32_f16_sdwa v137, v124 dst_sel:DWORD dst_unused:UNUSED_PAD src0_sel:WORD_1
	v_cvt_f32_f16_e32 v142, v125
	v_cvt_f32_f16_sdwa v143, v125 dst_sel:DWORD dst_unused:UNUSED_PAD src0_sel:WORD_1
	v_cvt_f32_f16_e32 v140, v122
	v_cvt_f32_f16_sdwa v141, v122 dst_sel:DWORD dst_unused:UNUSED_PAD src0_sel:WORD_1
	v_cvt_f32_f16_e32 v146, v123
	v_cvt_f32_f16_sdwa v147, v123 dst_sel:DWORD dst_unused:UNUSED_PAD src0_sel:WORD_1
	s_waitcnt vmcnt(7)
	v_cvt_f32_f16_e32 v144, v120
	v_cvt_f32_f16_sdwa v145, v120 dst_sel:DWORD dst_unused:UNUSED_PAD src0_sel:WORD_1
	v_cvt_f32_f16_e32 v148, v121
	v_cvt_f32_f16_sdwa v149, v121 dst_sel:DWORD dst_unused:UNUSED_PAD src0_sel:WORD_1
	v_pk_mul_f32 v[232:233], v[134:135], v[134:135]
	v_pk_mul_f32 v[234:235], v[138:139], v[138:139]
	v_pk_mul_f32 v[236:237], v[136:137], v[136:137]
	v_pk_mul_f32 v[238:239], v[142:143], v[142:143]
	v_add_f32_e32 v236, v236, v237
	v_add_f32_e32 v208, v238, v239
	v_add_f32_e32 v234, v234, v235
	v_add_f32_e32 v232, v232, v233
	v_pk_mul_f32 v[240:241], v[140:141], v[140:141]
	v_pk_mul_f32 v[242:243], v[146:147], v[146:147]
	v_add_f32_e32 v208, v236, v208
	v_add_f32_e32 v232, v232, v234
	v_add_f32_e32 v208, v232, v208
	v_add_f32_e32 v232, v242, v243
	v_add_f32_e32 v233, v240, v241
	v_pk_mul_f32 v[244:245], v[144:145], v[144:145]
	v_pk_mul_f32 v[246:247], v[148:149], v[148:149]
	v_add_f32_e32 v232, v233, v232
	v_add_f32_e32 v208, v208, v232
	v_add_f32_e32 v232, v246, v247
	v_add_f32_e32 v233, v244, v245
	v_add_f32_e32 v232, v233, v232
	v_add_f32_e32 v208, v208, v232
	v_mov_b32_e32 v232, 0
	v_cvt_f32_f16_e32 v158, v130
	v_add_f32_dpp v208, v208, v208 quad_perm:[1,0,3,2] row_mask:0xf bank_mask:0xf bound_ctrl:1
	v_cvt_f32_f16_sdwa v159, v130 dst_sel:DWORD dst_unused:UNUSED_PAD src0_sel:WORD_1
	v_cvt_f32_f16_e32 v162, v131
	v_add_f32_dpp v208, v208, v208 quad_perm:[2,3,0,1] row_mask:0xf bank_mask:0xf bound_ctrl:1
	v_cvt_f32_f16_sdwa v163, v131 dst_sel:DWORD dst_unused:UNUSED_PAD src0_sel:WORD_1
	v_pk_mul_f32 v[238:239], v[158:159], v[158:159]
	v_add_f32_dpp v208, v208, v208 row_half_mirror row_mask:0xf bank_mask:0xf bound_ctrl:1
	v_pk_mul_f32 v[234:235], v[154:155], v[154:155]
	v_pk_mul_f32 v[240:241], v[162:163], v[162:163]
	v_add_f32_dpp v208, v208, v208 row_mirror row_mask:0xf bank_mask:0xf bound_ctrl:1
	v_pk_mul_f32 v[236:237], v[156:157], v[156:157]
	v_add_f32_e32 v234, v234, v235
	v_mov_b32_dpp v232, v208 row_bcast:15 row_mask:0xa bank_mask:0xf
	v_add_f32_e32 v208, v208, v232
	v_mov_b32_e32 v232, 0
	s_waitcnt vmcnt(6)
	v_cvt_f32_f16_e32 v160, v128
	v_mov_b32_dpp v232, v208 row_bcast:31 row_mask:0xc bank_mask:0xf
	v_add_f32_e32 v208, v208, v232
	s_waitcnt vmcnt(4)
	ds_write2_b64 v227, v[186:187], v[188:189] offset0:156 offset1:222
	global_load_dwordx2 v[188:189], v[204:205], off offset:512 nt
	v_cvt_f32_f16_e32 v170, v186
	v_cvt_f32_f16_sdwa v171, v186 dst_sel:DWORD dst_unused:UNUSED_PAD src0_sel:WORD_1
	v_cvt_f32_f16_e32 v174, v187
	v_cvt_f32_f16_sdwa v175, v187 dst_sel:DWORD dst_unused:UNUSED_PAD src0_sel:WORD_1
	global_load_dwordx2 v[186:187], v[204:205], off offset:1536 nt
	v_readlane_b32 s0, v208, 63
	v_cvt_f32_f16_sdwa v161, v128 dst_sel:DWORD dst_unused:UNUSED_PAD src0_sel:WORD_1
	v_cvt_f32_f16_e32 v166, v129
	v_fma_f32 v208, s0, v214, v213
	v_rsq_f32_e32 v208, v208
	v_cvt_f32_f16_sdwa v167, v129 dst_sel:DWORD dst_unused:UNUSED_PAD src0_sel:WORD_1
	v_cvt_f32_f16_e32 v164, v126
	v_cvt_f32_f16_sdwa v165, v126 dst_sel:DWORD dst_unused:UNUSED_PAD src0_sel:WORD_1
	v_cvt_f32_f16_e32 v168, v127
	v_cvt_f32_f16_sdwa v169, v127 dst_sel:DWORD dst_unused:UNUSED_PAD src0_sel:WORD_1
	v_cndmask_b32_e64 v233, v210, v208, s[10:11]
	v_add_f32_e32 v210, v240, v241
	v_add_f32_e32 v232, v238, v239
	v_add_f32_e32 v210, v232, v210
	v_add_f32_e32 v232, v236, v237
	v_pk_mul_f32 v[242:243], v[160:161], v[160:161]
	v_pk_mul_f32 v[244:245], v[166:167], v[166:167]
	v_add_f32_e32 v232, v234, v232
	v_add_f32_e32 v210, v232, v210
	v_add_f32_e32 v232, v244, v245
	v_add_f32_e32 v234, v242, v243
	v_pk_mul_f32 v[246:247], v[164:165], v[164:165]
	v_pk_mul_f32 v[248:249], v[168:169], v[168:169]
	v_add_f32_e32 v232, v234, v232
	v_add_f32_e32 v210, v210, v232
	v_add_f32_e32 v232, v248, v249
	v_add_f32_e32 v234, v246, v247
	v_add_f32_e32 v232, v234, v232
	v_add_f32_e32 v210, v210, v232
	v_mov_b32_e32 v232, 0
	s_waitcnt vmcnt(5)
; __device__ __forceinline__ unsigned pkb(float lo, float hi) { f32x2 v = {lo, hi}; bf16x2_t b = __builtin_convertvector(v, bf16x2_t); return __builtin_bit_cast(unsigned, b); }
; template <int R, bool RT = false>
; __device__ __forceinline__ void norm_phase(const NormArgs& a, LAS unsigned char* lds, bool ctx_rows, const float* ctx_src, const float* ctx_shift, const float* ctx_scale) {
;     ...
;             for (int q = 0; q < R; ++q) { float ss = 0.f;
; #pragma unroll
;                 for (int j = 0; j < 4; ++j) ss += (v[q][j][0] * v[q][j][0] + v[q][j][1] * v[q][j][1]) + (v[q][j][2] * v[q][j][2] + v[q][j][3] * v[q][j][3]);
;                 rstd[q] = __builtin_amdgcn_rsqf(wave_sum(ss) * (1.f / DM) + EPS);
;                 if constexpr (RT) rsel[q] = ((lane >> 4) == rr / 4) ? rstd[q] : rsel[q]; }
; #pragma unroll
;             for (int q = 0; q < R; ++q) { const int row = row0 + rr + q;
; #pragma unroll
;                 for (int j = 0; j < 4; ++j) v[q][j] = (v[q][j] * rstd[q]) * A[j] + Sh[j];
;                 if (a.fout) {
; #pragma unroll
;                     for (int j = 0; j < 4; ++j) *(f32x4*)(a.fout + (size_t)row * DM + 4 * lane + 256 * j) = v[q][j];
;                 }
;                 if (a.hout) {
; #pragma unroll
;                     for (int j = 0; j < 4; ++j) { u32x2 w; if (a.hbf) { w.x = pkb(v[q][j][0], v[q][j][1]); w.y = pkb(v[q][j][2], v[q][j][3]); } else { w.x = pkh(v[q][j][0], v[q][j][1]); w.y = pkh(v[q][j][2], v[q][j][3]); } *(u32x2*)(a.hout + (size_t)row * DM + 4 * lane + 256 * j) = w; }
;                 }
	v_cvt_f32_f16_e32 v172, v152
	v_add_f32_dpp v210, v210, v210 quad_perm:[1,0,3,2] row_mask:0xf bank_mask:0xf bound_ctrl:1
	v_cvt_f32_f16_sdwa v173, v152 dst_sel:DWORD dst_unused:UNUSED_PAD src0_sel:WORD_1
	v_cvt_f32_f16_e32 v178, v153
	v_add_f32_dpp v210, v210, v210 quad_perm:[2,3,0,1] row_mask:0xf bank_mask:0xf bound_ctrl:1
	v_cvt_f32_f16_sdwa v179, v153 dst_sel:DWORD dst_unused:UNUSED_PAD src0_sel:WORD_1
	s_waitcnt vmcnt(4)
	v_cvt_f32_f16_e32 v176, v150
	v_add_f32_dpp v210, v210, v210 row_half_mirror row_mask:0xf bank_mask:0xf bound_ctrl:1
	v_cvt_f32_f16_sdwa v177, v150 dst_sel:DWORD dst_unused:UNUSED_PAD src0_sel:WORD_1
	v_cvt_f32_f16_e32 v182, v151
	v_add_f32_dpp v210, v210, v210 row_mirror row_mask:0xf bank_mask:0xf bound_ctrl:1
	v_cvt_f32_f16_sdwa v183, v151 dst_sel:DWORD dst_unused:UNUSED_PAD src0_sel:WORD_1
	s_waitcnt vmcnt(3)
	v_cvt_f32_f16_e32 v180, v132
	v_mov_b32_dpp v232, v210 row_bcast:15 row_mask:0xa bank_mask:0xf
	v_add_f32_e32 v210, v210, v232
	v_mov_b32_e32 v232, 0
	v_cvt_f32_f16_sdwa v181, v132 dst_sel:DWORD dst_unused:UNUSED_PAD src0_sel:WORD_1
	v_cvt_f32_f16_e32 v184, v133
	v_mov_b32_dpp v232, v210 row_bcast:31 row_mask:0xc bank_mask:0xf
	v_add_f32_e32 v210, v210, v232
	v_cvt_f32_f16_sdwa v185, v133 dst_sel:DWORD dst_unused:UNUSED_PAD src0_sel:WORD_1
	v_readlane_b32 s0, v210, 63
	v_pk_mul_f32 v[234:235], v[170:171], v[170:171]
	v_pk_mul_f32 v[236:237], v[174:175], v[174:175]
	v_fma_f32 v210, s0, v214, v213
	v_rsq_f32_e32 v210, v210
	v_pk_mul_f32 v[238:239], v[172:173], v[172:173]
	v_pk_mul_f32 v[240:241], v[178:179], v[178:179]
	v_add_f32_e32 v238, v238, v239
	v_cndmask_b32_e64 v232, v212, v210, s[10:11]
	v_add_f32_e32 v212, v240, v241
	v_add_f32_e32 v236, v236, v237
	v_add_f32_e32 v234, v234, v235
	v_pk_mul_f32 v[242:243], v[176:177], v[176:177]
	v_pk_mul_f32 v[244:245], v[182:183], v[182:183]
	v_add_f32_e32 v212, v238, v212
	v_add_f32_e32 v234, v234, v236
	v_add_f32_e32 v212, v234, v212
	v_add_f32_e32 v234, v244, v245
	v_add_f32_e32 v235, v242, v243
	v_pk_mul_f32 v[246:247], v[180:181], v[180:181]
	v_pk_mul_f32 v[248:249], v[184:185], v[184:185]
	v_add_f32_e32 v234, v235, v234
	v_add_f32_e32 v212, v212, v234
	v_add_f32_e32 v234, v248, v249
	v_add_f32_e32 v235, v246, v247
	v_add_f32_e32 v234, v235, v234
	v_add_f32_e32 v212, v212, v234
	v_mov_b32_e32 v234, 0
	s_waitcnt vmcnt(1)
	v_cvt_f32_f16_e32 v196, v188
	v_add_f32_dpp v212, v212, v212 quad_perm:[1,0,3,2] row_mask:0xf bank_mask:0xf bound_ctrl:1
	v_cvt_f32_f16_sdwa v197, v188 dst_sel:DWORD dst_unused:UNUSED_PAD src0_sel:WORD_1
	v_cvt_f32_f16_e32 v198, v189
	v_add_f32_dpp v212, v212, v212 quad_perm:[2,3,0,1] row_mask:0xf bank_mask:0xf bound_ctrl:1
	v_cvt_f32_f16_sdwa v199, v189 dst_sel:DWORD dst_unused:UNUSED_PAD src0_sel:WORD_1
	v_cvt_f32_f16_e32 v200, v190
	v_add_f32_dpp v212, v212, v212 row_half_mirror row_mask:0xf bank_mask:0xf bound_ctrl:1
	v_cvt_f32_f16_sdwa v201, v190 dst_sel:DWORD dst_unused:UNUSED_PAD src0_sel:WORD_1
	v_cvt_f32_f16_e32 v202, v191
	v_add_f32_dpp v212, v212, v212 row_mirror row_mask:0xf bank_mask:0xf bound_ctrl:1
	v_cvt_f32_f16_sdwa v203, v191 dst_sel:DWORD dst_unused:UNUSED_PAD src0_sel:WORD_1
	v_pk_mul_f32 v[236:237], v[194:195], v[194:195]
	v_mov_b32_dpp v234, v212 row_bcast:15 row_mask:0xa bank_mask:0xf
	v_add_f32_e32 v212, v212, v234
	v_mov_b32_e32 v234, 0
	s_waitcnt vmcnt(0)
	v_cvt_f32_f16_e32 v204, v186
	v_cvt_f32_f16_sdwa v205, v186 dst_sel:DWORD dst_unused:UNUSED_PAD src0_sel:WORD_1
	v_mov_b32_dpp v234, v212 row_bcast:31 row_mask:0xc bank_mask:0xf
	v_add_f32_e32 v212, v212, v234
	v_pk_mul_f32 v[234:235], v[192:193], v[192:193]
	v_cvt_f32_f16_e32 v206, v187
	v_cvt_f32_f16_sdwa v207, v187 dst_sel:DWORD dst_unused:UNUSED_PAD src0_sel:WORD_1
	v_pk_mul_f32 v[238:239], v[196:197], v[196:197]
	v_pk_mul_f32 v[240:241], v[198:199], v[198:199]
	v_add_f32_e32 v236, v236, v237
	v_add_f32_e32 v234, v234, v235
	v_add_f32_e32 v234, v234, v236
	v_add_f32_e32 v235, v240, v241
	v_add_f32_e32 v236, v238, v239
	v_pk_mul_f32 v[242:243], v[200:201], v[200:201]
	v_pk_mul_f32 v[244:245], v[202:203], v[202:203]
	v_add_f32_e32 v235, v236, v235
	v_add_f32_e32 v234, v234, v235
	v_add_f32_e32 v235, v244, v245
	v_add_f32_e32 v236, v242, v243
	v_pk_mul_f32 v[246:247], v[204:205], v[204:205]
	v_pk_mul_f32 v[248:249], v[206:207], v[206:207]
	v_add_f32_e32 v235, v236, v235
	v_pk_mul_f32 v[134:135], v[134:135], v[208:209] op_sel_hi:[1,0]
	v_pk_mul_f32 v[138:139], v[138:139], v[208:209] op_sel_hi:[1,0]
	v_add_f32_e32 v234, v234, v235
	v_add_f32_e32 v235, v248, v249
	v_add_f32_e32 v236, v246, v247
	v_pk_fma_f32 v[138:139], v[34:35], v[138:139], v[4:5]
	v_pk_fma_f32 v[134:135], v[36:37], v[134:135], v[2:3]
	v_pk_mul_f32 v[136:137], v[136:137], v[208:209] op_sel_hi:[1,0]
	v_pk_mul_f32 v[142:143], v[142:143], v[208:209] op_sel_hi:[1,0]
	v_add_f32_e32 v235, v236, v235
	v_pk_fma_f32 v[142:143], v[40:41], v[142:143], v[8:9]
	v_pk_fma_f32 v[136:137], v[42:43], v[136:137], v[6:7]
	v_pk_mul_f32 v[140:141], v[140:141], v[208:209] op_sel_hi:[1,0]
	v_pk_mul_f32 v[146:147], v[146:147], v[208:209] op_sel_hi:[1,0]
	v_cvt_pk_bf16_f32 v134, v134, v135
	v_cvt_pk_bf16_f32 v135, v138, v139
	v_lshl_add_u64 v[138:139], v[24:25], 0, s[24:25]
	v_add_f32_e32 v234, v234, v235
	v_pk_fma_f32 v[146:147], v[44:45], v[146:147], v[12:13]
	v_pk_fma_f32 v[140:141], v[46:47], v[140:141], v[10:11]
	v_pk_mul_f32 v[144:145], v[144:145], v[208:209] op_sel_hi:[1,0]
	v_pk_mul_f32 v[148:149], v[148:149], v[208:209] op_sel_hi:[1,0]
	global_store_dwordx2 v[138:139], v[134:135], off
	v_cvt_pk_bf16_f32 v134, v136, v137
	v_cvt_pk_bf16_f32 v135, v142, v143
	v_add_f32_dpp v234, v234, v234 quad_perm:[1,0,3,2] row_mask:0xf bank_mask:0xf bound_ctrl:1
; #define LAS __attribute__((address_space(3)))
; __device__ __forceinline__ unsigned pkb(float lo, float hi) { f32x2 v = {lo, hi}; bf16x2_t b = __builtin_convertvector(v, bf16x2_t); return __builtin_bit_cast(unsigned, b); }
; template <int R, bool RT = false>
; __device__ __forceinline__ void norm_phase(const NormArgs& a, LAS unsigned char* lds, bool ctx_rows, const float* ctx_src, const float* ctx_shift, const float* ctx_scale) {
;     ...
;             for (int q = 0; q < R; ++q) { const int row = row0 + rr + q;
; #pragma unroll
;                 for (int j = 0; j < 4; ++j) v[q][j] = (v[q][j] * rstd[q]) * A[j] + Sh[j];
;                 if (a.fout) {
; #pragma unroll
;                     for (int j = 0; j < 4; ++j) *(f32x4*)(a.fout + (size_t)row * DM + 4 * lane + 256 * j) = v[q][j];
;                 }
;                 if (a.hout) {
; #pragma unroll
;                     for (int j = 0; j < 4; ++j) { u32x2 w; if (a.hbf) { w.x = pkb(v[q][j][0], v[q][j][1]); w.y = pkb(v[q][j][2], v[q][j][3]); } else { w.x = pkh(v[q][j][0], v[q][j][1]); w.y = pkh(v[q][j][2], v[q][j][3]); } *(u32x2*)(a.hout + (size_t)row * DM + 4 * lane + 256 * j) = w; }
;                 }
;     ...
;             const int i16 = lane & 15, c4 = lane >> 4;
;             const LAS unsigned char* ap = hs + i16 * 528 + 16 * c4; const LAS unsigned char* bp = lds + i16 * 2048;
;             const int xa = (c4 ^ i16) << 4;
;             f32x4 acc0 = {0.f, 0.f, 0.f, 0.f}, acc1 = acc0, acc2 = acc0, acc3 = acc0;
; #pragma unroll
;             for (int j = 0; j < 4; ++j) {
; #pragma unroll
;                 for (int g = 0; g < 4; ++g)
; #pragma unroll
;                     for (int q = 0; q < 4; ++q) { const int row = 4 * g + q; if (j > 0) *(LAS u32x2*)(hs + row * 528 + 8 * lane) = xp[g][q][j > 0 ? j - 1 : 0]; }
; #pragma unroll
;                 for (int s8 = 0; s8 < 8; ++s8) {
;                     if ((s8 & 3) == 0) asm volatile("" ::: "memory");
;                     const f16x8 Af = *(const LAS f16x8*)(ap + 64 * s8);
;                     const f16x8 Bh = *(const LAS f16x8*)(bp + ((512 * j + 64 * s8) ^ xa)), Bl = *(const LAS f16x8*)(bp + 32768 + ((512 * j + 64 * s8) ^ xa));
	v_pk_fma_f32 v[148:149], v[52:53], v[148:149], v[16:17]
	v_pk_fma_f32 v[144:145], v[54:55], v[144:145], v[14:15]
	global_store_dwordx2 v[138:139], v[134:135], off offset:512
	v_cvt_pk_bf16_f32 v134, v140, v141
	v_cvt_pk_bf16_f32 v135, v146, v147
	v_add_f32_dpp v234, v234, v234 quad_perm:[2,3,0,1] row_mask:0xf bank_mask:0xf bound_ctrl:1
	global_store_dwordx2 v[138:139], v[134:135], off offset:1024
	v_cvt_pk_bf16_f32 v134, v144, v145
	v_cvt_pk_bf16_f32 v135, v148, v149
	v_readlane_b32 s0, v212, 63
	v_add_f32_dpp v234, v234, v234 row_half_mirror row_mask:0xf bank_mask:0xf bound_ctrl:1
	global_store_dwordx2 v[138:139], v[134:135], off offset:1536
	v_pk_mul_f32 v[134:135], v[154:155], v[210:211] op_sel_hi:[1,0]
	v_pk_mul_f32 v[136:137], v[156:157], v[210:211] op_sel_hi:[1,0]
	v_fma_f32 v212, s0, v214, v213
	v_add_f32_dpp v234, v234, v234 row_mirror row_mask:0xf bank_mask:0xf bound_ctrl:1
	v_mov_b32_e32 v235, 0
	v_pk_fma_f32 v[136:137], v[34:35], v[136:137], v[4:5]
	v_pk_fma_f32 v[134:135], v[36:37], v[134:135], v[2:3]
	v_pk_mul_f32 v[138:139], v[158:159], v[210:211] op_sel_hi:[1,0]
	v_pk_mul_f32 v[140:141], v[162:163], v[210:211] op_sel_hi:[1,0]
	v_rsq_f32_e32 v212, v212
	v_mov_b32_dpp v235, v234 row_bcast:15 row_mask:0xa bank_mask:0xf
	v_pk_fma_f32 v[140:141], v[40:41], v[140:141], v[8:9]
	v_pk_fma_f32 v[138:139], v[42:43], v[138:139], v[6:7]
	v_pk_mul_f32 v[142:143], v[160:161], v[210:211] op_sel_hi:[1,0]
	v_pk_mul_f32 v[144:145], v[166:167], v[210:211] op_sel_hi:[1,0]
	v_cvt_pk_bf16_f32 v134, v134, v135
	v_cvt_pk_bf16_f32 v135, v136, v137
	v_lshl_add_u64 v[136:137], v[24:25], 0, s[26:27]
	v_add_f32_e32 v234, v234, v235
	v_mov_b32_e32 v235, 0
	v_pk_fma_f32 v[144:145], v[44:45], v[144:145], v[12:13]
	v_pk_fma_f32 v[142:143], v[46:47], v[142:143], v[10:11]
	v_pk_mul_f32 v[146:147], v[164:165], v[210:211] op_sel_hi:[1,0]
	v_pk_mul_f32 v[148:149], v[168:169], v[210:211] op_sel_hi:[1,0]
	global_store_dwordx2 v[136:137], v[134:135], off
	v_cvt_pk_bf16_f32 v134, v138, v139
	v_cvt_pk_bf16_f32 v135, v140, v141
	v_mov_b32_dpp v235, v234 row_bcast:31 row_mask:0xc bank_mask:0xf
	v_pk_fma_f32 v[148:149], v[52:53], v[148:149], v[16:17]
	v_pk_fma_f32 v[146:147], v[54:55], v[146:147], v[14:15]
	global_store_dwordx2 v[136:137], v[134:135], off offset:512
	v_cvt_pk_bf16_f32 v134, v142, v143
	v_cvt_pk_bf16_f32 v135, v144, v145
	v_add_f32_e32 v234, v234, v235
	global_store_dwordx2 v[136:137], v[134:135], off offset:1024
	v_cvt_pk_bf16_f32 v134, v146, v147
	v_cvt_pk_bf16_f32 v135, v148, v149
	v_readlane_b32 s0, v234, 63
	global_store_dwordx2 v[136:137], v[134:135], off offset:1536
	v_pk_mul_f32 v[134:135], v[170:171], v[212:213] op_sel_hi:[1,0]
	v_pk_mul_f32 v[136:137], v[174:175], v[212:213] op_sel_hi:[1,0]
	v_fma_f32 v234, s0, v214, v213
	v_pk_fma_f32 v[136:137], v[34:35], v[136:137], v[4:5]
	v_pk_fma_f32 v[134:135], v[36:37], v[134:135], v[2:3]
	v_pk_mul_f32 v[138:139], v[172:173], v[212:213] op_sel_hi:[1,0]
	v_pk_mul_f32 v[140:141], v[178:179], v[212:213] op_sel_hi:[1,0]
	v_rsq_f32_e32 v234, v234
	v_pk_fma_f32 v[140:141], v[40:41], v[140:141], v[8:9]
	v_pk_fma_f32 v[138:139], v[42:43], v[138:139], v[6:7]
	v_pk_mul_f32 v[142:143], v[176:177], v[212:213] op_sel_hi:[1,0]
	v_pk_mul_f32 v[144:145], v[182:183], v[212:213] op_sel_hi:[1,0]
	v_cvt_pk_bf16_f32 v134, v134, v135
	v_cvt_pk_bf16_f32 v135, v136, v137
	v_lshl_add_u64 v[136:137], v[24:25], 0, s[28:29]
	v_pk_fma_f32 v[144:145], v[44:45], v[144:145], v[12:13]
	v_pk_fma_f32 v[142:143], v[46:47], v[142:143], v[10:11]
	v_pk_mul_f32 v[146:147], v[180:181], v[212:213] op_sel_hi:[1,0]
	v_pk_mul_f32 v[148:149], v[184:185], v[212:213] op_sel_hi:[1,0]
	global_store_dwordx2 v[136:137], v[134:135], off
	v_cvt_pk_bf16_f32 v134, v138, v139
	v_cvt_pk_bf16_f32 v135, v140, v141
	v_pk_fma_f32 v[148:149], v[52:53], v[148:149], v[16:17]
	v_pk_fma_f32 v[146:147], v[54:55], v[146:147], v[14:15]
	global_store_dwordx2 v[136:137], v[134:135], off offset:512
	v_cvt_pk_bf16_f32 v134, v142, v143
	v_cvt_pk_bf16_f32 v135, v144, v145
	global_store_dwordx2 v[136:137], v[134:135], off offset:1024
	v_cvt_pk_bf16_f32 v134, v146, v147
	v_cvt_pk_bf16_f32 v135, v148, v149
	global_store_dwordx2 v[136:137], v[134:135], off offset:1536
	v_pk_mul_f32 v[134:135], v[192:193], v[234:235] op_sel_hi:[1,0]
	v_pk_mul_f32 v[136:137], v[194:195], v[234:235] op_sel_hi:[1,0]
	v_pk_fma_f32 v[2:3], v[36:37], v[134:135], v[2:3]
	v_pk_fma_f32 v[4:5], v[34:35], v[136:137], v[4:5]
	v_pk_mul_f32 v[34:35], v[196:197], v[234:235] op_sel_hi:[1,0]
	v_pk_mul_f32 v[36:37], v[198:199], v[234:235] op_sel_hi:[1,0]
	v_pk_fma_f32 v[6:7], v[42:43], v[34:35], v[6:7]
	v_pk_fma_f32 v[8:9], v[40:41], v[36:37], v[8:9]
	v_pk_mul_f32 v[34:35], v[200:201], v[234:235] op_sel_hi:[1,0]
	v_pk_mul_f32 v[36:37], v[202:203], v[234:235] op_sel_hi:[1,0]
	v_cvt_pk_bf16_f32 v2, v2, v3
	v_cvt_pk_bf16_f32 v3, v4, v5
	v_lshl_add_u64 v[4:5], v[24:25], 0, s[30:31]
	v_pk_fma_f32 v[12:13], v[44:45], v[36:37], v[12:13]
	v_pk_fma_f32 v[10:11], v[46:47], v[34:35], v[10:11]
	v_pk_mul_f32 v[34:35], v[204:205], v[234:235] op_sel_hi:[1,0]
	v_pk_mul_f32 v[36:37], v[206:207], v[234:235] op_sel_hi:[1,0]
	global_store_dwordx2 v[4:5], v[2:3], off
	v_cvt_pk_bf16_f32 v2, v6, v7
	v_cvt_pk_bf16_f32 v3, v8, v9
	v_pk_fma_f32 v[16:17], v[52:53], v[36:37], v[16:17]
	v_pk_fma_f32 v[14:15], v[54:55], v[34:35], v[14:15]
	global_store_dwordx2 v[4:5], v[2:3], off offset:512
	v_cvt_pk_bf16_f32 v2, v10, v11
	v_cvt_pk_bf16_f32 v3, v12, v13
	global_store_dwordx2 v[4:5], v[2:3], off offset:1024
	v_cvt_pk_bf16_f32 v2, v14, v15
	v_cvt_pk_bf16_f32 v3, v16, v17
	global_store_dwordx2 v[4:5], v[2:3], off offset:1536
	ds_read_b128 v[2:5], v215 offset:32768
	ds_read_b128 v[6:9], v215
	ds_read_b128 v[10:13], v216
	s_waitcnt lgkmcnt(0)
; #define LAS __attribute__((address_space(3)))
; template <int R, bool RT = false>
; __device__ __forceinline__ void norm_phase(const NormArgs& a, LAS unsigned char* lds, bool ctx_rows, const float* ctx_src, const float* ctx_shift, const float* ctx_scale) {
;     ...
;             for (int j = 0; j < 4; ++j) {
; #pragma unroll
;                 for (int g = 0; g < 4; ++g)
; #pragma unroll
;                     for (int q = 0; q < 4; ++q) { const int row = 4 * g + q; if (j > 0) *(LAS u32x2*)(hs + row * 528 + 8 * lane) = xp[g][q][j > 0 ? j - 1 : 0]; }
; #pragma unroll
;                 for (int s8 = 0; s8 < 8; ++s8) {
;                     if ((s8 & 3) == 0) asm volatile("" ::: "memory");
;                     const f16x8 Af = *(const LAS f16x8*)(ap + 64 * s8);
;                     const f16x8 Bh = *(const LAS f16x8*)(bp + ((512 * j + 64 * s8) ^ xa)), Bl = *(const LAS f16x8*)(bp + 32768 + ((512 * j + 64 * s8) ^ xa));
;                     if (s8 & 1) { acc1 = __builtin_amdgcn_mfma_f32_16x16x32_f16(Af, Bh, acc1, 0, 0, 0); acc3 = __builtin_amdgcn_mfma_f32_16x16x32_f16(Af, Bl, acc3, 0, 0, 0); }
;                     else        { acc0 = __builtin_amdgcn_mfma_f32_16x16x32_f16(Af, Bh, acc0, 0, 0, 0); acc2 = __builtin_amdgcn_mfma_f32_16x16x32_f16(Af, Bl, acc2, 0, 0, 0); } }
	v_mfma_f32_16x16x32_f16 v[6:9], v[10:13], v[6:9], 0
	v_cndmask_b32_e64 v230, v230, v212, s[10:11]
	v_cndmask_b32_e64 v231, v231, v234, s[10:11]
	s_and_b32 s0, s14, 0x7f0
	v_mfma_f32_16x16x32_f16 v[2:5], v[10:13], v[2:5], 0
	ds_read_b128 v[10:13], v216 offset:64
	ds_read_b128 v[14:17], v217 offset:32768
	ds_read_b128 v[34:37], v217
	s_lshl_b32 s0, s0, 2
	s_add_i32 s14, s14, 0x8000
	s_waitcnt lgkmcnt(0)
	v_mfma_f32_16x16x32_f16 v[34:37], v[10:13], v[34:37], 0
	v_mfma_f32_16x16x32_f16 v[10:13], v[10:13], v[14:17], 0
	ds_read_b128 v[14:17], v216 offset:128
	ds_read_b128 v[40:43], v218 offset:32768
	ds_read_b128 v[44:47], v218
	s_waitcnt lgkmcnt(0)
	v_mfma_f32_16x16x32_f16 v[6:9], v[14:17], v[44:47], v[6:9]
	v_mfma_f32_16x16x32_f16 v[2:5], v[14:17], v[40:43], v[2:5]
	ds_read_b128 v[14:17], v216 offset:192
	ds_read_b128 v[40:43], v219 offset:32768
	ds_read_b128 v[44:47], v219
	s_waitcnt lgkmcnt(0)
	v_mfma_f32_16x16x32_f16 v[34:37], v[14:17], v[44:47], v[34:37]
	v_mfma_f32_16x16x32_f16 v[10:13], v[14:17], v[40:43], v[10:13]
	ds_read_b128 v[14:17], v215 offset:33024
	ds_read_b128 v[40:43], v215 offset:256
	ds_read_b128 v[44:47], v216 offset:256
	s_waitcnt lgkmcnt(0)
	v_mfma_f32_16x16x32_f16 v[6:9], v[44:47], v[40:43], v[6:9]
	v_mfma_f32_16x16x32_f16 v[2:5], v[44:47], v[14:17], v[2:5]
	ds_read_b128 v[14:17], v216 offset:320
	ds_read_b128 v[40:43], v217 offset:33024
	ds_read_b128 v[44:47], v217 offset:256
	s_waitcnt lgkmcnt(0)
	v_mfma_f32_16x16x32_f16 v[34:37], v[14:17], v[44:47], v[34:37]
	v_mfma_f32_16x16x32_f16 v[10:13], v[14:17], v[40:43], v[10:13]
	ds_read_b128 v[14:17], v216 offset:384
	ds_read_b128 v[40:43], v218 offset:33024
	ds_read_b128 v[44:47], v218 offset:256
	s_waitcnt lgkmcnt(0)
	v_mfma_f32_16x16x32_f16 v[6:9], v[14:17], v[44:47], v[6:9]
	v_mfma_f32_16x16x32_f16 v[2:5], v[14:17], v[40:43], v[2:5]
	ds_read_b128 v[14:17], v216 offset:448
	ds_read_b128 v[40:43], v219 offset:33024
	ds_read_b128 v[44:47], v219 offset:256
	ds_write2_b64 v211, v[48:49], v[58:59] offset1:66
	ds_write2_b64 v211, v[64:65], v[70:71] offset0:132 offset1:198
	ds_write2_b64 v225, v[76:77], v[82:83] offset0:8 offset1:74
	ds_write2_b64 v225, v[88:89], v[94:95] offset0:140 offset1:206
	ds_write2_b64 v226, v[100:101], v[106:107] offset0:16 offset1:82
	ds_write2_b64 v226, v[112:113], v[118:119] offset0:148 offset1:214
	ds_write2_b64 v227, v[124:125], v[130:131] offset0:24 offset1:90
	ds_write2_b64 v227, v[152:153], v[188:189] offset0:156 offset1:222
	s_waitcnt lgkmcnt(8)
	v_mfma_f32_16x16x32_f16 v[34:37], v[14:17], v[44:47], v[34:37]
	v_mfma_f32_16x16x32_f16 v[10:13], v[14:17], v[40:43], v[10:13]
	ds_read_b128 v[14:17], v215 offset:33280
	ds_read_b128 v[40:43], v215 offset:512
	ds_read_b128 v[44:47], v216
	s_waitcnt lgkmcnt(0)
	v_mfma_f32_16x16x32_f16 v[6:9], v[44:47], v[40:43], v[6:9]
	v_mfma_f32_16x16x32_f16 v[2:5], v[44:47], v[14:17], v[2:5]
	ds_read_b128 v[14:17], v216 offset:64
	ds_read_b128 v[40:43], v217 offset:33280
	ds_read_b128 v[44:47], v217 offset:512
	s_waitcnt lgkmcnt(0)
	v_mfma_f32_16x16x32_f16 v[34:37], v[14:17], v[44:47], v[34:37]
	v_mfma_f32_16x16x32_f16 v[10:13], v[14:17], v[40:43], v[10:13]
	ds_read_b128 v[14:17], v216 offset:128
	ds_read_b128 v[40:43], v218 offset:33280
	ds_read_b128 v[44:47], v218 offset:512
	s_waitcnt lgkmcnt(0)
	v_mfma_f32_16x16x32_f16 v[6:9], v[14:17], v[44:47], v[6:9]
	v_mfma_f32_16x16x32_f16 v[2:5], v[14:17], v[40:43], v[2:5]
	ds_read_b128 v[14:17], v216 offset:192
	ds_read_b128 v[40:43], v219 offset:33280
	ds_read_b128 v[44:47], v219 offset:512
	s_waitcnt lgkmcnt(0)
	v_mfma_f32_16x16x32_f16 v[34:37], v[14:17], v[44:47], v[34:37]
	v_mfma_f32_16x16x32_f16 v[10:13], v[14:17], v[40:43], v[10:13]
	ds_read_b128 v[14:17], v215 offset:33536
	ds_read_b128 v[40:43], v215 offset:768
	ds_read_b128 v[44:47], v216 offset:256
	s_waitcnt lgkmcnt(0)
	v_mfma_f32_16x16x32_f16 v[6:9], v[44:47], v[40:43], v[6:9]
	v_mfma_f32_16x16x32_f16 v[2:5], v[44:47], v[14:17], v[2:5]
	ds_read_b128 v[14:17], v216 offset:320
	ds_read_b128 v[40:43], v217 offset:33536
	ds_read_b128 v[44:47], v217 offset:768
	s_waitcnt lgkmcnt(0)
	v_mfma_f32_16x16x32_f16 v[34:37], v[14:17], v[44:47], v[34:37]
	v_mfma_f32_16x16x32_f16 v[10:13], v[14:17], v[40:43], v[10:13]
	ds_read_b128 v[14:17], v216 offset:384
	ds_read_b128 v[40:43], v218 offset:33536
	ds_read_b128 v[44:47], v218 offset:768
	s_waitcnt lgkmcnt(0)
	v_mfma_f32_16x16x32_f16 v[6:9], v[14:17], v[44:47], v[6:9]
	v_mfma_f32_16x16x32_f16 v[2:5], v[14:17], v[40:43], v[2:5]
	ds_read_b128 v[14:17], v216 offset:448
	ds_read_b128 v[40:43], v219 offset:33536
	ds_read_b128 v[44:47], v219 offset:768
	ds_write2_b64 v211, v[38:39], v[56:57] offset1:66
	ds_write2_b64 v211, v[62:63], v[68:69] offset0:132 offset1:198
	ds_write2_b64 v225, v[74:75], v[80:81] offset0:8 offset1:74
	ds_write2_b64 v225, v[86:87], v[92:93] offset0:140 offset1:206
	ds_write2_b64 v226, v[98:99], v[104:105] offset0:16 offset1:82
	ds_write2_b64 v226, v[110:111], v[116:117] offset0:148 offset1:214
	ds_write2_b64 v227, v[122:123], v[128:129] offset0:24 offset1:90
	ds_write2_b64 v227, v[150:151], v[190:191] offset0:156 offset1:222
	s_waitcnt lgkmcnt(8)
	v_mfma_f32_16x16x32_f16 v[34:37], v[14:17], v[44:47], v[34:37]
	v_mfma_f32_16x16x32_f16 v[10:13], v[14:17], v[40:43], v[10:13]
	ds_read_b128 v[14:17], v215 offset:33792
	ds_read_b128 v[38:41], v215 offset:1024
	ds_read_b128 v[42:45], v216
	s_waitcnt lgkmcnt(0)
	v_mfma_f32_16x16x32_f16 v[6:9], v[42:45], v[38:41], v[6:9]
	v_mfma_f32_16x16x32_f16 v[2:5], v[42:45], v[14:17], v[2:5]
	ds_read_b128 v[14:17], v216 offset:64
	ds_read_b128 v[38:41], v217 offset:33792
	ds_read_b128 v[42:45], v217 offset:1024
	s_waitcnt lgkmcnt(0)
; #define LAS __attribute__((address_space(3)))
; template <int R, bool RT = false>
; __device__ __forceinline__ void norm_phase(const NormArgs& a, LAS unsigned char* lds, bool ctx_rows, const float* ctx_src, const float* ctx_shift, const float* ctx_scale) {
;     ...
;             for (int j = 0; j < 4; ++j) {
; #pragma unroll
;                 for (int g = 0; g < 4; ++g)
; #pragma unroll
;                     for (int q = 0; q < 4; ++q) { const int row = 4 * g + q; if (j > 0) *(LAS u32x2*)(hs + row * 528 + 8 * lane) = xp[g][q][j > 0 ? j - 1 : 0]; }
; #pragma unroll
;                 for (int s8 = 0; s8 < 8; ++s8) {
;                     if ((s8 & 3) == 0) asm volatile("" ::: "memory");
;                     const f16x8 Af = *(const LAS f16x8*)(ap + 64 * s8);
;                     const f16x8 Bh = *(const LAS f16x8*)(bp + ((512 * j + 64 * s8) ^ xa)), Bl = *(const LAS f16x8*)(bp + 32768 + ((512 * j + 64 * s8) ^ xa));
;                     if (s8 & 1) { acc1 = __builtin_amdgcn_mfma_f32_16x16x32_f16(Af, Bh, acc1, 0, 0, 0); acc3 = __builtin_amdgcn_mfma_f32_16x16x32_f16(Af, Bl, acc3, 0, 0, 0); }
;                     else        { acc0 = __builtin_amdgcn_mfma_f32_16x16x32_f16(Af, Bh, acc0, 0, 0, 0); acc2 = __builtin_amdgcn_mfma_f32_16x16x32_f16(Af, Bl, acc2, 0, 0, 0); } }
;             }
;             const f32x4 d4 = (acc0 + acc1) + (acc2 + acc3);
;             f32x4 o4;
; #pragma unroll
;             for (int r = 0; r < 4; ++r) { const float lgt = rsel[r] * d4[r] + ce; float mx = lgt;
; #pragma unroll
;                 for (int o = 1; o < 16; o <<= 1) mx = fmaxf(mx, __shfl_xor(mx, o));
;                 const float ex = expf(lgt - mx); float sm = ex;
; #pragma unroll
;                 for (int o = 1; o < 16; o <<= 1) sm += __shfl_xor(sm, o);
	v_mfma_f32_16x16x32_f16 v[34:37], v[14:17], v[42:45], v[34:37]
	v_mfma_f32_16x16x32_f16 v[10:13], v[14:17], v[38:41], v[10:13]
	ds_read_b128 v[14:17], v216 offset:128
	ds_read_b128 v[38:41], v218 offset:33792
	ds_read_b128 v[42:45], v218 offset:1024
	s_waitcnt lgkmcnt(0)
	v_mfma_f32_16x16x32_f16 v[6:9], v[14:17], v[42:45], v[6:9]
	v_mfma_f32_16x16x32_f16 v[2:5], v[14:17], v[38:41], v[2:5]
	ds_read_b128 v[14:17], v216 offset:192
	ds_read_b128 v[38:41], v219 offset:33792
	ds_read_b128 v[42:45], v219 offset:1024
	s_waitcnt lgkmcnt(0)
	v_mfma_f32_16x16x32_f16 v[34:37], v[14:17], v[42:45], v[34:37]
	v_mfma_f32_16x16x32_f16 v[10:13], v[14:17], v[38:41], v[10:13]
	ds_read_b128 v[14:17], v215 offset:34048
	ds_read_b128 v[38:41], v215 offset:1280
	ds_read_b128 v[42:45], v216 offset:256
	s_waitcnt lgkmcnt(0)
	v_mfma_f32_16x16x32_f16 v[6:9], v[42:45], v[38:41], v[6:9]
	v_mfma_f32_16x16x32_f16 v[2:5], v[42:45], v[14:17], v[2:5]
	ds_read_b128 v[14:17], v216 offset:320
	ds_read_b128 v[38:41], v217 offset:34048
	ds_read_b128 v[42:45], v217 offset:1280
	s_waitcnt lgkmcnt(0)
	v_mfma_f32_16x16x32_f16 v[34:37], v[14:17], v[42:45], v[34:37]
	v_mfma_f32_16x16x32_f16 v[10:13], v[14:17], v[38:41], v[10:13]
	ds_read_b128 v[14:17], v216 offset:384
	ds_read_b128 v[38:41], v218 offset:34048
	ds_read_b128 v[42:45], v218 offset:1280
	s_waitcnt lgkmcnt(0)
	v_mfma_f32_16x16x32_f16 v[6:9], v[14:17], v[42:45], v[6:9]
	v_mfma_f32_16x16x32_f16 v[2:5], v[14:17], v[38:41], v[2:5]
	ds_read_b128 v[14:17], v216 offset:448
	ds_read_b128 v[38:41], v219 offset:34048
	ds_read_b128 v[42:45], v219 offset:1280
	ds_write2_b64 v211, v[32:33], v[50:51] offset1:66
	ds_write2_b64 v211, v[60:61], v[66:67] offset0:132 offset1:198
	ds_write2_b64 v225, v[72:73], v[78:79] offset0:8 offset1:74
	ds_write2_b64 v225, v[84:85], v[90:91] offset0:140 offset1:206
	ds_write2_b64 v226, v[96:97], v[102:103] offset0:16 offset1:82
	ds_write2_b64 v226, v[108:109], v[114:115] offset0:148 offset1:214
	ds_write2_b64 v227, v[120:121], v[126:127] offset0:24 offset1:90
	ds_write2_b64 v227, v[132:133], v[186:187] offset0:156 offset1:222
	s_waitcnt lgkmcnt(8)
	v_mfma_f32_16x16x32_f16 v[34:37], v[14:17], v[42:45], v[34:37]
	v_mfma_f32_16x16x32_f16 v[10:13], v[14:17], v[38:41], v[10:13]
	ds_read_b128 v[14:17], v215 offset:34304
	ds_read_b128 v[38:41], v215 offset:1536
	ds_read_b128 v[42:45], v216
	s_waitcnt lgkmcnt(0)
	v_mfma_f32_16x16x32_f16 v[6:9], v[42:45], v[38:41], v[6:9]
	v_mfma_f32_16x16x32_f16 v[2:5], v[42:45], v[14:17], v[2:5]
	ds_read_b128 v[14:17], v216 offset:64
	ds_read_b128 v[38:41], v217 offset:34304
	ds_read_b128 v[42:45], v217 offset:1536
	s_waitcnt lgkmcnt(0)
	v_mfma_f32_16x16x32_f16 v[32:35], v[14:17], v[42:45], v[34:37]
	v_mfma_f32_16x16x32_f16 v[10:13], v[14:17], v[38:41], v[10:13]
	ds_read_b128 v[14:17], v216 offset:128
	s_nop 0
	ds_read_b128 v[36:39], v218 offset:34304
	ds_read_b128 v[40:43], v218 offset:1536
	s_waitcnt lgkmcnt(0)
	v_mfma_f32_16x16x32_f16 v[6:9], v[14:17], v[40:43], v[6:9]
	v_mfma_f32_16x16x32_f16 v[2:5], v[14:17], v[36:39], v[2:5]
	ds_read_b128 v[14:17], v216 offset:192
	ds_read_b128 v[36:39], v219 offset:34304
	ds_read_b128 v[40:43], v219 offset:1536
	s_waitcnt lgkmcnt(0)
	v_mfma_f32_16x16x32_f16 v[32:35], v[14:17], v[40:43], v[32:35]
	v_mfma_f32_16x16x32_f16 v[10:13], v[14:17], v[36:39], v[10:13]
	ds_read_b128 v[14:17], v215 offset:34560
	ds_read_b128 v[36:39], v215 offset:1792
	ds_read_b128 v[40:43], v216 offset:256
	s_waitcnt lgkmcnt(0)
	v_mfma_f32_16x16x32_f16 v[6:9], v[40:43], v[36:39], v[6:9]
	v_mfma_f32_16x16x32_f16 v[2:5], v[40:43], v[14:17], v[2:5]
	ds_read_b128 v[14:17], v216 offset:320
	ds_read_b128 v[36:39], v217 offset:34560
	ds_read_b128 v[40:43], v217 offset:1792
	s_waitcnt lgkmcnt(0)
	v_mfma_f32_16x16x32_f16 v[32:35], v[14:17], v[40:43], v[32:35]
	v_mfma_f32_16x16x32_f16 v[10:13], v[14:17], v[36:39], v[10:13]
	ds_read_b128 v[14:17], v216 offset:384
	ds_read_b128 v[36:39], v218 offset:34560
	ds_read_b128 v[40:43], v218 offset:1792
	s_waitcnt lgkmcnt(0)
	v_mfma_f32_16x16x32_f16 v[6:9], v[14:17], v[40:43], v[6:9]
	v_mfma_f32_16x16x32_f16 v[2:5], v[14:17], v[36:39], v[2:5]
	ds_read_b128 v[14:17], v216 offset:448
	ds_read_b128 v[36:39], v219 offset:34560
	ds_read_b128 v[40:43], v219 offset:1792
	s_waitcnt lgkmcnt(0)
	v_mfma_f32_16x16x32_f16 v[32:35], v[14:17], v[40:43], v[32:35]
	v_mfma_f32_16x16x32_f16 v[10:13], v[14:17], v[36:39], v[10:13]
	s_nop 6
	v_add_f32_e64 v8, v8, v34
	v_add_f32_e64 v9, v9, v35
	v_pk_add_f32 v[6:7], v[6:7], v[32:33]
	v_pk_add_f32 v[4:5], v[4:5], v[12:13]
	v_pk_add_f32 v[10:11], v[2:3], v[10:11]
	v_pk_add_f32 v[2:3], v[8:9], v[4:5]
	v_pk_add_f32 v[4:5], v[6:7], v[10:11]
	v_cndmask_b32_e32 v6, v220, v222, vcc
	v_fma_f32 v4, v233, v4, v1
	v_lshlrev_b32_e32 v12, 2, v6
	ds_bpermute_b32 v6, v12, v4
	v_cmp_lt_i32_e32 vcc, v223, v221
	v_fma_f32 v2, v230, v2, v1
	ds_bpermute_b32 v10, v12, v2
	v_cndmask_b32_e32 v7, v220, v223, vcc
	s_waitcnt lgkmcnt(1)
	v_max_f32_e32 v6, v6, v6
	v_max_f32_e32 v6, v4, v6
	v_lshlrev_b32_e32 v13, 2, v7
	ds_bpermute_b32 v7, v13, v6
	s_waitcnt lgkmcnt(1)
	v_max_f32_e32 v10, v10, v10
	v_cmp_lt_i32_e32 vcc, v224, v221
	v_max_f32_e32 v10, v2, v10
	ds_bpermute_b32 v11, v13, v10
	s_waitcnt lgkmcnt(1)
	v_max_f32_e32 v7, v7, v7
	v_max_f32_e32 v6, v6, v7
	v_cndmask_b32_e32 v7, v220, v224, vcc
	v_lshlrev_b32_e32 v14, 2, v7
	ds_bpermute_b32 v7, v14, v6
	s_waitcnt lgkmcnt(1)
	v_max_f32_e32 v11, v11, v11
	v_max_f32_e32 v10, v10, v11
	v_cmp_lt_i32_e32 vcc, v228, v221
	ds_bpermute_b32 v11, v14, v10
	s_waitcnt lgkmcnt(1)
; template <int R, bool RT = false>
; __device__ __forceinline__ void norm_phase(const NormArgs& a, LAS unsigned char* lds, bool ctx_rows, const float* ctx_src, const float* ctx_shift, const float* ctx_scale) {
;     ...
;             for (int r = 0; r < 4; ++r) { const float lgt = rsel[r] * d4[r] + ce; float mx = lgt;
; #pragma unroll
;                 for (int o = 1; o < 16; o <<= 1) mx = fmaxf(mx, __shfl_xor(mx, o));
;                 const float ex = expf(lgt - mx); float sm = ex;
; #pragma unroll
;                 for (int o = 1; o < 16; o <<= 1) sm += __shfl_xor(sm, o);
;                 o4[r] = ex / sm; }
;             *(f32x4*)(a.aff + ((size_t)b * NE + i16) * SEQ + (row0 & (SEQ - 1)) + 4 * c4) = o4;
	v_max_f32_e32 v7, v7, v7
	v_max_f32_e32 v6, v6, v7
	v_cndmask_b32_e32 v7, v220, v228, vcc
	v_lshlrev_b32_e32 v15, 2, v7
	ds_bpermute_b32 v7, v15, v6
	s_waitcnt lgkmcnt(1)
	v_max_f32_e32 v11, v11, v11
	v_max_f32_e32 v10, v10, v11
	ds_bpermute_b32 v11, v15, v10
	v_fma_f32 v5, v232, v5, v1
	s_waitcnt lgkmcnt(1)
	v_max_f32_e32 v7, v7, v7
	v_max_f32_e32 v6, v6, v7
	v_sub_f32_e32 v4, v4, v6
	v_mul_f32_e32 v6, 0x3fb8aa3b, v4
	v_fma_f32 v7, v4, s35, -v6
	v_rndne_f32_e32 v8, v6
	s_waitcnt lgkmcnt(0)
	v_max_f32_e32 v11, v11, v11
	v_fmac_f32_e32 v7, 0x32a5705f, v4
	v_sub_f32_e32 v6, v6, v8
	v_max_f32_e32 v10, v10, v11
	v_add_f32_e32 v6, v6, v7
	v_sub_f32_e32 v2, v2, v10
	v_exp_f32_e32 v6, v6
	v_cvt_i32_f32_e32 v7, v8
	v_mul_f32_e32 v10, 0x3fb8aa3b, v2
	v_fma_f32 v11, v2, s35, -v10
	v_rndne_f32_e32 v16, v10
	v_fmac_f32_e32 v11, 0x32a5705f, v2
	v_sub_f32_e32 v10, v10, v16
	v_add_f32_e32 v10, v10, v11
	v_ldexp_f32 v6, v6, v7
	ds_bpermute_b32 v7, v12, v5
	v_exp_f32_e32 v10, v10
	v_cvt_i32_f32_e32 v11, v16
	v_fma_f32 v3, v231, v3, v1
	v_cmp_ngt_f32_e32 vcc, s36, v4
	s_waitcnt lgkmcnt(0)
	v_max_f32_e32 v7, v7, v7
	v_ldexp_f32 v10, v10, v11
	ds_bpermute_b32 v11, v12, v3
	v_max_f32_e32 v7, v5, v7
	ds_bpermute_b32 v8, v13, v7
	v_cndmask_b32_e32 v6, 0, v6, vcc
	v_cmp_nlt_f32_e32 vcc, s37, v4
	s_waitcnt lgkmcnt(1)
	v_max_f32_e32 v11, v11, v11
	v_max_f32_e32 v11, v3, v11
	ds_bpermute_b32 v16, v13, v11
	s_waitcnt lgkmcnt(1)
	v_max_f32_e32 v8, v8, v8
	v_max_f32_e32 v7, v7, v8
	ds_bpermute_b32 v8, v14, v7
	v_cndmask_b32_e32 v4, v229, v6, vcc
	s_waitcnt lgkmcnt(1)
	v_max_f32_e32 v16, v16, v16
	v_max_f32_e32 v11, v11, v16
	ds_bpermute_b32 v16, v14, v11
	s_waitcnt lgkmcnt(1)
	v_max_f32_e32 v8, v8, v8
	v_max_f32_e32 v7, v7, v8
	ds_bpermute_b32 v8, v15, v7
	ds_bpermute_b32 v6, v12, v4
	s_waitcnt lgkmcnt(2)
	v_max_f32_e32 v16, v16, v16
	v_max_f32_e32 v11, v11, v16
	ds_bpermute_b32 v16, v15, v11
	s_waitcnt lgkmcnt(2)
	v_max_f32_e32 v8, v8, v8
	v_max_f32_e32 v7, v7, v8
	v_sub_f32_e32 v5, v5, v7
	v_mul_f32_e32 v7, 0x3fb8aa3b, v5
	v_fma_f32 v8, v5, s35, -v7
	v_rndne_f32_e32 v9, v7
	s_waitcnt lgkmcnt(0)
	v_max_f32_e32 v16, v16, v16
	v_fmac_f32_e32 v8, 0x32a5705f, v5
	v_sub_f32_e32 v7, v7, v9
	v_max_f32_e32 v11, v11, v16
	v_add_f32_e32 v7, v7, v8
	v_sub_f32_e32 v3, v3, v11
	v_exp_f32_e32 v7, v7
	v_cvt_i32_f32_e32 v8, v9
	v_mul_f32_e32 v11, 0x3fb8aa3b, v3
	v_fma_f32 v16, v3, s35, -v11
	v_rndne_f32_e32 v17, v11
	v_fmac_f32_e32 v16, 0x32a5705f, v3
	v_sub_f32_e32 v11, v11, v17
	v_add_f32_e32 v11, v11, v16
	v_ldexp_f32 v7, v7, v8
	v_cmp_ngt_f32_e32 vcc, s36, v5
	v_exp_f32_e32 v11, v11
	v_cvt_i32_f32_e32 v16, v17
	v_cndmask_b32_e32 v7, 0, v7, vcc
	v_cmp_nlt_f32_e32 vcc, s37, v5
	v_ldexp_f32 v11, v11, v16
	s_nop 0
	v_cndmask_b32_e32 v5, v229, v7, vcc
	v_cmp_ngt_f32_e32 vcc, s36, v2
	ds_bpermute_b32 v7, v12, v5
	s_waitcnt lgkmcnt(0)
	v_pk_add_f32 v[6:7], v[4:5], v[6:7]
	v_cndmask_b32_e32 v10, 0, v10, vcc
	v_cmp_nlt_f32_e32 vcc, s37, v2
	ds_bpermute_b32 v8, v13, v6
	ds_bpermute_b32 v9, v13, v7
	v_cndmask_b32_e32 v10, v229, v10, vcc
	v_cmp_ngt_f32_e32 vcc, s36, v3
	ds_bpermute_b32 v2, v12, v10
	s_waitcnt lgkmcnt(1)
	v_pk_add_f32 v[6:7], v[6:7], v[8:9]
	v_cndmask_b32_e32 v11, 0, v11, vcc
	v_cmp_nlt_f32_e32 vcc, s37, v3
	ds_bpermute_b32 v8, v14, v6
	ds_bpermute_b32 v9, v14, v7
	v_cndmask_b32_e32 v11, v229, v11, vcc
	ds_bpermute_b32 v3, v12, v11
	s_waitcnt lgkmcnt(1)
	v_pk_add_f32 v[6:7], v[6:7], v[8:9]
	ds_bpermute_b32 v8, v15, v6
	s_waitcnt lgkmcnt(1)
	v_pk_add_f32 v[2:3], v[10:11], v[2:3]
	ds_bpermute_b32 v12, v13, v2
	ds_bpermute_b32 v13, v13, v3
	ds_bpermute_b32 v9, v15, v7
	s_waitcnt lgkmcnt(1)
	v_pk_add_f32 v[2:3], v[2:3], v[12:13]
	ds_bpermute_b32 v12, v14, v2
	ds_bpermute_b32 v13, v14, v3
	s_waitcnt lgkmcnt(0)
	v_pk_add_f32 v[2:3], v[2:3], v[12:13]
	ds_bpermute_b32 v12, v15, v2
	ds_bpermute_b32 v13, v15, v3
	s_waitcnt lgkmcnt(0)
	v_pk_add_f32 v[12:13], v[2:3], v[12:13]
	v_pk_add_f32 v[2:3], v[6:7], v[8:9]
	s_nop 0
	v_div_scale_f32 v6, s[2:3], v3, v3, v5
	v_rcp_f32_e32 v7, v6
	s_nop 0
	v_fma_f32 v8, -v6, v7, 1.0
	v_fmac_f32_e32 v7, v8, v7
	v_div_scale_f32 v8, vcc, v5, v3, v5
	v_mul_f32_e32 v9, v8, v7
	v_fma_f32 v14, -v6, v9, v8
	v_fmac_f32_e32 v9, v14, v7
	v_fma_f32 v6, -v6, v9, v8
	v_div_fmas_f32 v6, v6, v7, v9
	v_div_fixup_f32 v3, v6, v3, v5
	v_div_scale_f32 v5, s[2:3], v2, v2, v4
	v_rcp_f32_e32 v6, v5
	s_nop 0
	v_fma_f32 v7, -v5, v6, 1.0
	v_fmac_f32_e32 v6, v7, v6
	v_div_scale_f32 v7, vcc, v4, v2, v4
	v_mul_f32_e32 v8, v7, v6
	v_fma_f32 v9, -v5, v8, v7
	v_fmac_f32_e32 v8, v9, v6
	v_fma_f32 v5, -v5, v8, v7
	v_div_fmas_f32 v5, v5, v6, v8
	v_div_fixup_f32 v2, v5, v2, v4
	v_div_scale_f32 v4, s[2:3], v13, v13, v11
	v_rcp_f32_e32 v5, v4
	s_nop 0
	v_fma_f32 v6, -v4, v5, 1.0
	v_fmac_f32_e32 v5, v6, v5
	v_div_scale_f32 v6, vcc, v11, v13, v11
	v_mul_f32_e32 v7, v6, v5
	v_fma_f32 v8, -v4, v7, v6
	v_fmac_f32_e32 v7, v8, v5
	v_fma_f32 v4, -v4, v7, v6
	v_div_fmas_f32 v4, v4, v5, v7
	v_div_fixup_f32 v5, v4, v13, v11
	v_div_scale_f32 v4, s[2:3], v12, v12, v10
	v_rcp_f32_e32 v6, v4
	s_lshl_b64 s[2:3], s[22:23], 17
	v_fma_f32 v7, -v4, v6, 1.0
	v_fmac_f32_e32 v6, v7, v6
	v_div_scale_f32 v7, vcc, v10, v12, v10
	v_mul_f32_e32 v8, v7, v6
	v_fma_f32 v9, -v4, v8, v7
	v_fmac_f32_e32 v8, v9, v6
	v_fma_f32 v4, -v4, v8, v7
	v_div_fmas_f32 v4, v4, v6, v8
	v_lshl_add_u64 v[6:7], v[26:27], 0, s[2:3]
	v_lshl_add_u64 v[6:7], v[6:7], 0, s[0:1]
	s_add_i32 s0, s34, 0x800
	v_div_fixup_f32 v4, v4, v12, v10
	v_lshl_add_u64 v[6:7], v[6:7], 0, v[18:19]
	s_cmp_lt_i32 s34, 0
	s_mov_b32 s34, s0
	global_store_dwordx4 v[6:7], v[2:5], off
	s_cbranch_scc1 .LBB0_808

; #define LAS __attribute__((address_space(3)))
; template <int R, bool RT = false>
; __device__ __forceinline__ void norm_phase(const NormArgs& a, LAS unsigned char* lds, bool ctx_rows, const float* ctx_src, const float* ctx_shift, const float* ctx_scale) {
;     ...
;             for (int q = 0; q < R; ++q) { const int row = row0 + rr + q;
;                 if (a.src16) { const f16* xr = a.src16 + (size_t)row * DM;
; #pragma unroll
;                     for (int j = 0; j < 4; ++j) { const f16x4 t = *(const f16x4*)(xr + 4 * lane + 256 * j); v[q][j] = (f32x4){(float)t[0], (float)t[1], (float)t[2], (float)t[3]};
;                         if constexpr (RT) { if (j == 0) *(LAS u32x2*)(hs + (rr + q) * 528 + 8 * lane) = __builtin_bit_cast(u32x2, t);
;                             else xp[rr / 4][q][j - 1] = __builtin_bit_cast(u32x2, t); } } }
;                 else { const float* xr = a.src + (size_t)row * DM;
; #pragma unroll
;                     for (int j = 0; j < 4; ++j) v[q][j] = *(const f32x4*)(xr + 4 * lane + 256 * j); } }
;             if (a.y2) {
;                 unsigned long long mask[R]; int ee[R][4]; float wgt[R][4]; f16x4 ld[R][4][4];
;                 int cnt[R];
; #pragma unroll
;                 for (int q = 0; q < R; ++q) { mask[q] = __ballot(sl[q] >= 0); cnt[q] = __builtin_popcountll(mask[q]);
; #pragma unroll
;                     for (int i = 0; i < 4; ++i) { if (mask[q]) { ee[q][i] = __builtin_ctzll(mask[q]); mask[q] &= mask[q] - 1; wgt[q][i] = 1.f; } else { ee[q][i] = i ? ee[q][0] : 0; wgt[q][i] = 0.f; } }
; #pragma unroll
;                     for (int i = 0; i < 4; ++i) {
;                         if (i < cnt[q]) { int slot = __shfl(sl[q], ee[q][i]); slot = slot < 0 ? 0 : slot; const f16* yr = a.y2 + ((size_t)ee[q][i] * EROWS + b * CAP + slot) * DM + 4 * lane;
; #pragma unroll
;                             for (int j = 0; j < 4; ++j) ld[q][i][j] = *(const f16x4*)(yr + 256 * j); } } }
; #pragma unroll
;                 for (int q = 0; q < R; ++q) { const int row = row0 + rr + q;
;                     f32x4 cs[4];
; #pragma unroll
;                     for (int j = 0; j < 4; ++j) cs[j] = (f32x4){0.f, 0.f, 0.f, 0.f};
; #pragma unroll
;                     for (int i = 0; i < 4; ++i) if (i < cnt[q]) {
; #pragma unroll
.LBB0_831:
	s_or_b32 s20, s30, s29
	s_ashr_i32 s21, s20, 31
	s_lshl_b64 s[0:1], s[20:21], 11
	v_lshl_add_u64 v[18:19], v[100:101], 0, s[0:1]
	global_load_dwordx2 v[20:21], v[18:19], off nt
	global_load_dwordx2 v[24:25], v[18:19], off offset:512 nt
	global_load_dwordx2 v[28:29], v[18:19], off offset:1024 nt
	global_load_dwordx2 v[32:33], v[18:19], off offset:1536 nt
	s_or_b32 s2, s20, 1
	s_ashr_i32 s3, s2, 31
	s_lshl_b64 s[2:3], s[2:3], 11
	v_lshl_add_u64 v[18:19], v[100:101], 0, s[2:3]
	global_load_dwordx2 v[36:37], v[18:19], off nt
	global_load_dwordx2 v[40:41], v[18:19], off offset:512 nt
	global_load_dwordx2 v[44:45], v[18:19], off offset:1024 nt
	global_load_dwordx2 v[48:49], v[18:19], off offset:1536 nt
	s_or_b32 s18, s20, 2
	s_ashr_i32 s19, s18, 31
	s_lshl_b64 s[18:19], s[18:19], 11
	v_lshl_add_u64 v[18:19], v[100:101], 0, s[18:19]
	global_load_dwordx2 v[52:53], v[18:19], off nt
	global_load_dwordx2 v[56:57], v[18:19], off offset:512 nt
	global_load_dwordx2 v[60:61], v[18:19], off offset:1024 nt
	global_load_dwordx2 v[64:65], v[18:19], off offset:1536 nt
	s_or_b32 s20, s20, 3
	s_ashr_i32 s21, s20, 31
	s_lshl_b64 s[20:21], s[20:21], 11
	v_lshl_add_u64 v[18:19], v[100:101], 0, s[20:21]
	global_load_dwordx2 v[68:69], v[18:19], off nt
	global_load_dwordx2 v[72:73], v[18:19], off offset:512 nt
	global_load_dwordx2 v[76:77], v[18:19], off offset:1024 nt
	global_load_dwordx2 v[80:81], v[18:19], off offset:1536 nt
	s_and_b64 vcc, exec, s[4:5]
	s_waitcnt vmcnt(15)
	v_cvt_f32_f16_e32 v18, v20
	v_cvt_f32_f16_sdwa v19, v20 dst_sel:DWORD dst_unused:UNUSED_PAD src0_sel:WORD_1
	v_cvt_f32_f16_e32 v20, v21
	v_cvt_f32_f16_sdwa v21, v21 dst_sel:DWORD dst_unused:UNUSED_PAD src0_sel:WORD_1
	s_waitcnt vmcnt(14)
	v_cvt_f32_f16_e32 v22, v24
	v_cvt_f32_f16_sdwa v23, v24 dst_sel:DWORD dst_unused:UNUSED_PAD src0_sel:WORD_1
	v_cvt_f32_f16_e32 v24, v25
	v_cvt_f32_f16_sdwa v25, v25 dst_sel:DWORD dst_unused:UNUSED_PAD src0_sel:WORD_1
	s_waitcnt vmcnt(13)
	v_cvt_f32_f16_e32 v26, v28
	v_cvt_f32_f16_sdwa v27, v28 dst_sel:DWORD dst_unused:UNUSED_PAD src0_sel:WORD_1
	v_cvt_f32_f16_e32 v28, v29
	v_cvt_f32_f16_sdwa v29, v29 dst_sel:DWORD dst_unused:UNUSED_PAD src0_sel:WORD_1
	s_waitcnt vmcnt(12)
	v_cvt_f32_f16_e32 v30, v32
	v_cvt_f32_f16_sdwa v31, v32 dst_sel:DWORD dst_unused:UNUSED_PAD src0_sel:WORD_1
	v_cvt_f32_f16_e32 v32, v33
	v_cvt_f32_f16_sdwa v33, v33 dst_sel:DWORD dst_unused:UNUSED_PAD src0_sel:WORD_1
	s_waitcnt lgkmcnt(0)
	v_mov_b32_e32 v84, v19
	v_mov_b32_e32 v85, v21
	v_mov_b32_e32 v82, v18
	v_mov_b32_e32 v83, v20
	v_pk_mul_f32 v[84:85], v[84:85], v[84:85]
	v_mov_b32_e32 v86, v23
	v_mov_b32_e32 v87, v25
	v_pk_fma_f32 v[82:83], v[82:83], v[82:83], v[84:85]
	v_mov_b32_e32 v84, v22
	v_mov_b32_e32 v85, v24
	v_pk_mul_f32 v[86:87], v[86:87], v[86:87]
	v_mul_f32_e32 v88, v29, v29
	v_pk_fma_f32 v[84:85], v[84:85], v[84:85], v[86:87]
	v_mul_f32_e32 v86, v27, v27
	s_waitcnt vmcnt(11)
	v_cvt_f32_f16_e32 v34, v36
	v_cvt_f32_f16_sdwa v35, v36 dst_sel:DWORD dst_unused:UNUSED_PAD src0_sel:WORD_1
	v_cvt_f32_f16_e32 v36, v37
	v_cvt_f32_f16_sdwa v37, v37 dst_sel:DWORD dst_unused:UNUSED_PAD src0_sel:WORD_1
	v_pk_add_f32 v[82:83], v[82:83], v[82:83] op_sel:[0,1] op_sel_hi:[1,0]
	v_pk_add_f32 v[84:85], v[84:85], v[84:85] op_sel:[0,1] op_sel_hi:[1,0]
	v_pk_fma_f32 v[86:87], v[26:27], v[26:27], v[86:87] op_sel_hi:[1,1,0]
	v_pk_fma_f32 v[88:89], v[28:29], v[28:29], v[88:89] op_sel_hi:[1,1,0]
	v_pk_mul_f32 v[90:91], v[30:31], v[30:31]
	v_pk_mul_f32 v[92:93], v[32:33], v[32:33]
	s_waitcnt vmcnt(10)
	v_cvt_f32_f16_e32 v38, v40
	v_cvt_f32_f16_sdwa v39, v40 dst_sel:DWORD dst_unused:UNUSED_PAD src0_sel:WORD_1
	v_cvt_f32_f16_e32 v40, v41
	v_cvt_f32_f16_sdwa v41, v41 dst_sel:DWORD dst_unused:UNUSED_PAD src0_sel:WORD_1
	v_mov_b32_e32 v83, v90
	v_mov_b32_e32 v85, v91
	v_mov_b32_e32 v87, v92
	v_mov_b32_e32 v89, v93
	v_pk_add_f32 v[82:83], v[82:83], v[84:85]
	v_pk_add_f32 v[84:85], v[86:87], v[88:89]
	s_waitcnt vmcnt(9)
	v_cvt_f32_f16_e32 v42, v44
	v_cvt_f32_f16_sdwa v43, v44 dst_sel:DWORD dst_unused:UNUSED_PAD src0_sel:WORD_1
	v_cvt_f32_f16_e32 v44, v45
	v_cvt_f32_f16_sdwa v45, v45 dst_sel:DWORD dst_unused:UNUSED_PAD src0_sel:WORD_1
	v_pk_add_f32 v[82:83], v[82:83], v[84:85]
	s_waitcnt vmcnt(8)
	v_cvt_f32_f16_e32 v46, v48
	v_cvt_f32_f16_sdwa v47, v48 dst_sel:DWORD dst_unused:UNUSED_PAD src0_sel:WORD_1
	v_cvt_f32_f16_e32 v48, v49
	v_cvt_f32_f16_sdwa v49, v49 dst_sel:DWORD dst_unused:UNUSED_PAD src0_sel:WORD_1
	v_add_f32_e32 v82, v82, v83
	v_mov_b32_e32 v86, v35
	v_mov_b32_e32 v87, v37
	v_add_f32_dpp v82, v82, v82 quad_perm:[1,0,3,2] row_mask:0xf bank_mask:0xf bound_ctrl:1
	v_mov_b32_e32 v84, v34
	v_mov_b32_e32 v85, v36
	v_pk_mul_f32 v[86:87], v[86:87], v[86:87]
	v_mov_b32_e32 v88, v39
	v_mov_b32_e32 v89, v41
	v_add_f32_dpp v82, v82, v82 quad_perm:[2,3,0,1] row_mask:0xf bank_mask:0xf bound_ctrl:1
	v_pk_fma_f32 v[84:85], v[84:85], v[84:85], v[86:87]
	v_mov_b32_e32 v86, v38
	v_mov_b32_e32 v87, v40
	v_pk_mul_f32 v[88:89], v[88:89], v[88:89]
	v_add_f32_dpp v82, v82, v82 row_half_mirror row_mask:0xf bank_mask:0xf bound_ctrl:1
	v_pk_fma_f32 v[86:87], v[86:87], v[86:87], v[88:89]
	v_mul_f32_e32 v88, v43, v43
	v_mul_f32_e32 v90, v45, v45
	v_add_f32_dpp v82, v82, v82 row_mirror row_mask:0xf bank_mask:0xf bound_ctrl:1
	v_mov_b32_e32 v83, 0
	v_pk_add_f32 v[84:85], v[84:85], v[84:85] op_sel:[0,1] op_sel_hi:[1,0]
	v_pk_add_f32 v[86:87], v[86:87], v[86:87] op_sel:[0,1] op_sel_hi:[1,0]
	v_pk_fma_f32 v[88:89], v[42:43], v[42:43], v[88:89] op_sel_hi:[1,1,0]
	v_pk_fma_f32 v[90:91], v[44:45], v[44:45], v[90:91] op_sel_hi:[1,1,0]
	v_pk_mul_f32 v[92:93], v[46:47], v[46:47]
	v_pk_mul_f32 v[94:95], v[48:49], v[48:49]
	v_mov_b32_dpp v83, v82 row_bcast:15 row_mask:0xa bank_mask:0xf
	v_mov_b32_e32 v85, v92
	v_mov_b32_e32 v87, v93
	v_mov_b32_e32 v89, v94
	v_mov_b32_e32 v91, v95
	v_add_f32_e32 v82, v82, v83
	v_mov_b32_e32 v83, 0
	v_pk_add_f32 v[84:85], v[84:85], v[86:87]
	v_pk_add_f32 v[86:87], v[88:89], v[90:91]
	s_waitcnt vmcnt(7)
; template <int R, bool RT = false>
; __device__ __forceinline__ void norm_phase(const NormArgs& a, LAS unsigned char* lds, bool ctx_rows, const float* ctx_src, const float* ctx_shift, const float* ctx_scale) {
;     ...
;             for (int q = 0; q < R; ++q) { float ss = 0.f;
; #pragma unroll
;                 for (int j = 0; j < 4; ++j) ss += (v[q][j][0] * v[q][j][0] + v[q][j][1] * v[q][j][1]) + (v[q][j][2] * v[q][j][2] + v[q][j][3] * v[q][j][3]);
;                 rstd[q] = __builtin_amdgcn_rsqf(wave_sum(ss) * (1.f / DM) + EPS);
;                 if constexpr (RT) rsel[q] = ((lane >> 4) == rr / 4) ? rstd[q] : rsel[q]; }
	v_cvt_f32_f16_e32 v50, v52
	v_cvt_f32_f16_sdwa v51, v52 dst_sel:DWORD dst_unused:UNUSED_PAD src0_sel:WORD_1
	v_cvt_f32_f16_e32 v52, v53
	v_cvt_f32_f16_sdwa v53, v53 dst_sel:DWORD dst_unused:UNUSED_PAD src0_sel:WORD_1
	v_mov_b32_dpp v83, v82 row_bcast:31 row_mask:0xc bank_mask:0xf
	v_pk_add_f32 v[84:85], v[84:85], v[86:87]
	s_waitcnt vmcnt(6)
	v_cvt_f32_f16_e32 v54, v56
	v_cvt_f32_f16_sdwa v55, v56 dst_sel:DWORD dst_unused:UNUSED_PAD src0_sel:WORD_1
	v_cvt_f32_f16_e32 v56, v57
	v_cvt_f32_f16_sdwa v57, v57 dst_sel:DWORD dst_unused:UNUSED_PAD src0_sel:WORD_1
	v_add_f32_e32 v82, v82, v83
	v_add_f32_e32 v83, v84, v85
	s_waitcnt vmcnt(5)
	v_cvt_f32_f16_e32 v58, v60
	v_cvt_f32_f16_sdwa v59, v60 dst_sel:DWORD dst_unused:UNUSED_PAD src0_sel:WORD_1
	v_add_f32_dpp v83, v83, v83 quad_perm:[1,0,3,2] row_mask:0xf bank_mask:0xf bound_ctrl:1
	v_cvt_f32_f16_e32 v60, v61
	v_cvt_f32_f16_sdwa v61, v61 dst_sel:DWORD dst_unused:UNUSED_PAD src0_sel:WORD_1
	v_add_f32_dpp v83, v83, v83 quad_perm:[2,3,0,1] row_mask:0xf bank_mask:0xf bound_ctrl:1
	s_waitcnt vmcnt(4)
	v_cvt_f32_f16_e32 v62, v64
	v_cvt_f32_f16_sdwa v63, v64 dst_sel:DWORD dst_unused:UNUSED_PAD src0_sel:WORD_1
	v_cvt_f32_f16_e32 v64, v65
	v_cvt_f32_f16_sdwa v65, v65 dst_sel:DWORD dst_unused:UNUSED_PAD src0_sel:WORD_1
	v_add_f32_dpp v83, v83, v83 row_half_mirror row_mask:0xf bank_mask:0xf bound_ctrl:1
	v_mov_b32_e32 v88, v51
	v_mov_b32_e32 v89, v53
	v_add_f32_dpp v83, v83, v83 row_mirror row_mask:0xf bank_mask:0xf bound_ctrl:1
	v_mov_b32_e32 v84, 0
	v_mov_b32_e32 v86, v50
	v_mov_b32_e32 v87, v52
	v_pk_mul_f32 v[88:89], v[88:89], v[88:89]
	v_mov_b32_e32 v90, v55
	v_mov_b32_e32 v91, v57
	v_mov_b32_dpp v84, v83 row_bcast:15 row_mask:0xa bank_mask:0xf
	v_pk_fma_f32 v[86:87], v[86:87], v[86:87], v[88:89]
	v_mov_b32_e32 v88, v54
	v_mov_b32_e32 v89, v56
	v_pk_mul_f32 v[90:91], v[90:91], v[90:91]
	v_add_f32_e32 v83, v83, v84
	v_mov_b32_e32 v84, 0
	v_pk_fma_f32 v[88:89], v[88:89], v[88:89], v[90:91]
	v_mul_f32_e32 v90, v59, v59
	v_mul_f32_e32 v92, v61, v61
	v_mov_b32_dpp v84, v83 row_bcast:31 row_mask:0xc bank_mask:0xf
	v_pk_add_f32 v[86:87], v[86:87], v[86:87] op_sel:[0,1] op_sel_hi:[1,0]
	v_pk_add_f32 v[88:89], v[88:89], v[88:89] op_sel:[0,1] op_sel_hi:[1,0]
	v_pk_fma_f32 v[90:91], v[58:59], v[58:59], v[90:91] op_sel_hi:[1,1,0]
	v_pk_fma_f32 v[92:93], v[60:61], v[60:61], v[92:93] op_sel_hi:[1,1,0]
	v_pk_mul_f32 v[94:95], v[62:63], v[62:63]
	v_pk_mul_f32 v[96:97], v[64:65], v[64:65]
	v_readlane_b32 s31, v82, 63
	v_add_f32_e32 v83, v83, v84
	v_mov_b32_e32 v87, v94
	v_mov_b32_e32 v89, v95
	v_mov_b32_e32 v91, v96
	v_mov_b32_e32 v93, v97
	v_fma_f32 v82, s31, v130, v129
	v_readlane_b32 s31, v83, 63
	v_pk_add_f32 v[86:87], v[86:87], v[88:89]
	v_pk_add_f32 v[88:89], v[90:91], v[92:93]
	s_waitcnt vmcnt(3)
	v_cvt_f32_f16_e32 v66, v68
	v_cvt_f32_f16_sdwa v67, v68 dst_sel:DWORD dst_unused:UNUSED_PAD src0_sel:WORD_1
	v_cvt_f32_f16_e32 v68, v69
	v_cvt_f32_f16_sdwa v69, v69 dst_sel:DWORD dst_unused:UNUSED_PAD src0_sel:WORD_1
	v_fma_f32 v83, s31, v130, v129
	v_pk_add_f32 v[86:87], v[86:87], v[88:89]
	s_waitcnt vmcnt(2)
	v_cvt_f32_f16_e32 v70, v72
	v_cvt_f32_f16_sdwa v71, v72 dst_sel:DWORD dst_unused:UNUSED_PAD src0_sel:WORD_1
	v_cvt_f32_f16_e32 v72, v73
	v_cvt_f32_f16_sdwa v73, v73 dst_sel:DWORD dst_unused:UNUSED_PAD src0_sel:WORD_1
	v_rsq_f32_e32 v84, v83
	v_add_f32_e32 v83, v86, v87
	s_waitcnt vmcnt(1)
	v_cvt_f32_f16_e32 v74, v76
	v_cvt_f32_f16_sdwa v75, v76 dst_sel:DWORD dst_unused:UNUSED_PAD src0_sel:WORD_1
	v_add_f32_dpp v83, v83, v83 quad_perm:[1,0,3,2] row_mask:0xf bank_mask:0xf bound_ctrl:1
	v_cvt_f32_f16_e32 v76, v77
	v_cvt_f32_f16_sdwa v77, v77 dst_sel:DWORD dst_unused:UNUSED_PAD src0_sel:WORD_1
	v_add_f32_dpp v83, v83, v83 quad_perm:[2,3,0,1] row_mask:0xf bank_mask:0xf bound_ctrl:1
	s_waitcnt vmcnt(0)
	v_cvt_f32_f16_e32 v78, v80
	v_cvt_f32_f16_sdwa v79, v80 dst_sel:DWORD dst_unused:UNUSED_PAD src0_sel:WORD_1
	v_cvt_f32_f16_e32 v80, v81
	v_cvt_f32_f16_sdwa v81, v81 dst_sel:DWORD dst_unused:UNUSED_PAD src0_sel:WORD_1
	v_add_f32_dpp v83, v83, v83 row_half_mirror row_mask:0xf bank_mask:0xf bound_ctrl:1
	v_mov_b32_e32 v90, v67
	v_mov_b32_e32 v91, v69
	v_add_f32_dpp v83, v83, v83 row_mirror row_mask:0xf bank_mask:0xf bound_ctrl:1
	v_mov_b32_e32 v85, 0
	v_mov_b32_e32 v88, v66
	v_mov_b32_e32 v89, v68
	v_pk_mul_f32 v[90:91], v[90:91], v[90:91]
	v_mov_b32_e32 v92, v71
	v_mov_b32_e32 v93, v73
	v_mov_b32_dpp v85, v83 row_bcast:15 row_mask:0xa bank_mask:0xf
	v_pk_fma_f32 v[88:89], v[88:89], v[88:89], v[90:91]
	v_mov_b32_e32 v90, v70
	v_mov_b32_e32 v91, v72
	v_pk_mul_f32 v[92:93], v[92:93], v[92:93]
	v_add_f32_e32 v83, v83, v85
	v_mov_b32_e32 v85, 0
	v_pk_fma_f32 v[90:91], v[90:91], v[90:91], v[92:93]
	v_mul_f32_e32 v92, v75, v75
	v_mul_f32_e32 v94, v77, v77
	v_mov_b32_dpp v85, v83 row_bcast:31 row_mask:0xc bank_mask:0xf
	v_pk_add_f32 v[88:89], v[88:89], v[88:89] op_sel:[0,1] op_sel_hi:[1,0]
	v_pk_add_f32 v[90:91], v[90:91], v[90:91] op_sel:[0,1] op_sel_hi:[1,0]
	v_pk_fma_f32 v[92:93], v[74:75], v[74:75], v[92:93] op_sel_hi:[1,1,0]
	v_pk_fma_f32 v[94:95], v[76:77], v[76:77], v[94:95] op_sel_hi:[1,1,0]
	v_pk_mul_f32 v[96:97], v[78:79], v[78:79]
	v_pk_mul_f32 v[134:135], v[80:81], v[80:81]
	v_add_f32_e32 v83, v83, v85
	v_mov_b32_e32 v89, v96
	v_mov_b32_e32 v91, v97
	v_mov_b32_e32 v93, v134
	v_mov_b32_e32 v95, v135
	v_readlane_b32 s31, v83, 63
	v_pk_add_f32 v[88:89], v[88:89], v[90:91]
	v_pk_add_f32 v[90:91], v[92:93], v[94:95]
	v_fma_f32 v83, s31, v130, v129
	v_pk_add_f32 v[88:89], v[88:89], v[90:91]
	v_rsq_f32_e32 v86, v83
	v_add_f32_e32 v83, v88, v89
	v_mov_b32_e32 v85, 0
	v_rsq_f32_e32 v82, v82
; __device__ __forceinline__ unsigned pkb(float lo, float hi) { f32x2 v = {lo, hi}; bf16x2_t b = __builtin_convertvector(v, bf16x2_t); return __builtin_bit_cast(unsigned, b); }
; template <int R, bool RT = false>
; __device__ __forceinline__ void norm_phase(const NormArgs& a, LAS unsigned char* lds, bool ctx_rows, const float* ctx_src, const float* ctx_shift, const float* ctx_scale) {
;     ...
;             float rstd[R];
; #pragma unroll
;             for (int q = 0; q < R; ++q) { float ss = 0.f;
; #pragma unroll
;                 for (int j = 0; j < 4; ++j) ss += (v[q][j][0] * v[q][j][0] + v[q][j][1] * v[q][j][1]) + (v[q][j][2] * v[q][j][2] + v[q][j][3] * v[q][j][3]);
;                 rstd[q] = __builtin_amdgcn_rsqf(wave_sum(ss) * (1.f / DM) + EPS);
;                 if constexpr (RT) rsel[q] = ((lane >> 4) == rr / 4) ? rstd[q] : rsel[q]; }
; #pragma unroll
;             for (int q = 0; q < R; ++q) { const int row = row0 + rr + q;
; #pragma unroll
;                 for (int j = 0; j < 4; ++j) v[q][j] = (v[q][j] * rstd[q]) * A[j] + Sh[j];
;                 if (a.fout) {
; #pragma unroll
;                     for (int j = 0; j < 4; ++j) *(f32x4*)(a.fout + (size_t)row * DM + 4 * lane + 256 * j) = v[q][j];
;                 }
;                 if (a.hout) {
; #pragma unroll
;                     for (int j = 0; j < 4; ++j) { u32x2 w; if (a.hbf) { w.x = pkb(v[q][j][0], v[q][j][1]); w.y = pkb(v[q][j][2], v[q][j][3]); } else { w.x = pkh(v[q][j][0], v[q][j][1]); w.y = pkh(v[q][j][2], v[q][j][3]); } *(u32x2*)(a.hout + (size_t)row * DM + 4 * lane + 256 * j) = w; }
;                 }
	v_add_f32_dpp v83, v83, v83 quad_perm:[1,0,3,2] row_mask:0xf bank_mask:0xf bound_ctrl:1
	v_lshl_add_u64 v[90:91], v[102:103], 0, s[0:1]
	v_pk_mul_f32 v[50:51], v[50:51], v[86:87] op_sel_hi:[1,0]
	v_add_f32_dpp v83, v83, v83 quad_perm:[2,3,0,1] row_mask:0xf bank_mask:0xf bound_ctrl:1
	v_pk_mul_f32 v[52:53], v[52:53], v[86:87] op_sel_hi:[1,0]
	v_pk_fma_f32 v[50:51], v[114:115], v[50:51], v[2:3]
	v_add_f32_dpp v83, v83, v83 row_half_mirror row_mask:0xf bank_mask:0xf bound_ctrl:1
	v_pk_fma_f32 v[52:53], v[112:113], v[52:53], v[4:5]
	v_pk_mul_f32 v[54:55], v[54:55], v[86:87] op_sel_hi:[1,0]
	v_add_f32_dpp v83, v83, v83 row_mirror row_mask:0xf bank_mask:0xf bound_ctrl:1
	v_pk_mul_f32 v[56:57], v[56:57], v[86:87] op_sel_hi:[1,0]
	v_pk_fma_f32 v[54:55], v[118:119], v[54:55], v[6:7]
	v_mov_b32_dpp v85, v83 row_bcast:15 row_mask:0xa bank_mask:0xf
	v_add_f32_e32 v83, v83, v85
	v_mov_b32_e32 v85, 0
	v_pk_fma_f32 v[56:57], v[116:117], v[56:57], v[8:9]
	v_pk_mul_f32 v[58:59], v[58:59], v[86:87] op_sel_hi:[1,0]
	v_mov_b32_dpp v85, v83 row_bcast:31 row_mask:0xc bank_mask:0xf
	v_add_f32_e32 v83, v83, v85
	v_pk_mul_f32 v[34:35], v[34:35], v[84:85] op_sel_hi:[1,0]
	v_readlane_b32 s31, v83, 63
	v_pk_mul_f32 v[36:37], v[36:37], v[84:85] op_sel_hi:[1,0]
	v_pk_fma_f32 v[34:35], v[114:115], v[34:35], v[2:3]
	v_fma_f32 v83, s31, v130, v129
	v_pk_mul_f32 v[18:19], v[18:19], v[82:83] op_sel_hi:[1,0]
	v_pk_mul_f32 v[20:21], v[20:21], v[82:83] op_sel_hi:[1,0]
	v_pk_fma_f32 v[18:19], v[114:115], v[18:19], v[2:3]
	v_pk_fma_f32 v[20:21], v[112:113], v[20:21], v[4:5]
	v_pk_mul_f32 v[22:23], v[22:23], v[82:83] op_sel_hi:[1,0]
	v_pk_mul_f32 v[24:25], v[24:25], v[82:83] op_sel_hi:[1,0]
	v_rsq_f32_e32 v88, v83
	v_pk_fma_f32 v[24:25], v[116:117], v[24:25], v[8:9]
	v_pk_fma_f32 v[22:23], v[118:119], v[22:23], v[6:7]
	v_pk_mul_f32 v[26:27], v[26:27], v[82:83] op_sel_hi:[1,0]
	v_pk_mul_f32 v[28:29], v[28:29], v[82:83] op_sel_hi:[1,0]
	v_pk_mul_f32 v[30:31], v[30:31], v[82:83] op_sel_hi:[1,0]
	v_pk_mul_f32 v[32:33], v[32:33], v[82:83] op_sel_hi:[1,0]
	v_cvt_pk_bf16_f32 v82, v18, v19
	v_cvt_pk_bf16_f32 v83, v20, v21
	v_pk_fma_f32 v[28:29], v[120:121], v[28:29], v[12:13]
	v_pk_fma_f32 v[26:27], v[122:123], v[26:27], v[10:11]
	global_store_dwordx2 v[90:91], v[82:83], off
	v_cvt_pk_bf16_f32 v82, v22, v23
	v_cvt_pk_bf16_f32 v83, v24, v25
	v_pk_fma_f32 v[32:33], v[124:125], v[32:33], v[16:17]
	v_pk_fma_f32 v[30:31], v[126:127], v[30:31], v[14:15]
	global_store_dwordx2 v[90:91], v[82:83], off offset:512
	v_cvt_pk_bf16_f32 v82, v26, v27
	v_cvt_pk_bf16_f32 v83, v28, v29
	global_store_dwordx2 v[90:91], v[82:83], off offset:1024
	v_cvt_pk_bf16_f32 v82, v30, v31
	v_cvt_pk_bf16_f32 v83, v32, v33
	v_pk_fma_f32 v[36:37], v[112:113], v[36:37], v[4:5]
	v_pk_mul_f32 v[38:39], v[38:39], v[84:85] op_sel_hi:[1,0]
	v_pk_mul_f32 v[40:41], v[40:41], v[84:85] op_sel_hi:[1,0]
	global_store_dwordx2 v[90:91], v[82:83], off offset:1536
	v_pk_fma_f32 v[40:41], v[116:117], v[40:41], v[8:9]
	v_pk_fma_f32 v[38:39], v[118:119], v[38:39], v[6:7]
	v_pk_mul_f32 v[42:43], v[42:43], v[84:85] op_sel_hi:[1,0]
	v_pk_mul_f32 v[44:45], v[44:45], v[84:85] op_sel_hi:[1,0]
	v_pk_mul_f32 v[46:47], v[46:47], v[84:85] op_sel_hi:[1,0]
	v_pk_mul_f32 v[48:49], v[48:49], v[84:85] op_sel_hi:[1,0]
	v_cvt_pk_bf16_f32 v82, v34, v35
	v_cvt_pk_bf16_f32 v83, v36, v37
	v_lshl_add_u64 v[84:85], v[102:103], 0, s[2:3]
	v_pk_fma_f32 v[44:45], v[120:121], v[44:45], v[12:13]
	v_pk_fma_f32 v[42:43], v[122:123], v[42:43], v[10:11]
	global_store_dwordx2 v[84:85], v[82:83], off
	v_cvt_pk_bf16_f32 v82, v38, v39
	v_cvt_pk_bf16_f32 v83, v40, v41
	v_pk_fma_f32 v[48:49], v[124:125], v[48:49], v[16:17]
	v_pk_fma_f32 v[46:47], v[126:127], v[46:47], v[14:15]
	global_store_dwordx2 v[84:85], v[82:83], off offset:512
	v_cvt_pk_bf16_f32 v82, v42, v43
	v_cvt_pk_bf16_f32 v83, v44, v45
	global_store_dwordx2 v[84:85], v[82:83], off offset:1024
	v_cvt_pk_bf16_f32 v82, v46, v47
	v_cvt_pk_bf16_f32 v83, v48, v49
	global_store_dwordx2 v[84:85], v[82:83], off offset:1536
	v_pk_mul_f32 v[60:61], v[60:61], v[86:87] op_sel_hi:[1,0]
	v_cvt_pk_bf16_f32 v82, v50, v51
	v_cvt_pk_bf16_f32 v83, v52, v53
	v_lshl_add_u64 v[84:85], v[102:103], 0, s[18:19]
	v_pk_fma_f32 v[60:61], v[120:121], v[60:61], v[12:13]
	v_pk_fma_f32 v[58:59], v[122:123], v[58:59], v[10:11]
	v_pk_mul_f32 v[62:63], v[62:63], v[86:87] op_sel_hi:[1,0]
	v_pk_mul_f32 v[64:65], v[64:65], v[86:87] op_sel_hi:[1,0]
	global_store_dwordx2 v[84:85], v[82:83], off
	v_cvt_pk_bf16_f32 v82, v54, v55
	v_cvt_pk_bf16_f32 v83, v56, v57
	v_pk_fma_f32 v[64:65], v[124:125], v[64:65], v[16:17]
	v_pk_fma_f32 v[62:63], v[126:127], v[62:63], v[14:15]
	global_store_dwordx2 v[84:85], v[82:83], off offset:512
	v_cvt_pk_bf16_f32 v82, v58, v59
	v_cvt_pk_bf16_f32 v83, v60, v61
	v_pk_mul_f32 v[66:67], v[66:67], v[88:89] op_sel_hi:[1,0]
	v_pk_mul_f32 v[68:69], v[68:69], v[88:89] op_sel_hi:[1,0]
	global_store_dwordx2 v[84:85], v[82:83], off offset:1024
	v_cvt_pk_bf16_f32 v82, v62, v63
	v_cvt_pk_bf16_f32 v83, v64, v65
	v_pk_fma_f32 v[68:69], v[112:113], v[68:69], v[4:5]
	v_pk_fma_f32 v[66:67], v[114:115], v[66:67], v[2:3]
	v_pk_mul_f32 v[70:71], v[70:71], v[88:89] op_sel_hi:[1,0]
	v_pk_mul_f32 v[72:73], v[72:73], v[88:89] op_sel_hi:[1,0]
	global_store_dwordx2 v[84:85], v[82:83], off offset:1536
	v_pk_fma_f32 v[72:73], v[116:117], v[72:73], v[8:9]
	v_pk_fma_f32 v[70:71], v[118:119], v[70:71], v[6:7]
	v_pk_mul_f32 v[74:75], v[74:75], v[88:89] op_sel_hi:[1,0]
	v_pk_mul_f32 v[76:77], v[76:77], v[88:89] op_sel_hi:[1,0]
	v_cvt_pk_bf16_f32 v82, v66, v67
	v_cvt_pk_bf16_f32 v83, v68, v69
	v_lshl_add_u64 v[84:85], v[102:103], 0, s[20:21]
	v_pk_fma_f32 v[76:77], v[120:121], v[76:77], v[12:13]
	v_pk_fma_f32 v[74:75], v[122:123], v[74:75], v[10:11]
	v_pk_mul_f32 v[78:79], v[78:79], v[88:89] op_sel_hi:[1,0]
	v_pk_mul_f32 v[80:81], v[80:81], v[88:89] op_sel_hi:[1,0]
	global_store_dwordx2 v[84:85], v[82:83], off
	v_cvt_pk_bf16_f32 v82, v70, v71
	v_cvt_pk_bf16_f32 v83, v72, v73
	v_pk_fma_f32 v[80:81], v[124:125], v[80:81], v[16:17]
	v_pk_fma_f32 v[78:79], v[126:127], v[78:79], v[14:15]
	global_store_dwordx2 v[84:85], v[82:83], off offset:512
	v_cvt_pk_bf16_f32 v82, v74, v75
	v_cvt_pk_bf16_f32 v83, v76, v77
	global_store_dwordx2 v[84:85], v[82:83], off offset:1024
	v_cvt_pk_bf16_f32 v82, v78, v79
	v_cvt_pk_bf16_f32 v83, v80, v81
	global_store_dwordx2 v[84:85], v[82:83], off offset:1536
	s_cbranch_vccnz .LBB0_830
	s_mov_b64 s[0:1], 0
	s_branch .LBB0_834

; #define LAS __attribute__((address_space(3)))
; template <bool BF> __device__ __forceinline__ unsigned pk16(float lo, float hi) { return BF ? pkb(lo, hi) : pkh(lo, hi); }
; template <bool BF, class RowMap>
; __device__ __forceinline__ void cvt_block(const float* W, int K, int N, f16* WT, const RowMap& rm, int item, int tid, LAS unsigned char* S) {
;     const int lane = tid & 63, wave = tid >> 6;
;     const int nblk = N / 128, kb = item / nblk, nb = item % nblk, k0 = 256 * kb, n0 = 128 * nb;
;     const float* src = W + (size_t)(k0 + 32 * wave + (lane >> 5)) * N + n0 + 4 * (lane & 31);
;     f32x4 v[16];
; #pragma unroll
;     for (int i = 0; i < 16; ++i) v[i] = *(const f32x4*)(src + (size_t)(2 * i) * N);
; #pragma unroll
;     for (int i = 0; i < 16; ++i) { u32x2 w; w.x = pk16<BF>(v[i][0], v[i][1]); w.y = pk16<BF>(v[i][2], v[i][3]);
;         *(LAS u32x2*)(S + (32 * wave + 2 * i + (lane >> 5)) * CVB_RS + 8 * (lane & 31)) = w; }
;     __syncthreads();
; __device__ __forceinline__ void cvt_moe(const float* w1, const float* w3, const float* w2, f16* W13, f16* W2T, int tid, LAS unsigned char* S) {
;     constexpr int I13 = (DM / 256) * (DE / 128), I2 = (DE / 256) * (DM / 128);
;     constexpr int NIT = NE * (2 * I13 + I2);
;     for (int it = blockIdx.x; it < NIT; it += gridDim.x) {
;         const int e = it / (2 * I13 + I2); int r = it % (2 * I13 + I2);
;         if (r < I13) { cvt_block<MOE_BF16>(w1 + (size_t)e * DM * DE, DM, DE, W13 + (size_t)e * 2 * DE * DM, MapGLU{0}, r, tid, S); continue; } r -= I13;
;         if (r < I13) { cvt_block<MOE_BF16>(w3 + (size_t)e * DM * DE, DM, DE, W13 + (size_t)e * 2 * DE * DM, MapGLU{128}, r, tid, S); continue; } r -= I13;
;         cvt_block<MOE_BF16>(w2 + (size_t)e * DE * DM, DE, DM, W2T + (size_t)e * DM * DE, MapPlain{}, r, tid, S);
.LBB0_1209:
	s_mul_hi_i32 s0, s35, 0x3e0f83e1
	s_lshr_b32 s2, s0, 31
	s_ashr_i32 s37, s0, 6
	s_add_i32 s37, s37, s2
	s_mul_i32 s0, s37, 0xfffffef8
	s_add_i32 s36, s35, s0
	s_cmpk_gt_i32 s36, 0x57
	s_mov_b64 s[2:3], -1
	s_cbranch_scc0 .LBB0_1215
	s_cmpk_gt_u32 s36, 0xaf
	s_cbranch_scc0 .LBB0_1212
	v_readlane_b32 s40, v251, 0
	s_mul_i32 s2, s37, 0xb00000
	v_readlane_b32 s44, v251, 4
	s_mul_hi_i32 s0, s37, 0xb00000
	v_readlane_b32 s41, v251, 1
	v_readlane_b32 s45, v251, 5
	s_add_u32 s40, s44, s2
	s_addc_u32 s41, s45, s0
	s_mul_i32 s2, s37, 0x580000
	s_mul_hi_i32 s0, s37, 0x580000
	s_add_u32 s3, s78, s2
	v_readlane_b32 s2, v250, 16
	s_addc_u32 s38, s2, s0
	s_lshl_b32 s0, s37, 8
	s_sub_i32 s0, s6, s0
	s_and_b32 s39, s0, 0xf00
	v_or_b32_e32 v5, s39, v1
	s_and_b32 s2, s4, 0x380
	v_lshlrev_b32_e32 v22, 12, v5
	v_mov_b32_e32 v23, v3
	v_lshl_add_u64 v[22:23], s[40:41], 0, v[22:23]
	s_lshl_b32 s0, s2, 2
	v_lshl_add_u64 v[22:23], v[22:23], 0, s[0:1]
	v_lshl_add_u64 v[82:83], v[22:23], 0, v[2:3]
	s_movk_i32 s0, 0x2000
	v_add_co_u32_e32 v26, vcc, s0, v82
	s_movk_i32 s0, 0x4000
	s_nop 0
	v_addc_co_u32_e32 v27, vcc, 0, v83, vcc
	v_add_co_u32_e32 v30, vcc, s0, v82
	s_movk_i32 s0, 0x6000
	s_nop 0
	v_addc_co_u32_e32 v31, vcc, 0, v83, vcc
	v_add_co_u32_e32 v34, vcc, s0, v82
	s_mov_b32 s0, 0x8000
	s_nop 0
	v_addc_co_u32_e32 v35, vcc, 0, v83, vcc
	v_add_co_u32_e32 v38, vcc, s0, v82
	global_load_dwordx4 v[22:25], v[82:83], off nt
	s_nop 0
	global_load_dwordx4 v[26:29], v[26:27], off nt
	v_addc_co_u32_e32 v39, vcc, 0, v83, vcc
	v_add_co_u32_e32 v42, vcc, s10, v82
	global_load_dwordx4 v[30:33], v[30:31], off nt
	s_nop 0
	global_load_dwordx4 v[34:37], v[34:35], off nt
	v_addc_co_u32_e32 v43, vcc, 0, v83, vcc
	v_add_co_u32_e32 v46, vcc, s11, v82
	global_load_dwordx4 v[38:41], v[38:39], off nt
	s_nop 0
	global_load_dwordx4 v[42:45], v[42:43], off nt
	v_addc_co_u32_e32 v47, vcc, 0, v83, vcc
	v_add_co_u32_e32 v50, vcc, s12, v82
	s_lshl_b32 s0, s39, 1
	s_nop 0
	v_addc_co_u32_e32 v51, vcc, 0, v83, vcc
	v_add_co_u32_e32 v54, vcc, s13, v82
	global_load_dwordx4 v[46:49], v[46:47], off nt
	s_nop 0
	global_load_dwordx4 v[50:53], v[50:51], off nt
	v_addc_co_u32_e32 v55, vcc, 0, v83, vcc
	v_add_co_u32_e32 v58, vcc, s14, v82
	s_add_u32 s40, s3, s0
	s_nop 0
	v_addc_co_u32_e32 v59, vcc, 0, v83, vcc
	v_add_co_u32_e32 v62, vcc, s15, v82
	global_load_dwordx4 v[54:57], v[54:55], off nt
	s_nop 0
	global_load_dwordx4 v[58:61], v[58:59], off nt
	v_addc_co_u32_e32 v63, vcc, 0, v83, vcc
	v_add_co_u32_e32 v66, vcc, s16, v82
	s_addc_u32 s41, s38, 0
	s_nop 0
	v_addc_co_u32_e32 v67, vcc, 0, v83, vcc
	v_add_co_u32_e32 v70, vcc, s17, v82
	global_load_dwordx4 v[62:65], v[62:63], off nt
	s_nop 0
	global_load_dwordx4 v[66:69], v[66:67], off nt
	v_addc_co_u32_e32 v71, vcc, 0, v83, vcc
	v_add_co_u32_e32 v74, vcc, s18, v82
	v_mov_b32_e32 v5, v3
	s_nop 0
	v_addc_co_u32_e32 v75, vcc, 0, v83, vcc
	v_add_co_u32_e32 v78, vcc, s19, v82
	global_load_dwordx4 v[70:73], v[70:71], off nt
	s_nop 0
	global_load_dwordx4 v[74:77], v[74:75], off nt
	v_addc_co_u32_e32 v79, vcc, 0, v83, vcc
	v_add_co_u32_e32 v82, vcc, s20, v82
	global_load_dwordx4 v[78:81], v[78:79], off nt
	s_nop 0
	v_addc_co_u32_e32 v83, vcc, 0, v83, vcc
	global_load_dwordx4 v[82:85], v[82:83], off nt
	v_readlane_b32 s42, v251, 2
	v_readlane_b32 s43, v251, 3
	v_readlane_b32 s46, v251, 6
	v_readlane_b32 s47, v251, 7
	s_waitcnt vmcnt(15)
	v_cvt_pk_bf16_f32 v22, v22, v23
	v_cvt_pk_bf16_f32 v23, v24, v25
	s_waitcnt vmcnt(14)
	v_cvt_pk_bf16_f32 v24, v26, v27
	v_cvt_pk_bf16_f32 v25, v28, v29
	ds_write2_b64 v14, v[22:23], v[24:25] offset1:66
	s_waitcnt vmcnt(13)
	v_cvt_pk_bf16_f32 v22, v30, v31
	v_cvt_pk_bf16_f32 v23, v32, v33
	s_waitcnt vmcnt(12)
	v_cvt_pk_bf16_f32 v24, v34, v35
	v_cvt_pk_bf16_f32 v25, v36, v37
	ds_write2_b64 v14, v[22:23], v[24:25] offset0:132 offset1:198
	s_waitcnt vmcnt(11)
	v_cvt_pk_bf16_f32 v22, v38, v39
	v_cvt_pk_bf16_f32 v23, v40, v41
	s_waitcnt vmcnt(10)
	v_cvt_pk_bf16_f32 v24, v42, v43
	v_cvt_pk_bf16_f32 v25, v44, v45
	ds_write2_b64 v18, v[22:23], v[24:25] offset0:8 offset1:74
	s_waitcnt vmcnt(9)
	v_cvt_pk_bf16_f32 v22, v46, v47
	v_cvt_pk_bf16_f32 v23, v48, v49
	s_waitcnt vmcnt(8)
	v_cvt_pk_bf16_f32 v24, v50, v51
	v_cvt_pk_bf16_f32 v25, v52, v53
	ds_write2_b64 v18, v[22:23], v[24:25] offset0:140 offset1:206
	s_waitcnt vmcnt(7)
	v_cvt_pk_bf16_f32 v22, v54, v55
	v_cvt_pk_bf16_f32 v23, v56, v57
	s_waitcnt vmcnt(6)
	v_cvt_pk_bf16_f32 v24, v58, v59
	v_cvt_pk_bf16_f32 v25, v60, v61
	ds_write2_b64 v19, v[22:23], v[24:25] offset0:16 offset1:82
	s_waitcnt vmcnt(5)
	v_cvt_pk_bf16_f32 v22, v62, v63
	v_cvt_pk_bf16_f32 v23, v64, v65
	s_waitcnt vmcnt(4)
	v_cvt_pk_bf16_f32 v24, v66, v67
	v_cvt_pk_bf16_f32 v25, v68, v69
	ds_write2_b64 v19, v[22:23], v[24:25] offset0:148 offset1:214
	s_waitcnt vmcnt(3)
	v_cvt_pk_bf16_f32 v22, v70, v71
	v_cvt_pk_bf16_f32 v23, v72, v73
	s_waitcnt vmcnt(2)
	v_cvt_pk_bf16_f32 v24, v74, v75
	v_cvt_pk_bf16_f32 v25, v76, v77
	ds_write2_b64 v20, v[22:23], v[24:25] offset0:24 offset1:90
	s_waitcnt vmcnt(1)
	v_cvt_pk_bf16_f32 v22, v78, v79
	v_cvt_pk_bf16_f32 v23, v80, v81
	s_waitcnt vmcnt(0)
	v_cvt_pk_bf16_f32 v24, v82, v83
	v_cvt_pk_bf16_f32 v25, v84, v85
	ds_write2_b64 v20, v[22:23], v[24:25] offset0:156 offset1:222
	s_waitcnt lgkmcnt(0)
	s_barrier
; #define LAS __attribute__((address_space(3)))
; #define LDS_WAIT() asm volatile("s_waitcnt lgkmcnt(0)" ::: "memory")
; template <bool BF, class RowMap>
; __device__ __forceinline__ void cvt_block(const float* W, int K, int N, f16* WT, const RowMap& rm, int item, int tid, LAS unsigned char* S) {
;     ...
;     const int g = lane >> 4, i16 = lane & 15, q_ = i16 >> 2, p_ = i16 & 3;
;     LAS unsigned char* T = S;
;     u32x4 wv[8];
; #pragma unroll
;     for (int st = 0; st < 8; ++st) {
;         const int ch = 4 * st + g;
;         const LAS unsigned char* ap = S + (8 * ch + q_) * CVB_RS + (16 * wave + 4 * p_) * 2;
;         const s16x4 lo = __builtin_amdgcn_ds_read_tr16_b64_v4i16((LAS s16x4*)ap);
;         const s16x4 hi = __builtin_amdgcn_ds_read_tr16_b64_v4i16((LAS s16x4*)(ap + 4 * CVB_RS));
;         const u32x2 l2 = __builtin_bit_cast(u32x2, lo), h2 = __builtin_bit_cast(u32x2, hi); wv[st].x = l2.x; wv[st].y = l2.y; wv[st].z = h2.x; wv[st].w = h2.y;
;     }
;     __syncthreads();
; #pragma unroll
;     for (int st = 0; st < 8; ++st) *(LAS u32x4*)(T + (16 * wave + i16) * CVT_TS + 16 * (4 * st + g)) = wv[st];
;     LDS_WAIT();
; #pragma unroll
;     for (int j = 0; j < 8; ++j) { const int nr = 16 * wave + 2 * j + (lane >> 5), ch = lane & 31;
;         const u32x4 w = *(const LAS u32x4*)(T + nr * CVT_TS + 16 * ch);
;         *(u32x4*)(WT + (size_t)rm(n0 + nr) * K + k0 + 8 * ch) = w; }
; __device__ __forceinline__ void cvt_moe(const float* w1, const float* w3, const float* w2, f16* W13, f16* W2T, int tid, LAS unsigned char* S) {
;     ...
;         const int e = it / (2 * I13 + I2); int r = it % (2 * I13 + I2);
;         if (r < I13) { cvt_block<MOE_BF16>(w1 + (size_t)e * DM * DE, DM, DE, W13 + (size_t)e * 2 * DE * DM, MapGLU{0}, r, tid, S); continue; } r -= I13;
;         if (r < I13) { cvt_block<MOE_BF16>(w3 + (size_t)e * DM * DE, DM, DE, W13 + (size_t)e * 2 * DE * DM, MapGLU{128}, r, tid, S); continue; } r -= I13;
	ds_read_b64_tr_b16 v[22:23], v15
	ds_read_b64_tr_b16 v[24:25], v15 offset:1056
	ds_read_b64_tr_b16 v[26:27], v15 offset:8448
	ds_read_b64_tr_b16 v[28:29], v15 offset:9504
	ds_read_b64_tr_b16 v[30:31], v15 offset:16896
	ds_read_b64_tr_b16 v[32:33], v15 offset:17952
	ds_read_b64_tr_b16 v[34:35], v15 offset:25344
	ds_read_b64_tr_b16 v[36:37], v15 offset:26400
	ds_read_b64_tr_b16 v[38:39], v15 offset:33792
	ds_read_b64_tr_b16 v[40:41], v15 offset:34848
	ds_read_b64_tr_b16 v[42:43], v15 offset:42240
	ds_read_b64_tr_b16 v[44:45], v15 offset:43296
	ds_read_b64_tr_b16 v[46:47], v15 offset:50688
	ds_read_b64_tr_b16 v[48:49], v15 offset:51744
	ds_read_b64_tr_b16 v[50:51], v15 offset:59136
	ds_read_b64_tr_b16 v[52:53], v15 offset:60192
	s_waitcnt lgkmcnt(0)
	s_barrier
	ds_write_b128 v16, v[22:25]
	ds_write_b128 v16, v[26:29] offset:64
	ds_write_b128 v16, v[30:33] offset:128
	ds_write_b128 v16, v[34:37] offset:192
	ds_write_b128 v16, v[38:41] offset:256
	ds_write_b128 v16, v[42:45] offset:320
	ds_write_b128 v16, v[46:49] offset:384
	ds_write_b128 v16, v[50:53] offset:448
	s_waitcnt lgkmcnt(0)
	v_lshl_add_u64 v[30:31], s[40:41], 0, v[4:5]
	ds_read_b128 v[22:25], v17
	v_or_b32_e32 v5, s2, v6
	v_mul_u32_u24_e32 v26, 0x1600, v5
	v_mov_b32_e32 v27, v3
	v_lshl_add_u64 v[32:33], v[30:31], 0, v[26:27]
	ds_read_b128 v[26:29], v17 offset:1056
	v_or_b32_e32 v5, s2, v7
	s_waitcnt lgkmcnt(1)
	global_store_dwordx4 v[32:33], v[22:25], off nt
	s_nop 1
	v_mul_u32_u24_e32 v22, 0x1600, v5
	v_mov_b32_e32 v23, v3
	v_lshl_add_u64 v[22:23], v[30:31], 0, v[22:23]
	s_waitcnt lgkmcnt(0)
	global_store_dwordx4 v[22:23], v[26:29], off nt
	ds_read_b128 v[22:25], v17 offset:2112
	v_or_b32_e32 v5, s2, v8
	v_mul_u32_u24_e32 v26, 0x1600, v5
	v_mov_b32_e32 v27, v3
	v_lshl_add_u64 v[32:33], v[30:31], 0, v[26:27]
	ds_read_b128 v[26:29], v17 offset:3168
	v_or_b32_e32 v5, s2, v9
	s_waitcnt lgkmcnt(1)
	global_store_dwordx4 v[32:33], v[22:25], off nt
	s_nop 1
	v_mul_u32_u24_e32 v22, 0x1600, v5
	v_mov_b32_e32 v23, v3
	v_lshl_add_u64 v[22:23], v[30:31], 0, v[22:23]
	s_waitcnt lgkmcnt(0)
	global_store_dwordx4 v[22:23], v[26:29], off nt
	ds_read_b128 v[22:25], v17 offset:4224
	v_or_b32_e32 v5, s2, v10
	v_mul_u32_u24_e32 v26, 0x1600, v5
	v_mov_b32_e32 v27, v3
	v_lshl_add_u64 v[32:33], v[30:31], 0, v[26:27]
	ds_read_b128 v[26:29], v17 offset:5280
	v_or_b32_e32 v5, s2, v11
	s_waitcnt lgkmcnt(1)
	global_store_dwordx4 v[32:33], v[22:25], off nt
	s_nop 1
	v_mul_u32_u24_e32 v22, 0x1600, v5
	v_mov_b32_e32 v23, v3
	v_lshl_add_u64 v[22:23], v[30:31], 0, v[22:23]
	s_waitcnt lgkmcnt(0)
	global_store_dwordx4 v[22:23], v[26:29], off nt
	ds_read_b128 v[22:25], v17 offset:6336
	v_or_b32_e32 v5, s2, v12
	v_mul_u32_u24_e32 v26, 0x1600, v5
	v_mov_b32_e32 v27, v3
	v_lshl_add_u64 v[32:33], v[30:31], 0, v[26:27]
	ds_read_b128 v[26:29], v17 offset:7392
	v_or_b32_e32 v5, s2, v13
	s_waitcnt lgkmcnt(1)
	global_store_dwordx4 v[32:33], v[22:25], off nt
	s_mov_b64 s[2:3], 0
	s_nop 0
	v_mul_u32_u24_e32 v22, 0x1600, v5
	v_mov_b32_e32 v23, v3
	v_lshl_add_u64 v[22:23], v[30:31], 0, v[22:23]
	s_waitcnt lgkmcnt(0)
	global_store_dwordx4 v[22:23], v[26:29], off nt
	s_barrier
.LBB0_1212:
	s_andn2_b64 vcc, exec, s[2:3]
	s_cbranch_vccnz .LBB0_1214
	v_readlane_b32 s40, v251, 0
	s_mul_i32 s2, s37, 0xb00000
	v_readlane_b32 s42, v251, 2
	s_mul_hi_i32 s0, s37, 0xb00000
	v_readlane_b32 s41, v251, 1
	v_readlane_b32 s43, v251, 3
	s_add_u32 s40, s42, s2
	s_addc_u32 s41, s43, s0
	s_add_u32 s3, s84, s2
	s_addc_u32 s38, s85, s0
	s_add_i32 s0, s36, 0xffa8
	s_bfe_u32 s2, s0, 0x70001
	s_mulk_i32 s2, 0xbb
	s_bfe_u32 s39, s2, 0x5000b
	s_mul_i32 s2, s39, 22
	s_sub_i32 s2, s0, s2
	v_lshl_or_b32 v5, s39, 8, v1
	s_and_b32 s0, s2, 0xff
	v_mul_u32_u24_e32 v22, 0x2c00, v5
	v_mov_b32_e32 v23, v3
	v_lshl_add_u64 v[22:23], s[40:41], 0, v[22:23]
	s_lshl_b32 s0, s0, 9
	v_lshl_add_u64 v[22:23], v[22:23], 0, s[0:1]
	v_lshl_add_u64 v[82:83], v[22:23], 0, v[2:3]
	v_add_co_u32_e32 v26, vcc, s21, v82
	s_lshl_b32 s0, s39, 9
	s_nop 0
	v_addc_co_u32_e32 v27, vcc, 0, v83, vcc
	v_add_co_u32_e32 v30, vcc, s22, v82
	global_load_dwordx4 v[22:25], v[82:83], off nt
	s_nop 0
	global_load_dwordx4 v[26:29], v[26:27], off offset:2048 nt
	v_addc_co_u32_e32 v31, vcc, 0, v83, vcc
	v_add_co_u32_e32 v34, vcc, s13, v82
	s_add_u32 s40, s3, s0
	s_nop 0
	v_addc_co_u32_e32 v35, vcc, 0, v83, vcc
	v_add_co_u32_e32 v38, vcc, s16, v82
	global_load_dwordx4 v[30:33], v[30:31], off nt
	s_nop 0
	global_load_dwordx4 v[34:37], v[34:35], off offset:2048 nt
	v_addc_co_u32_e32 v39, vcc, 0, v83, vcc
	v_add_co_u32_e32 v42, vcc, s23, v82
	s_addc_u32 s41, s38, 0
	s_nop 0
	v_addc_co_u32_e32 v43, vcc, 0, v83, vcc
	v_add_co_u32_e32 v46, vcc, s24, v82
	global_load_dwordx4 v[38:41], v[38:39], off nt
	s_nop 0
	global_load_dwordx4 v[42:45], v[42:43], off offset:2048 nt
	v_addc_co_u32_e32 v47, vcc, 0, v83, vcc
	v_add_co_u32_e32 v50, vcc, s25, v82
	s_lshl_b32 s0, s2, 8
	s_nop 0
	v_addc_co_u32_e32 v51, vcc, 0, v83, vcc
	v_add_co_u32_e32 v54, vcc, s26, v82
	global_load_dwordx4 v[46:49], v[46:47], off nt
	s_nop 0
	global_load_dwordx4 v[50:53], v[50:51], off offset:2048 nt
	v_addc_co_u32_e32 v55, vcc, 0, v83, vcc
	v_add_co_u32_e32 v58, vcc, s27, v82
	v_mov_b32_e32 v5, v3
	s_nop 0
	v_addc_co_u32_e32 v59, vcc, 0, v83, vcc
	v_add_co_u32_e32 v62, vcc, s28, v82
	global_load_dwordx4 v[54:57], v[54:55], off nt
	s_nop 0
	global_load_dwordx4 v[58:61], v[58:59], off offset:2048 nt
	v_addc_co_u32_e32 v63, vcc, 0, v83, vcc
	v_add_co_u32_e32 v66, vcc, s29, v82
	s_and_b32 s0, s0, 0x3f00
	s_nop 0
	v_addc_co_u32_e32 v67, vcc, 0, v83, vcc
	v_add_co_u32_e32 v70, vcc, s30, v82
	global_load_dwordx4 v[62:65], v[62:63], off nt
	s_nop 0
	global_load_dwordx4 v[66:69], v[66:67], off offset:2048 nt
	v_addc_co_u32_e32 v71, vcc, 0, v83, vcc
	v_add_co_u32_e32 v74, vcc, s31, v82
	v_readlane_b32 s44, v251, 4
	s_nop 0
	v_addc_co_u32_e32 v75, vcc, 0, v83, vcc
	v_add_co_u32_e32 v78, vcc, s33, v82
	global_load_dwordx4 v[70:73], v[70:71], off nt
	s_nop 0
	global_load_dwordx4 v[74:77], v[74:75], off offset:2048 nt
	v_addc_co_u32_e32 v79, vcc, 0, v83, vcc
	v_add_co_u32_e32 v82, vcc, s34, v82
	global_load_dwordx4 v[78:81], v[78:79], off nt
	s_nop 0
	v_addc_co_u32_e32 v83, vcc, 0, v83, vcc
	global_load_dwordx4 v[82:85], v[82:83], off offset:2048 nt
	v_readlane_b32 s45, v251, 5
	v_readlane_b32 s46, v251, 6
	v_readlane_b32 s47, v251, 7
	s_waitcnt vmcnt(15)
; #define LAS __attribute__((address_space(3)))
; #define LDS_WAIT() asm volatile("s_waitcnt lgkmcnt(0)" ::: "memory")
; template <bool BF> __device__ __forceinline__ unsigned pk16(float lo, float hi) { return BF ? pkb(lo, hi) : pkh(lo, hi); }
; template <bool BF, class RowMap>
; __device__ __forceinline__ void cvt_block(const float* W, int K, int N, f16* WT, const RowMap& rm, int item, int tid, LAS unsigned char* S) {
;     ...
;     for (int i = 0; i < 16; ++i) { u32x2 w; w.x = pk16<BF>(v[i][0], v[i][1]); w.y = pk16<BF>(v[i][2], v[i][3]);
;         *(LAS u32x2*)(S + (32 * wave + 2 * i + (lane >> 5)) * CVB_RS + 8 * (lane & 31)) = w; }
;     __syncthreads();
;     const int g = lane >> 4, i16 = lane & 15, q_ = i16 >> 2, p_ = i16 & 3;
;     LAS unsigned char* T = S;
;     u32x4 wv[8];
; #pragma unroll
;     for (int st = 0; st < 8; ++st) {
;         const int ch = 4 * st + g;
;         const LAS unsigned char* ap = S + (8 * ch + q_) * CVB_RS + (16 * wave + 4 * p_) * 2;
;         const s16x4 lo = __builtin_amdgcn_ds_read_tr16_b64_v4i16((LAS s16x4*)ap);
;         const s16x4 hi = __builtin_amdgcn_ds_read_tr16_b64_v4i16((LAS s16x4*)(ap + 4 * CVB_RS));
;         const u32x2 l2 = __builtin_bit_cast(u32x2, lo), h2 = __builtin_bit_cast(u32x2, hi); wv[st].x = l2.x; wv[st].y = l2.y; wv[st].z = h2.x; wv[st].w = h2.y;
;     }
;     __syncthreads();
; #pragma unroll
;     for (int st = 0; st < 8; ++st) *(LAS u32x4*)(T + (16 * wave + i16) * CVT_TS + 16 * (4 * st + g)) = wv[st];
;     LDS_WAIT();
; #pragma unroll
;     for (int j = 0; j < 8; ++j) { const int nr = 16 * wave + 2 * j + (lane >> 5), ch = lane & 31;
;         const u32x4 w = *(const LAS u32x4*)(T + nr * CVT_TS + 16 * ch);
;         *(u32x4*)(WT + (size_t)rm(n0 + nr) * K + k0 + 8 * ch) = w; }
	v_cvt_pk_bf16_f32 v22, v22, v23
	v_cvt_pk_bf16_f32 v23, v24, v25
	s_waitcnt vmcnt(14)
	v_cvt_pk_bf16_f32 v24, v26, v27
	v_cvt_pk_bf16_f32 v25, v28, v29
	ds_write2_b64 v14, v[22:23], v[24:25] offset1:66
	s_waitcnt vmcnt(13)
	v_cvt_pk_bf16_f32 v22, v30, v31
	v_cvt_pk_bf16_f32 v23, v32, v33
	s_waitcnt vmcnt(12)
	v_cvt_pk_bf16_f32 v24, v34, v35
	v_cvt_pk_bf16_f32 v25, v36, v37
	ds_write2_b64 v14, v[22:23], v[24:25] offset0:132 offset1:198
	s_waitcnt vmcnt(11)
	v_cvt_pk_bf16_f32 v22, v38, v39
	v_cvt_pk_bf16_f32 v23, v40, v41
	s_waitcnt vmcnt(10)
	v_cvt_pk_bf16_f32 v24, v42, v43
	v_cvt_pk_bf16_f32 v25, v44, v45
	ds_write2_b64 v18, v[22:23], v[24:25] offset0:8 offset1:74
	s_waitcnt vmcnt(9)
	v_cvt_pk_bf16_f32 v22, v46, v47
	v_cvt_pk_bf16_f32 v23, v48, v49
	s_waitcnt vmcnt(8)
	v_cvt_pk_bf16_f32 v24, v50, v51
	v_cvt_pk_bf16_f32 v25, v52, v53
	ds_write2_b64 v18, v[22:23], v[24:25] offset0:140 offset1:206
	s_waitcnt vmcnt(7)
	v_cvt_pk_bf16_f32 v22, v54, v55
	v_cvt_pk_bf16_f32 v23, v56, v57
	s_waitcnt vmcnt(6)
	v_cvt_pk_bf16_f32 v24, v58, v59
	v_cvt_pk_bf16_f32 v25, v60, v61
	ds_write2_b64 v19, v[22:23], v[24:25] offset0:16 offset1:82
	s_waitcnt vmcnt(5)
	v_cvt_pk_bf16_f32 v22, v62, v63
	v_cvt_pk_bf16_f32 v23, v64, v65
	s_waitcnt vmcnt(4)
	v_cvt_pk_bf16_f32 v24, v66, v67
	v_cvt_pk_bf16_f32 v25, v68, v69
	ds_write2_b64 v19, v[22:23], v[24:25] offset0:148 offset1:214
	s_waitcnt vmcnt(3)
	v_cvt_pk_bf16_f32 v22, v70, v71
	v_cvt_pk_bf16_f32 v23, v72, v73
	s_waitcnt vmcnt(2)
	v_cvt_pk_bf16_f32 v24, v74, v75
	v_cvt_pk_bf16_f32 v25, v76, v77
	ds_write2_b64 v20, v[22:23], v[24:25] offset0:24 offset1:90
	s_waitcnt vmcnt(1)
	v_cvt_pk_bf16_f32 v22, v78, v79
	v_cvt_pk_bf16_f32 v23, v80, v81
	s_waitcnt vmcnt(0)
	v_cvt_pk_bf16_f32 v24, v82, v83
	v_cvt_pk_bf16_f32 v25, v84, v85
	ds_write2_b64 v20, v[22:23], v[24:25] offset0:156 offset1:222
	s_waitcnt lgkmcnt(0)
	s_barrier
	ds_read_b64_tr_b16 v[22:23], v15
	ds_read_b64_tr_b16 v[24:25], v15 offset:1056
	ds_read_b64_tr_b16 v[26:27], v15 offset:8448
	ds_read_b64_tr_b16 v[28:29], v15 offset:9504
	ds_read_b64_tr_b16 v[30:31], v15 offset:16896
	ds_read_b64_tr_b16 v[32:33], v15 offset:17952
	ds_read_b64_tr_b16 v[34:35], v15 offset:25344
	ds_read_b64_tr_b16 v[36:37], v15 offset:26400
	ds_read_b64_tr_b16 v[38:39], v15 offset:33792
	ds_read_b64_tr_b16 v[40:41], v15 offset:34848
	ds_read_b64_tr_b16 v[42:43], v15 offset:42240
	ds_read_b64_tr_b16 v[44:45], v15 offset:43296
	ds_read_b64_tr_b16 v[46:47], v15 offset:50688
	ds_read_b64_tr_b16 v[48:49], v15 offset:51744
	ds_read_b64_tr_b16 v[50:51], v15 offset:59136
	ds_read_b64_tr_b16 v[52:53], v15 offset:60192
	s_waitcnt lgkmcnt(0)
	s_barrier
	ds_write_b128 v16, v[22:25]
	ds_write_b128 v16, v[26:29] offset:64
	ds_write_b128 v16, v[30:33] offset:128
	ds_write_b128 v16, v[34:37] offset:192
	ds_write_b128 v16, v[38:41] offset:256
	ds_write_b128 v16, v[42:45] offset:320
	ds_write_b128 v16, v[46:49] offset:384
	ds_write_b128 v16, v[50:53] offset:448
	s_waitcnt lgkmcnt(0)
	v_lshl_add_u64 v[30:31], s[40:41], 0, v[4:5]
	v_or_b32_e32 v5, s0, v6
	ds_read_b128 v[22:25], v17
	v_lshlrev_b32_e32 v5, 11, v5
	v_or_b32_e32 v26, 0x40000, v5
	v_mov_b32_e32 v27, v3
	v_lshl_add_u64 v[32:33], v[30:31], 0, v[26:27]
	ds_read_b128 v[26:29], v17 offset:1056
	s_waitcnt lgkmcnt(1)
	global_store_dwordx4 v[32:33], v[22:25], off nt
	s_nop 1
	v_or_b32_e32 v22, 0x41000, v5
	v_mov_b32_e32 v23, v3
	v_lshl_add_u64 v[22:23], v[30:31], 0, v[22:23]
	s_waitcnt lgkmcnt(0)
	global_store_dwordx4 v[22:23], v[26:29], off nt
	ds_read_b128 v[22:25], v17 offset:2112
	s_nop 0
	v_or_b32_e32 v26, 0x42000, v5
	v_mov_b32_e32 v27, v3
	v_lshl_add_u64 v[32:33], v[30:31], 0, v[26:27]
	ds_read_b128 v[26:29], v17 offset:3168
	s_waitcnt lgkmcnt(1)
	global_store_dwordx4 v[32:33], v[22:25], off nt
	s_nop 1
	v_or_b32_e32 v22, 0x43000, v5
	v_mov_b32_e32 v23, v3
	v_lshl_add_u64 v[22:23], v[30:31], 0, v[22:23]
	s_waitcnt lgkmcnt(0)
	global_store_dwordx4 v[22:23], v[26:29], off nt
	ds_read_b128 v[22:25], v17 offset:4224
	s_nop 0
	v_or_b32_e32 v26, 0x44000, v5
	v_mov_b32_e32 v27, v3
	v_lshl_add_u64 v[32:33], v[30:31], 0, v[26:27]
	ds_read_b128 v[26:29], v17 offset:5280
	s_waitcnt lgkmcnt(1)
	global_store_dwordx4 v[32:33], v[22:25], off nt
	s_nop 1
	v_or_b32_e32 v22, 0x45000, v5
	v_mov_b32_e32 v23, v3
	v_lshl_add_u64 v[22:23], v[30:31], 0, v[22:23]
	s_waitcnt lgkmcnt(0)
	global_store_dwordx4 v[22:23], v[26:29], off nt
	ds_read_b128 v[22:25], v17 offset:6336
	s_nop 0
	v_or_b32_e32 v26, 0x46000, v5
	v_mov_b32_e32 v27, v3
	v_lshl_add_u64 v[32:33], v[30:31], 0, v[26:27]
	ds_read_b128 v[26:29], v17 offset:7392
	s_waitcnt lgkmcnt(1)
	global_store_dwordx4 v[32:33], v[22:25], off nt
	s_nop 1
	v_or_b32_e32 v22, 0x47000, v5
	v_mov_b32_e32 v23, v3
	v_lshl_add_u64 v[22:23], v[30:31], 0, v[22:23]
	s_waitcnt lgkmcnt(0)
	global_store_dwordx4 v[22:23], v[26:29], off nt
	s_barrier

; #define LAS __attribute__((address_space(3)))
; template <bool BF> __device__ __forceinline__ unsigned pk16(float lo, float hi) { return BF ? pkb(lo, hi) : pkh(lo, hi); }
; template <bool BF, class RowMap>
; __device__ __forceinline__ void cvt_block(const float* W, int K, int N, f16* WT, const RowMap& rm, int item, int tid, LAS unsigned char* S) {
;     ...
;     const int nblk = N / 128, kb = item / nblk, nb = item % nblk, k0 = 256 * kb, n0 = 128 * nb;
;     const float* src = W + (size_t)(k0 + 32 * wave + (lane >> 5)) * N + n0 + 4 * (lane & 31);
;     f32x4 v[16];
; #pragma unroll
;     for (int i = 0; i < 16; ++i) v[i] = *(const f32x4*)(src + (size_t)(2 * i) * N);
; #pragma unroll
;     for (int i = 0; i < 16; ++i) { u32x2 w; w.x = pk16<BF>(v[i][0], v[i][1]); w.y = pk16<BF>(v[i][2], v[i][3]);
;         *(LAS u32x2*)(S + (32 * wave + 2 * i + (lane >> 5)) * CVB_RS + 8 * (lane & 31)) = w; }
;     __syncthreads();
; __device__ __forceinline__ void cvt_moe(const float* w1, const float* w3, const float* w2, f16* W13, f16* W2T, int tid, LAS unsigned char* S) {
;     ...
;         const int e = it / (2 * I13 + I2); int r = it % (2 * I13 + I2);
;         if (r < I13) { cvt_block<MOE_BF16>(w1 + (size_t)e * DM * DE, DM, DE, W13 + (size_t)e * 2 * DE * DM, MapGLU{0}, r, tid, S); continue; } r -= I13;
.LBB0_1215:
	s_andn2_b64 vcc, exec, s[2:3]
	s_cbranch_vccnz .LBB0_1208
	s_mul_hi_i32 s2, s37, 0xb00000
	s_mul_i32 s37, s37, 0xb00000
	v_readlane_b32 s40, v251, 0
	v_readlane_b32 s41, v251, 1
	s_add_u32 s38, s40, s37
	s_addc_u32 s39, s41, s2
	s_add_u32 s0, s84, s37
	s_addc_u32 s37, s85, s2
	s_mul_i32 s2, s36, 0xba3
	s_lshr_b32 s3, s2, 31
	s_lshr_b32 s2, s2, 16
	s_add_i32 s2, s2, s3
	s_sext_i32_i16 s3, s2
	s_mul_i32 s2, s2, 22
	s_sub_i32 s2, s36, s2
	s_sext_i32_i16 s36, s2
	s_lshl_b32 s2, s3, 8
	v_or_b32_e32 v5, s2, v1
	v_mul_i32_i24_e32 v22, 0x2c00, v5
	s_lshl_b32 s40, s36, 7
	v_ashrrev_i32_e32 v23, 31, v22
	v_lshl_add_u64 v[22:23], s[38:39], 0, v[22:23]
	s_ashr_i32 s41, s40, 31
	v_lshl_add_u64 v[22:23], s[40:41], 2, v[22:23]
	v_lshl_add_u64 v[82:83], v[22:23], 0, v[2:3]
	v_add_co_u32_e32 v26, vcc, s21, v82
	s_ashr_i32 s3, s2, 31
	s_nop 0
	v_addc_co_u32_e32 v27, vcc, 0, v83, vcc
	v_add_co_u32_e32 v30, vcc, s22, v82
	global_load_dwordx4 v[22:25], v[82:83], off nt
	s_nop 0
	global_load_dwordx4 v[26:29], v[26:27], off offset:2048 nt
	v_addc_co_u32_e32 v31, vcc, 0, v83, vcc
	v_add_co_u32_e32 v34, vcc, s13, v82
	s_lshl_b64 s[2:3], s[2:3], 1
	s_nop 0
	v_addc_co_u32_e32 v35, vcc, 0, v83, vcc
	v_add_co_u32_e32 v38, vcc, s16, v82
	global_load_dwordx4 v[30:33], v[30:31], off nt
	s_nop 0
	global_load_dwordx4 v[34:37], v[34:35], off offset:2048 nt
	v_addc_co_u32_e32 v39, vcc, 0, v83, vcc
	v_add_co_u32_e32 v42, vcc, s23, v82
	s_add_u32 s2, s0, s2
	s_nop 0
	v_addc_co_u32_e32 v43, vcc, 0, v83, vcc
	v_add_co_u32_e32 v46, vcc, s24, v82
	global_load_dwordx4 v[38:41], v[38:39], off nt
	s_nop 0
	global_load_dwordx4 v[42:45], v[42:43], off offset:2048 nt
	v_addc_co_u32_e32 v47, vcc, 0, v83, vcc
	v_add_co_u32_e32 v50, vcc, s25, v82
	s_addc_u32 s3, s37, s3
	s_nop 0
	v_addc_co_u32_e32 v51, vcc, 0, v83, vcc
	v_add_co_u32_e32 v54, vcc, s26, v82
	global_load_dwordx4 v[46:49], v[46:47], off nt
	s_nop 0
	global_load_dwordx4 v[50:53], v[50:51], off offset:2048 nt
	v_addc_co_u32_e32 v55, vcc, 0, v83, vcc
	v_add_co_u32_e32 v58, vcc, s27, v82
	s_lshl_b32 s0, s36, 8
	s_nop 0
	v_addc_co_u32_e32 v59, vcc, 0, v83, vcc
	v_add_co_u32_e32 v62, vcc, s28, v82
	global_load_dwordx4 v[54:57], v[54:55], off nt
	s_nop 0
	global_load_dwordx4 v[58:61], v[58:59], off offset:2048 nt
	v_addc_co_u32_e32 v63, vcc, 0, v83, vcc
	v_add_co_u32_e32 v66, vcc, s29, v82
	v_mov_b32_e32 v5, v3
	s_nop 0
	v_addc_co_u32_e32 v67, vcc, 0, v83, vcc
	v_add_co_u32_e32 v70, vcc, s30, v82
	global_load_dwordx4 v[62:65], v[62:63], off nt
	s_nop 0
	global_load_dwordx4 v[66:69], v[66:67], off offset:2048 nt
	v_addc_co_u32_e32 v71, vcc, 0, v83, vcc
	v_add_co_u32_e32 v74, vcc, s31, v82
	v_readlane_b32 s42, v251, 2
	s_nop 0
	v_addc_co_u32_e32 v75, vcc, 0, v83, vcc
	v_add_co_u32_e32 v78, vcc, s33, v82
	global_load_dwordx4 v[70:73], v[70:71], off nt
	s_nop 0
	global_load_dwordx4 v[74:77], v[74:75], off offset:2048 nt
	v_addc_co_u32_e32 v79, vcc, 0, v83, vcc
	v_add_co_u32_e32 v82, vcc, s34, v82
	global_load_dwordx4 v[78:81], v[78:79], off nt
	s_nop 0
	v_addc_co_u32_e32 v83, vcc, 0, v83, vcc
	global_load_dwordx4 v[82:85], v[82:83], off offset:2048 nt
	v_readlane_b32 s43, v251, 3
	v_readlane_b32 s44, v251, 4
	v_readlane_b32 s45, v251, 5
	v_readlane_b32 s46, v251, 6
	v_readlane_b32 s47, v251, 7
	s_waitcnt vmcnt(15)
	v_cvt_pk_bf16_f32 v22, v22, v23
	v_cvt_pk_bf16_f32 v23, v24, v25
	s_waitcnt vmcnt(14)
	v_cvt_pk_bf16_f32 v24, v26, v27
	v_cvt_pk_bf16_f32 v25, v28, v29
	ds_write2_b64 v14, v[22:23], v[24:25] offset1:66
	s_waitcnt vmcnt(13)
	v_cvt_pk_bf16_f32 v22, v30, v31
	v_cvt_pk_bf16_f32 v23, v32, v33
	s_waitcnt vmcnt(12)
	v_cvt_pk_bf16_f32 v24, v34, v35
	v_cvt_pk_bf16_f32 v25, v36, v37
	ds_write2_b64 v14, v[22:23], v[24:25] offset0:132 offset1:198
	s_waitcnt vmcnt(11)
	v_cvt_pk_bf16_f32 v22, v38, v39
	v_cvt_pk_bf16_f32 v23, v40, v41
	s_waitcnt vmcnt(10)
	v_cvt_pk_bf16_f32 v24, v42, v43
	v_cvt_pk_bf16_f32 v25, v44, v45
	ds_write2_b64 v18, v[22:23], v[24:25] offset0:8 offset1:74
	s_waitcnt vmcnt(9)
	v_cvt_pk_bf16_f32 v22, v46, v47
	v_cvt_pk_bf16_f32 v23, v48, v49
	s_waitcnt vmcnt(8)
	v_cvt_pk_bf16_f32 v24, v50, v51
	v_cvt_pk_bf16_f32 v25, v52, v53
	ds_write2_b64 v18, v[22:23], v[24:25] offset0:140 offset1:206
	s_waitcnt vmcnt(7)
	v_cvt_pk_bf16_f32 v22, v54, v55
	v_cvt_pk_bf16_f32 v23, v56, v57
	s_waitcnt vmcnt(6)
	v_cvt_pk_bf16_f32 v24, v58, v59
	v_cvt_pk_bf16_f32 v25, v60, v61
	ds_write2_b64 v19, v[22:23], v[24:25] offset0:16 offset1:82
	s_waitcnt vmcnt(5)
	v_cvt_pk_bf16_f32 v22, v62, v63
	v_cvt_pk_bf16_f32 v23, v64, v65
	s_waitcnt vmcnt(4)
	v_cvt_pk_bf16_f32 v24, v66, v67
	v_cvt_pk_bf16_f32 v25, v68, v69
	ds_write2_b64 v19, v[22:23], v[24:25] offset0:148 offset1:214
	s_waitcnt vmcnt(3)
	v_cvt_pk_bf16_f32 v22, v70, v71
	v_cvt_pk_bf16_f32 v23, v72, v73
	s_waitcnt vmcnt(2)
	v_cvt_pk_bf16_f32 v24, v74, v75
	v_cvt_pk_bf16_f32 v25, v76, v77
	ds_write2_b64 v20, v[22:23], v[24:25] offset0:24 offset1:90
	s_waitcnt vmcnt(1)
	v_cvt_pk_bf16_f32 v22, v78, v79
	v_cvt_pk_bf16_f32 v23, v80, v81
	s_waitcnt vmcnt(0)
	v_cvt_pk_bf16_f32 v24, v82, v83
	v_cvt_pk_bf16_f32 v25, v84, v85
	ds_write2_b64 v20, v[22:23], v[24:25] offset0:156 offset1:222
	s_waitcnt lgkmcnt(0)
	s_barrier
; #define LAS __attribute__((address_space(3)))
; #define LDS_WAIT() asm volatile("s_waitcnt lgkmcnt(0)" ::: "memory")
; template <bool BF, class RowMap>
; __device__ __forceinline__ void cvt_block(const float* W, int K, int N, f16* WT, const RowMap& rm, int item, int tid, LAS unsigned char* S) {
;     ...
;     const int g = lane >> 4, i16 = lane & 15, q_ = i16 >> 2, p_ = i16 & 3;
;     LAS unsigned char* T = S;
;     u32x4 wv[8];
; #pragma unroll
;     for (int st = 0; st < 8; ++st) {
;         const int ch = 4 * st + g;
;         const LAS unsigned char* ap = S + (8 * ch + q_) * CVB_RS + (16 * wave + 4 * p_) * 2;
;         const s16x4 lo = __builtin_amdgcn_ds_read_tr16_b64_v4i16((LAS s16x4*)ap);
;         const s16x4 hi = __builtin_amdgcn_ds_read_tr16_b64_v4i16((LAS s16x4*)(ap + 4 * CVB_RS));
;         const u32x2 l2 = __builtin_bit_cast(u32x2, lo), h2 = __builtin_bit_cast(u32x2, hi); wv[st].x = l2.x; wv[st].y = l2.y; wv[st].z = h2.x; wv[st].w = h2.y;
;     }
;     __syncthreads();
; #pragma unroll
;     for (int st = 0; st < 8; ++st) *(LAS u32x4*)(T + (16 * wave + i16) * CVT_TS + 16 * (4 * st + g)) = wv[st];
;     LDS_WAIT();
; #pragma unroll
;     for (int j = 0; j < 8; ++j) { const int nr = 16 * wave + 2 * j + (lane >> 5), ch = lane & 31;
;         const u32x4 w = *(const LAS u32x4*)(T + nr * CVT_TS + 16 * ch);
;         *(u32x4*)(WT + (size_t)rm(n0 + nr) * K + k0 + 8 * ch) = w; }
	ds_read_b64_tr_b16 v[22:23], v15
	ds_read_b64_tr_b16 v[24:25], v15 offset:1056
	ds_read_b64_tr_b16 v[26:27], v15 offset:8448
	ds_read_b64_tr_b16 v[28:29], v15 offset:9504
	ds_read_b64_tr_b16 v[30:31], v15 offset:16896
	ds_read_b64_tr_b16 v[32:33], v15 offset:17952
	ds_read_b64_tr_b16 v[34:35], v15 offset:25344
	ds_read_b64_tr_b16 v[36:37], v15 offset:26400
	ds_read_b64_tr_b16 v[38:39], v15 offset:33792
	ds_read_b64_tr_b16 v[40:41], v15 offset:34848
	ds_read_b64_tr_b16 v[42:43], v15 offset:42240
	ds_read_b64_tr_b16 v[44:45], v15 offset:43296
	ds_read_b64_tr_b16 v[46:47], v15 offset:50688
	ds_read_b64_tr_b16 v[48:49], v15 offset:51744
	ds_read_b64_tr_b16 v[50:51], v15 offset:59136
	ds_read_b64_tr_b16 v[52:53], v15 offset:60192
	s_waitcnt lgkmcnt(0)
	s_barrier
	ds_write_b128 v16, v[22:25]
	ds_write_b128 v16, v[26:29] offset:64
	ds_write_b128 v16, v[30:33] offset:128
	ds_write_b128 v16, v[34:37] offset:192
	ds_write_b128 v16, v[38:41] offset:256
	ds_write_b128 v16, v[42:45] offset:320
	ds_write_b128 v16, v[46:49] offset:384
	ds_write_b128 v16, v[50:53] offset:448
	s_waitcnt lgkmcnt(0)
	ds_read_b128 v[22:25], v17
	v_or_b32_e32 v26, s0, v6
	v_ashrrev_i32_e32 v27, 31, v26
	v_lshl_add_u64 v[30:31], s[2:3], 0, v[4:5]
	v_lshlrev_b64 v[26:27], 11, v[26:27]
	v_lshl_add_u64 v[32:33], v[30:31], 0, v[26:27]
	ds_read_b128 v[26:29], v17 offset:1056
	s_waitcnt lgkmcnt(1)
	global_store_dwordx4 v[32:33], v[22:25], off nt
	s_nop 1
	v_or_b32_e32 v22, s0, v7
	v_ashrrev_i32_e32 v23, 31, v22
	v_lshlrev_b64 v[22:23], 11, v[22:23]
	v_lshl_add_u64 v[22:23], v[30:31], 0, v[22:23]
	s_waitcnt lgkmcnt(0)
	global_store_dwordx4 v[22:23], v[26:29], off nt
	ds_read_b128 v[22:25], v17 offset:2112
	s_nop 0
	v_or_b32_e32 v26, s0, v8
	v_ashrrev_i32_e32 v27, 31, v26
	v_lshlrev_b64 v[26:27], 11, v[26:27]
	v_lshl_add_u64 v[32:33], v[30:31], 0, v[26:27]
	ds_read_b128 v[26:29], v17 offset:3168
	s_waitcnt lgkmcnt(1)
	global_store_dwordx4 v[32:33], v[22:25], off nt
	s_nop 1
	v_or_b32_e32 v22, s0, v9
	v_ashrrev_i32_e32 v23, 31, v22
	v_lshlrev_b64 v[22:23], 11, v[22:23]
	v_lshl_add_u64 v[22:23], v[30:31], 0, v[22:23]
	s_waitcnt lgkmcnt(0)
	global_store_dwordx4 v[22:23], v[26:29], off nt
	ds_read_b128 v[22:25], v17 offset:4224
	s_nop 0
	v_or_b32_e32 v26, s0, v10
	v_ashrrev_i32_e32 v27, 31, v26
	v_lshlrev_b64 v[26:27], 11, v[26:27]
	v_lshl_add_u64 v[32:33], v[30:31], 0, v[26:27]
	ds_read_b128 v[26:29], v17 offset:5280
	s_waitcnt lgkmcnt(1)
	global_store_dwordx4 v[32:33], v[22:25], off nt
	s_nop 1
	v_or_b32_e32 v22, s0, v11
	v_ashrrev_i32_e32 v23, 31, v22
	v_lshlrev_b64 v[22:23], 11, v[22:23]
	v_lshl_add_u64 v[22:23], v[30:31], 0, v[22:23]
	s_waitcnt lgkmcnt(0)
	global_store_dwordx4 v[22:23], v[26:29], off nt
	ds_read_b128 v[22:25], v17 offset:6336
	s_nop 0
	v_or_b32_e32 v26, s0, v12
	v_ashrrev_i32_e32 v27, 31, v26
	v_lshlrev_b64 v[26:27], 11, v[26:27]
	v_lshl_add_u64 v[32:33], v[30:31], 0, v[26:27]
	ds_read_b128 v[26:29], v17 offset:7392
	s_waitcnt lgkmcnt(1)
	global_store_dwordx4 v[32:33], v[22:25], off nt
	s_nop 1
	v_or_b32_e32 v22, s0, v13
	v_ashrrev_i32_e32 v23, 31, v22
	v_lshlrev_b64 v[22:23], 11, v[22:23]
	v_lshl_add_u64 v[22:23], v[30:31], 0, v[22:23]
	s_waitcnt lgkmcnt(0)
	global_store_dwordx4 v[22:23], v[26:29], off nt
	s_barrier
	s_branch .LBB0_1208

; template <int R, bool RT = false>
; __device__ __forceinline__ void norm_phase(const NormArgs& a, LAS unsigned char* lds, bool ctx_rows, const float* ctx_src, const float* ctx_shift, const float* ctx_scale) {
;     ...
;         int ipk[4] = {-1, -1, -1, -1};
;         if (a.y2) {
; #pragma unroll
;             for (int i = 0; i < 4; ++i) ipk[i] = a.inv[((size_t)b * NE + (lane & 15)) * SEQ + ((row0 + 4 * i + (lane >> 4)) & (SEQ - 1))]; }
;         u32x2 xp[RT ? 4 : 1][4][3]; float rsel[4] = {0.f, 0.f, 0.f, 0.f};
;         LAS unsigned char* hs = wave < 7 ? lds + 65536 + wave * 8448 : lds + 132608;
; #pragma unroll (RT ? 4 : 1)
;         for (int rr = 0; rr < 16; rr += R) {
;             if constexpr (RT) asm volatile("" ::: "memory");
;             f32x4 v[R][4];
;             int sl[R];
; #pragma unroll
;             for (int q = 0; q < R; ++q) { sl[q] = -1; if (a.y2) { const int r = rr + q; const int pk = r < 4 ? ipk[0] : (r < 8 ? ipk[1] : (r < 12 ? ipk[2] : ipk[3]));
;                     const int got = __shfl(pk, (lane & 15) + 16 * (r & 3)); sl[q] = lane < 16 ? got : -1; } }
; #pragma unroll
;             for (int q = 0; q < R; ++q) { const int row = row0 + rr + q;
;                 if (a.src16) { const f16* xr = a.src16 + (size_t)row * DM;
; #pragma unroll
;                     for (int j = 0; j < 4; ++j) { const f16x4 t = *(const f16x4*)(xr + 4 * lane + 256 * j); v[q][j] = (f32x4){(float)t[0], (float)t[1], (float)t[2], (float)t[3]};
;                         if constexpr (RT) { if (j == 0) *(LAS u32x2*)(hs + (rr + q) * 528 + 8 * lane) = __builtin_bit_cast(u32x2, t);
;                             else xp[rr / 4][q][j - 1] = __builtin_bit_cast(u32x2, t); } } }
;                 else { const float* xr = a.src + (size_t)row * DM;
; #pragma unroll
;                     for (int j = 0; j < 4; ++j) v[q][j] = *(const f32x4*)(xr + 4 * lane + 256 * j); } }
;             if (a.y2) {
;                 unsigned long long mask[R]; int ee[R][4]; float wgt[R][4]; f16x4 ld[R][4][4];
;                 int cnt[R];
; #pragma unroll
;                 for (int q = 0; q < R; ++q) { mask[q] = __ballot(sl[q] >= 0); cnt[q] = __builtin_popcountll(mask[q]);
; #pragma unroll
;                     for (int i = 0; i < 4; ++i) { if (mask[q]) { ee[q][i] = __builtin_ctzll(mask[q]); mask[q] &= mask[q] - 1; wgt[q][i] = 1.f; } else { ee[q][i] = i ? ee[q][0] : 0; wgt[q][i] = 0.f; } }
.LBB0_1933:
	s_cmp_lt_u32 s38, 4
	s_cselect_b64 vcc, -1, 0
	s_cmp_lt_u32 s38, 8
	s_cselect_b64 s[2:3], -1, 0
	s_cmp_lt_u32 s38, 12
	s_cselect_b64 s[4:5], -1, 0
	s_or_b32 s12, s38, s35
	s_ashr_i32 s13, s12, 31
	s_waitcnt vmcnt(0)
	v_cndmask_b32_e64 v2, v163, v162, s[4:5]
	s_lshl_b64 s[4:5], s[12:13], 11
	v_lshl_add_u64 v[136:137], v[56:57], 0, s[4:5]
	s_or_b32 s4, s12, 1
	s_ashr_i32 s5, s4, 31
	s_lshl_b64 s[14:15], s[4:5], 11
	v_lshl_add_u64 v[126:127], v[56:57], 0, s[14:15]
	global_load_dwordx2 v[144:145], v[136:137], off nt
	global_load_dwordx2 v[142:143], v[136:137], off offset:512 nt
	global_load_dwordx2 v[140:141], v[136:137], off offset:1024 nt
	global_load_dwordx2 v[138:139], v[136:137], off offset:1536 nt
	global_load_dwordx2 v[134:135], v[126:127], off nt
	global_load_dwordx2 v[132:133], v[126:127], off offset:512 nt
	global_load_dwordx2 v[130:131], v[126:127], off offset:1024 nt
	global_load_dwordx2 v[128:129], v[126:127], off offset:1536 nt
	v_cndmask_b32_e64 v2, v2, v161, s[2:3]
	s_lshl_b32 s2, s38, 4
	v_cndmask_b32_e32 v2, v2, v160, vcc
	v_and_or_b32 v4, s2, 32, v156
	v_bfe_i32 v2, v2, 0, 16
	v_lshlrev_b32_e32 v4, 2, v4
	ds_bpermute_b32 v5, v4, v2
	ds_bpermute_b32 v4, v4, v2 offset:64
	s_waitcnt lgkmcnt(1)
	v_cndmask_b32_e64 v146, -1, v5, s[0:1]
	v_cmp_lt_i32_e32 vcc, -1, v146
	s_cmp_eq_u64 vcc, 0
	s_cselect_b64 s[2:3], -1, 0
	s_cmp_lg_u64 vcc, 0
	s_cselect_b64 s[30:31], -1, 0
	s_ff1_i32_b64 s16, vcc
	s_cbranch_vccz .LBB0_1935
	v_or_b32_e32 v2, s16, v155
	v_lshlrev_b32_e32 v2, 2, v2
	ds_bpermute_b32 v2, v2, v146
	s_mov_b32 s17, s7
	s_lshl_b64 s[14:15], s[16:17], 12
	s_add_u32 s14, s14, s36
	s_addc_u32 s15, s15, s37
	s_waitcnt lgkmcnt(0)
	v_max_i32_e32 v2, 0, v2
	v_lshl_add_u64 v[6:7], s[14:15], 0, v[2:3]
	v_lshlrev_b64 v[6:7], 11, v[6:7]
	v_lshl_add_u64 v[6:7], v[58:59], 0, v[6:7]
	global_load_dwordx2 v[124:125], v[6:7], off nt
	global_load_dwordx2 v[122:123], v[6:7], off offset:512 nt
	global_load_dwordx2 v[120:121], v[6:7], off offset:1024 nt
	global_load_dwordx2 v[118:119], v[6:7], off offset:1536 nt
.LBB0_1935:
	s_bcnt1_i32_b64 s6, vcc
	s_add_u32 s14, vcc_lo, -1
	s_addc_u32 s15, vcc_hi, -1
	s_and_b64 s[14:15], s[14:15], vcc
	s_and_b64 s[2:3], s[2:3], exec
	v_cmp_lt_u64_e64 s[2:3], s[6:7], 2
	s_cselect_b32 s16, 0, s16
	v_cmp_gt_u64_e64 s[28:29], s[6:7], 1
	s_and_b64 vcc, exec, s[2:3]
	s_cbranch_vccnz .LBB0_1937
	s_cmp_eq_u64 s[14:15], 0
	s_ff1_i32_b64 s2, s[14:15]
	s_cselect_b32 s2, s16, s2
	v_or_b32_e32 v2, s2, v155
	v_lshlrev_b32_e32 v2, 2, v2
	ds_bpermute_b32 v2, v2, v146
	s_lshl_b32 s2, s2, 12
	s_add_u32 s2, s2, s36
	s_addc_u32 s3, 0, s37
	s_waitcnt lgkmcnt(0)
	v_max_i32_e32 v2, 0, v2
	v_lshl_add_u64 v[6:7], s[2:3], 0, v[2:3]
	v_lshlrev_b64 v[6:7], 11, v[6:7]
	v_lshl_add_u64 v[6:7], v[58:59], 0, v[6:7]
	global_load_dwordx2 v[116:117], v[6:7], off nt
	global_load_dwordx2 v[114:115], v[6:7], off offset:512 nt
	global_load_dwordx2 v[112:113], v[6:7], off offset:1024 nt
	global_load_dwordx2 v[110:111], v[6:7], off offset:1536 nt
.LBB0_1937:
	s_add_u32 s2, s14, -1
	s_addc_u32 s3, s15, -1
	s_and_b64 s[2:3], s[2:3], s[14:15]
	v_cmp_lt_u64_e64 s[14:15], s[6:7], 3
	v_cmp_gt_u64_e64 s[26:27], s[6:7], 2
	s_and_b64 vcc, exec, s[14:15]
	s_cbranch_vccnz .LBB0_1939
	s_cmp_eq_u64 s[2:3], 0
	s_ff1_i32_b64 s14, s[2:3]
	s_cselect_b32 s14, s16, s14
	v_or_b32_e32 v2, s14, v155
	v_lshlrev_b32_e32 v2, 2, v2
	ds_bpermute_b32 v2, v2, v146
	s_lshl_b32 s14, s14, 12
	s_add_u32 s14, s14, s36
	s_addc_u32 s15, 0, s37
	s_waitcnt lgkmcnt(0)
	v_max_i32_e32 v2, 0, v2
	v_lshl_add_u64 v[6:7], s[14:15], 0, v[2:3]
	v_lshlrev_b64 v[6:7], 11, v[6:7]
	v_lshl_add_u64 v[6:7], v[58:59], 0, v[6:7]
	global_load_dwordx2 v[108:109], v[6:7], off nt
	global_load_dwordx2 v[106:107], v[6:7], off offset:512 nt
	global_load_dwordx2 v[104:105], v[6:7], off offset:1024 nt
	global_load_dwordx2 v[102:103], v[6:7], off offset:1536 nt
; template <int R, bool RT = false>
; __device__ __forceinline__ void norm_phase(const NormArgs& a, LAS unsigned char* lds, bool ctx_rows, const float* ctx_src, const float* ctx_shift, const float* ctx_scale) {
;     ...
;                 for (int q = 0; q < R; ++q) { mask[q] = __ballot(sl[q] >= 0); cnt[q] = __builtin_popcountll(mask[q]);
; #pragma unroll
;                     for (int i = 0; i < 4; ++i) { if (mask[q]) { ee[q][i] = __builtin_ctzll(mask[q]); mask[q] &= mask[q] - 1; wgt[q][i] = 1.f; } else { ee[q][i] = i ? ee[q][0] : 0; wgt[q][i] = 0.f; } }
; #pragma unroll
;                     for (int i = 0; i < 4; ++i) {
;                         if (i < cnt[q]) { int slot = __shfl(sl[q], ee[q][i]); slot = slot < 0 ? 0 : slot; const f16* yr = a.y2 + ((size_t)ee[q][i] * EROWS + b * CAP + slot) * DM + 4 * lane;
; #pragma unroll
;                             for (int j = 0; j < 4; ++j) ld[q][i][j] = *(const f16x4*)(yr + 256 * j); } } }
.LBB0_1939:
	s_add_u32 s14, s2, -1
	s_addc_u32 s15, s3, -1
	s_and_b64 s[2:3], s[14:15], s[2:3]
	v_cmp_lt_u64_e64 s[14:15], s[6:7], 4
	v_cmp_gt_u64_e64 s[24:25], s[6:7], 3
	s_and_b64 vcc, exec, s[14:15]
	s_cbranch_vccnz .LBB0_1941
	s_cmp_eq_u64 s[2:3], 0
	s_ff1_i32_b64 s6, s[2:3]
	s_cselect_b32 s6, s16, s6
	v_or_b32_e32 v2, s6, v155
	v_lshlrev_b32_e32 v2, 2, v2
	ds_bpermute_b32 v2, v2, v146
	s_lshl_b32 s6, s6, 12
	s_add_u32 s14, s6, s36
	s_addc_u32 s15, 0, s37
	s_waitcnt lgkmcnt(0)
	v_max_i32_e32 v2, 0, v2
	v_lshl_add_u64 v[6:7], s[14:15], 0, v[2:3]
	v_lshlrev_b64 v[6:7], 11, v[6:7]
	v_lshl_add_u64 v[6:7], v[58:59], 0, v[6:7]
	global_load_dwordx2 v[100:101], v[6:7], off nt
	global_load_dwordx2 v[98:99], v[6:7], off offset:512 nt
	global_load_dwordx2 v[96:97], v[6:7], off offset:1024 nt
	global_load_dwordx2 v[94:95], v[6:7], off offset:1536 nt
.LBB0_1941:
	s_waitcnt lgkmcnt(0)
	v_cndmask_b32_e64 v164, -1, v4, s[0:1]
	v_cmp_lt_i32_e32 vcc, -1, v164
	s_cmp_eq_u64 vcc, 0
	s_cselect_b64 s[14:15], -1, 0
	s_cmp_lg_u64 vcc, 0
	s_cselect_b64 s[22:23], -1, 0
	s_ff1_i32_b64 s18, vcc
	s_cbranch_vccz .LBB0_1943
	v_or_b32_e32 v2, s18, v155
	v_lshlrev_b32_e32 v2, 2, v2
	ds_bpermute_b32 v2, v2, v164
	s_mov_b32 s19, s7
	s_lshl_b64 s[16:17], s[18:19], 12
	s_add_u32 s16, s16, s36
	s_addc_u32 s17, s17, s37
	s_waitcnt lgkmcnt(0)
	v_max_i32_e32 v2, 0, v2
	v_lshl_add_u64 v[4:5], s[16:17], 0, v[2:3]
	v_lshlrev_b64 v[4:5], 11, v[4:5]
	v_lshl_add_u64 v[4:5], v[58:59], 0, v[4:5]
	global_load_dwordx2 v[92:93], v[4:5], off nt
	global_load_dwordx2 v[90:91], v[4:5], off offset:512 nt
	global_load_dwordx2 v[88:89], v[4:5], off offset:1024 nt
	global_load_dwordx2 v[86:87], v[4:5], off offset:1536 nt
.LBB0_1943:
	s_bcnt1_i32_b64 s6, vcc
	s_add_u32 s16, vcc_lo, -1
	s_addc_u32 s17, vcc_hi, -1
	s_and_b64 s[16:17], s[16:17], vcc
	s_and_b64 s[14:15], s[14:15], exec
	v_cmp_lt_u64_e64 s[14:15], s[6:7], 2
	s_cselect_b32 s39, 0, s18
	v_cmp_gt_u64_e64 s[20:21], s[6:7], 1
	s_and_b64 vcc, exec, s[14:15]
	s_cbranch_vccnz .LBB0_1945
	s_cmp_eq_u64 s[16:17], 0
	s_ff1_i32_b64 s14, s[16:17]
	s_cselect_b32 s14, s39, s14
	v_or_b32_e32 v2, s14, v155
	v_lshlrev_b32_e32 v2, 2, v2
	ds_bpermute_b32 v2, v2, v164
	s_lshl_b32 s14, s14, 12
	s_add_u32 s14, s14, s36
	s_addc_u32 s15, 0, s37
	s_waitcnt lgkmcnt(0)
	v_max_i32_e32 v2, 0, v2
	v_lshl_add_u64 v[4:5], s[14:15], 0, v[2:3]
	v_lshlrev_b64 v[4:5], 11, v[4:5]
	v_lshl_add_u64 v[4:5], v[58:59], 0, v[4:5]
	global_load_dwordx2 v[84:85], v[4:5], off nt
	global_load_dwordx2 v[82:83], v[4:5], off offset:512 nt
	global_load_dwordx2 v[80:81], v[4:5], off offset:1024 nt
	global_load_dwordx2 v[78:79], v[4:5], off offset:1536 nt
.LBB0_1945:
	s_add_u32 s14, s16, -1
	s_addc_u32 s15, s17, -1
	s_and_b64 s[14:15], s[14:15], s[16:17]
	v_cmp_lt_u64_e64 s[16:17], s[6:7], 3
	v_cmp_gt_u64_e64 s[18:19], s[6:7], 2
	s_and_b64 vcc, exec, s[16:17]
	s_cbranch_vccnz .LBB0_1947
	s_cmp_eq_u64 s[14:15], 0
	s_ff1_i32_b64 s16, s[14:15]
	s_cselect_b32 s16, s39, s16
	v_or_b32_e32 v2, s16, v155
	v_lshlrev_b32_e32 v2, 2, v2
	ds_bpermute_b32 v2, v2, v164
	s_lshl_b32 s16, s16, 12
	s_add_u32 s16, s16, s36
	s_addc_u32 s17, 0, s37
	s_waitcnt lgkmcnt(0)
	v_max_i32_e32 v2, 0, v2
	v_lshl_add_u64 v[4:5], s[16:17], 0, v[2:3]
	v_lshlrev_b64 v[4:5], 11, v[4:5]
	v_lshl_add_u64 v[4:5], v[58:59], 0, v[4:5]
	global_load_dwordx2 v[76:77], v[4:5], off nt
	global_load_dwordx2 v[74:75], v[4:5], off offset:512 nt
	global_load_dwordx2 v[72:73], v[4:5], off offset:1024 nt
	global_load_dwordx2 v[70:71], v[4:5], off offset:1536 nt
.LBB0_1947:
	s_add_u32 s16, s14, -1
	s_addc_u32 s17, s15, -1
	v_cmp_lt_u64_e64 s[40:41], s[6:7], 4
	s_and_b64 s[14:15], s[16:17], s[14:15]
	v_cmp_gt_u64_e64 s[16:17], s[6:7], 3
	s_and_b64 vcc, exec, s[40:41]
	s_cbranch_vccnz .LBB0_1949
	s_cmp_eq_u64 s[14:15], 0
	s_ff1_i32_b64 s6, s[14:15]
	s_cselect_b32 s6, s39, s6
	v_or_b32_e32 v2, s6, v155
	v_lshlrev_b32_e32 v2, 2, v2
	ds_bpermute_b32 v2, v2, v164
	s_lshl_b32 s6, s6, 12
	s_add_u32 s40, s6, s36
	s_addc_u32 s41, 0, s37
	s_waitcnt lgkmcnt(0)
	v_max_i32_e32 v2, 0, v2
	v_lshl_add_u64 v[4:5], s[40:41], 0, v[2:3]
	v_lshlrev_b64 v[4:5], 11, v[4:5]
	v_lshl_add_u64 v[4:5], v[58:59], 0, v[4:5]
	global_load_dwordx2 v[68:69], v[4:5], off nt
	global_load_dwordx2 v[66:67], v[4:5], off offset:512 nt
	global_load_dwordx2 v[64:65], v[4:5], off offset:1024 nt
	global_load_dwordx2 v[62:63], v[4:5], off offset:1536 nt

; template <int R, bool RT = false>
; __device__ __forceinline__ void norm_phase(const NormArgs& a, LAS unsigned char* lds, bool ctx_rows, const float* ctx_src, const float* ctx_shift, const float* ctx_scale) {
;     ...
;                     while (mask[q]) {
;                         const int e2 = __builtin_ctzll(mask[q]); mask[q] &= mask[q] - 1; const int slot = __shfl(sl[q], e2); const f16* yr = a.y2 + ((size_t)e2 * EROWS + b * CAP + slot) * DM + 4 * lane;
; #pragma unroll
;                         for (int j = 0; j < 4; ++j) { const f16x4 t = *(const f16x4*)(yr + 256 * j); cs[j][0] += (float)t[0]; cs[j][1] += (float)t[1]; cs[j][2] += (float)t[2]; cs[j][3] += (float)t[3]; }
;                     }
.LBB0_1957:
	s_ff1_i32_b64 s6, s[2:3]
	v_or_b32_e32 v2, s6, v155
	v_lshlrev_b32_e32 v2, 2, v2
	ds_bpermute_b32 v148, v2, v146
	s_add_u32 s24, s2, -1
	s_addc_u32 s25, s3, -1
	s_lshl_b32 s6, s6, 12
	s_add_u32 s26, s6, s36
	s_addc_u32 s27, 0, s37
	s_waitcnt lgkmcnt(0)
	v_ashrrev_i32_e32 v149, 31, v148
	v_lshl_add_u64 v[148:149], s[26:27], 0, v[148:149]
	v_lshlrev_b64 v[148:149], 11, v[148:149]
	v_lshl_add_u64 v[148:149], v[58:59], 0, v[148:149]
	global_load_dwordx2 v[150:151], v[148:149], off nt
	global_load_dwordx2 v[152:153], v[148:149], off offset:512 nt
	global_load_dwordx2 v[166:167], v[148:149], off offset:1024 nt
	s_nop 0
	global_load_dwordx2 v[148:149], v[148:149], off offset:1536 nt
	s_and_b64 s[2:3], s[24:25], s[2:3]
	s_cmp_lg_u64 s[2:3], 0
	s_waitcnt vmcnt(3)
	v_cvt_f32_f16_e32 v168, v150
	v_cvt_f32_f16_sdwa v169, v150 dst_sel:DWORD dst_unused:UNUSED_PAD src0_sel:WORD_1
	v_cvt_f32_f16_e32 v150, v151
	v_cvt_f32_f16_sdwa v151, v151 dst_sel:DWORD dst_unused:UNUSED_PAD src0_sel:WORD_1
	s_waitcnt vmcnt(2)
	v_cvt_f32_f16_e32 v170, v152
	v_cvt_f32_f16_sdwa v171, v152 dst_sel:DWORD dst_unused:UNUSED_PAD src0_sel:WORD_1
	v_cvt_f32_f16_e32 v152, v153
	v_cvt_f32_f16_sdwa v153, v153 dst_sel:DWORD dst_unused:UNUSED_PAD src0_sel:WORD_1
	s_waitcnt vmcnt(1)
	v_cvt_f32_f16_e32 v172, v166
	v_cvt_f32_f16_e32 v174, v167
	s_waitcnt vmcnt(0)
	v_cvt_f32_f16_e32 v176, v148
	v_cvt_f32_f16_e32 v178, v149
	v_cvt_f32_f16_sdwa v179, v149 dst_sel:DWORD dst_unused:UNUSED_PAD src0_sel:WORD_1
	v_cvt_f32_f16_sdwa v177, v148 dst_sel:DWORD dst_unused:UNUSED_PAD src0_sel:WORD_1
	v_cvt_f32_f16_sdwa v175, v167 dst_sel:DWORD dst_unused:UNUSED_PAD src0_sel:WORD_1
	v_cvt_f32_f16_sdwa v173, v166 dst_sel:DWORD dst_unused:UNUSED_PAD src0_sel:WORD_1
	v_pk_add_f32 v[18:19], v[18:19], v[178:179]
	v_pk_add_f32 v[16:17], v[16:17], v[176:177]
	v_pk_add_f32 v[14:15], v[14:15], v[174:175]
	v_pk_add_f32 v[12:13], v[12:13], v[172:173]
	v_pk_add_f32 v[10:11], v[10:11], v[152:153]
	v_pk_add_f32 v[8:9], v[8:9], v[170:171]
	v_pk_add_f32 v[6:7], v[6:7], v[150:151]
	v_pk_add_f32 v[4:5], v[4:5], v[168:169]
	s_cbranch_scc1 .LBB0_1957

; template <int R, bool RT = false>
; __device__ __forceinline__ void norm_phase(const NormArgs& a, LAS unsigned char* lds, bool ctx_rows, const float* ctx_src, const float* ctx_shift, const float* ctx_scale) {
;     ...
;                     while (mask[q]) {
;                         const int e2 = __builtin_ctzll(mask[q]); mask[q] &= mask[q] - 1; const int slot = __shfl(sl[q], e2); const f16* yr = a.y2 + ((size_t)e2 * EROWS + b * CAP + slot) * DM + 4 * lane;
; #pragma unroll
;                         for (int j = 0; j < 4; ++j) { const f16x4 t = *(const f16x4*)(yr + 256 * j); cs[j][0] += (float)t[0]; cs[j][1] += (float)t[1]; cs[j][2] += (float)t[2]; cs[j][3] += (float)t[3]; }
;                     }
.LBB0_1975:
	s_ff1_i32_b64 s6, s[14:15]
	v_or_b32_e32 v2, s6, v155
	v_lshlrev_b32_e32 v2, 2, v2
	ds_bpermute_b32 v136, v2, v164
	s_add_u32 s16, s14, -1
	s_addc_u32 s17, s15, -1
	s_lshl_b32 s6, s6, 12
	s_add_u32 s18, s6, s36
	s_addc_u32 s19, 0, s37
	s_waitcnt lgkmcnt(0)
	v_ashrrev_i32_e32 v137, 31, v136
	v_lshl_add_u64 v[136:137], s[18:19], 0, v[136:137]
	v_lshlrev_b64 v[136:137], 11, v[136:137]
	v_lshl_add_u64 v[136:137], v[58:59], 0, v[136:137]
	global_load_dwordx2 v[166:167], v[136:137], off nt
	global_load_dwordx2 v[168:169], v[136:137], off offset:512 nt
	global_load_dwordx2 v[170:171], v[136:137], off offset:1024 nt
	s_nop 0
	global_load_dwordx2 v[136:137], v[136:137], off offset:1536 nt
	s_and_b64 s[14:15], s[16:17], s[14:15]
	s_cmp_lg_u64 s[14:15], 0
	s_waitcnt vmcnt(3)
	v_cvt_f32_f16_e32 v172, v166
	v_cvt_f32_f16_sdwa v173, v166 dst_sel:DWORD dst_unused:UNUSED_PAD src0_sel:WORD_1
	v_cvt_f32_f16_e32 v166, v167
	v_cvt_f32_f16_sdwa v167, v167 dst_sel:DWORD dst_unused:UNUSED_PAD src0_sel:WORD_1
	s_waitcnt vmcnt(2)
	v_cvt_f32_f16_e32 v174, v168
	v_cvt_f32_f16_sdwa v175, v168 dst_sel:DWORD dst_unused:UNUSED_PAD src0_sel:WORD_1
	v_cvt_f32_f16_e32 v168, v169
	v_cvt_f32_f16_sdwa v169, v169 dst_sel:DWORD dst_unused:UNUSED_PAD src0_sel:WORD_1
	s_waitcnt vmcnt(1)
	v_cvt_f32_f16_e32 v176, v170
	v_cvt_f32_f16_e32 v178, v171
	s_waitcnt vmcnt(0)
	v_cvt_f32_f16_e32 v180, v136
	v_cvt_f32_f16_e32 v182, v137
	v_cvt_f32_f16_sdwa v183, v137 dst_sel:DWORD dst_unused:UNUSED_PAD src0_sel:WORD_1
	v_cvt_f32_f16_sdwa v181, v136 dst_sel:DWORD dst_unused:UNUSED_PAD src0_sel:WORD_1
	v_cvt_f32_f16_sdwa v179, v171 dst_sel:DWORD dst_unused:UNUSED_PAD src0_sel:WORD_1
	v_cvt_f32_f16_sdwa v177, v170 dst_sel:DWORD dst_unused:UNUSED_PAD src0_sel:WORD_1
	v_pk_add_f32 v[18:19], v[18:19], v[182:183]
	v_pk_add_f32 v[16:17], v[16:17], v[180:181]
	v_pk_add_f32 v[14:15], v[14:15], v[178:179]
	v_pk_add_f32 v[12:13], v[12:13], v[176:177]
	v_pk_add_f32 v[10:11], v[10:11], v[168:169]
	v_pk_add_f32 v[8:9], v[8:9], v[174:175]
	v_pk_add_f32 v[6:7], v[6:7], v[166:167]
	v_pk_add_f32 v[4:5], v[4:5], v[172:173]
	s_cbranch_scc1 .LBB0_1975

; template <int R, bool RT = false>
; __device__ __forceinline__ void norm_phase(const NormArgs& a, LAS unsigned char* lds, bool ctx_rows, const float* ctx_src, const float* ctx_shift, const float* ctx_scale) {
;     ...
;             float rstd[R];
; #pragma unroll
;             for (int q = 0; q < R; ++q) { float ss = 0.f;
; #pragma unroll
;                 for (int j = 0; j < 4; ++j) ss += (v[q][j][0] * v[q][j][0] + v[q][j][1] * v[q][j][1]) + (v[q][j][2] * v[q][j][2] + v[q][j][3] * v[q][j][3]);
;                 rstd[q] = __builtin_amdgcn_rsqf(wave_sum(ss) * (1.f / DM) + EPS);
;                 if constexpr (RT) rsel[q] = ((lane >> 4) == rr / 4) ? rstd[q] : rsel[q]; }
; #pragma unroll
;             for (int q = 0; q < R; ++q) { const int row = row0 + rr + q;
; #pragma unroll
;                 for (int j = 0; j < 4; ++j) v[q][j] = (v[q][j] * rstd[q]) * A[j] + Sh[j];
;                 if (a.fout) {
; #pragma unroll
;                     for (int j = 0; j < 4; ++j) *(f32x4*)(a.fout + (size_t)row * DM + 4 * lane + 256 * j) = v[q][j];
;                 }
.LBB0_1986:
	v_mul_f32_e32 v2, v147, v147
	v_mul_f32_e32 v126, v145, v145
	v_fmac_f32_e32 v2, v146, v146
	v_fmac_f32_e32 v126, v144, v144
	v_add_f32_e32 v2, v2, v126
	v_mul_f32_e32 v126, v149, v149
	v_mul_f32_e32 v127, v143, v143
	v_fmac_f32_e32 v126, v148, v148
	v_fmac_f32_e32 v127, v142, v142
	v_add_f32_e32 v126, v126, v127
	v_add_f32_e32 v2, v2, v126
	v_mul_f32_e32 v126, v151, v151
	v_mul_f32_e32 v127, v141, v141
	v_fmac_f32_e32 v126, v150, v150
	v_fmac_f32_e32 v127, v140, v140
	v_add_f32_e32 v126, v126, v127
	v_add_f32_e32 v2, v126, v2
	v_mul_f32_e32 v126, v153, v153
	v_mul_f32_e32 v127, v139, v139
	v_fmac_f32_e32 v126, v152, v152
	v_fmac_f32_e32 v127, v138, v138
	v_add_f32_e32 v126, v126, v127
	v_add_f32_e32 v2, v126, v2
	v_mov_b32_e32 v126, 0
	v_mul_f32_e32 v127, v11, v11
	v_add_f32_dpp v2, v2, v2 quad_perm:[1,0,3,2] row_mask:0xf bank_mask:0xf bound_ctrl:1
	v_fmac_f32_e32 v127, v10, v10
	s_and_b64 vcc, exec, s[2:3]
	v_add_f32_dpp v2, v2, v2 quad_perm:[2,3,0,1] row_mask:0xf bank_mask:0xf bound_ctrl:1
	s_nop 1
	v_add_f32_dpp v2, v2, v2 row_half_mirror row_mask:0xf bank_mask:0xf bound_ctrl:1
	s_nop 1
	v_add_f32_dpp v2, v2, v2 row_mirror row_mask:0xf bank_mask:0xf bound_ctrl:1
	s_nop 1
	v_mov_b32_dpp v126, v2 row_bcast:15 row_mask:0xa bank_mask:0xf
	v_add_f32_e32 v2, v2, v126
	v_mov_b32_e32 v126, 0
	s_nop 1
	v_mov_b32_dpp v126, v2 row_bcast:31 row_mask:0xc bank_mask:0xf
	v_add_f32_e32 v2, v2, v126
	v_mul_f32_e32 v126, v7, v7
	v_readlane_b32 s6, v2, 63
	v_mul_f32_e32 v2, v5, v5
	v_fmac_f32_e32 v2, v4, v4
	v_fmac_f32_e32 v126, v6, v6
	v_add_f32_e32 v2, v2, v126
	v_mul_f32_e32 v126, v9, v9
	v_fmac_f32_e32 v126, v8, v8
	v_add_f32_e32 v126, v126, v127
	v_add_f32_e32 v2, v2, v126
	v_mul_f32_e32 v126, v13, v13
	v_mul_f32_e32 v127, v15, v15
	v_fmac_f32_e32 v126, v12, v12
	v_fmac_f32_e32 v127, v14, v14
	v_add_f32_e32 v126, v126, v127
	v_add_f32_e32 v2, v126, v2
	v_mul_f32_e32 v126, v17, v17
	v_mul_f32_e32 v127, v19, v19
	v_fmac_f32_e32 v126, v16, v16
	v_fmac_f32_e32 v127, v18, v18
	v_add_f32_e32 v126, v126, v127
	v_add_f32_e32 v2, v126, v2
	v_mov_b32_e32 v126, 0
	s_nop 0
	v_add_f32_dpp v2, v2, v2 quad_perm:[1,0,3,2] row_mask:0xf bank_mask:0xf bound_ctrl:1
	s_nop 1
	v_add_f32_dpp v2, v2, v2 quad_perm:[2,3,0,1] row_mask:0xf bank_mask:0xf bound_ctrl:1
	s_nop 1
	v_add_f32_dpp v2, v2, v2 row_half_mirror row_mask:0xf bank_mask:0xf bound_ctrl:1
	s_nop 1
	v_add_f32_dpp v2, v2, v2 row_mirror row_mask:0xf bank_mask:0xf bound_ctrl:1
	s_nop 1
	v_mov_b32_dpp v126, v2 row_bcast:15 row_mask:0xa bank_mask:0xf
	v_add_f32_e32 v2, v2, v126
	v_mov_b32_e32 v126, 0
	s_nop 1
	v_mov_b32_dpp v126, v2 row_bcast:31 row_mask:0xc bank_mask:0xf
	v_add_f32_e32 v2, v2, v126
	s_nop 0
	v_readlane_b32 s2, v2, 63
	s_cbranch_vccnz .LBB0_1988
	v_fma_f32 v2, s6, v159, v158
	v_fma_f32 v126, s2, v159, v158
	v_rsq_f32_e32 v2, v2
	v_rsq_f32_e32 v164, v126
	s_lshl_b64 s[2:3], s[12:13], 12
	v_lshl_add_u64 v[166:167], v[60:61], 0, s[2:3]
	v_pk_mul_f32 v[126:127], v[152:153], v[2:3] op_sel_hi:[1,0]
	v_pk_mul_f32 v[128:129], v[138:139], v[2:3] op_sel_hi:[1,0]
	v_pk_mul_f32 v[132:133], v[140:141], v[2:3] op_sel_hi:[1,0]
	v_pk_mul_f32 v[138:139], v[146:147], v[2:3] op_sel_hi:[1,0]
	v_pk_mul_f32 v[140:141], v[144:145], v[2:3] op_sel_hi:[1,0]
	v_pk_fma_f32 v[126:127], v[40:41], v[126:127], 0 op_sel_hi:[1,1,0]
	v_pk_mul_f32 v[130:131], v[150:151], v[2:3] op_sel_hi:[1,0]
	v_pk_mul_f32 v[134:135], v[148:149], v[2:3] op_sel_hi:[1,0]
	v_pk_mul_f32 v[136:137], v[142:143], v[2:3] op_sel_hi:[1,0]
	v_pk_fma_f32 v[140:141], v[22:23], v[140:141], 0 op_sel_hi:[1,1,0]
	v_pk_fma_f32 v[138:139], v[20:21], v[138:139], 0 op_sel_hi:[1,1,0]
	s_lshl_b64 s[2:3], s[4:5], 12
	v_pk_mul_f32 v[4:5], v[4:5], v[164:165] op_sel_hi:[1,0]
	v_pk_mul_f32 v[6:7], v[6:7], v[164:165] op_sel_hi:[1,0]
	v_pk_fma_f32 v[128:129], v[42:43], v[128:129], 0 op_sel_hi:[1,1,0]
	v_pk_fma_f32 v[132:133], v[38:39], v[132:133], 0 op_sel_hi:[1,1,0]
	v_pk_fma_f32 v[130:131], v[36:37], v[130:131], 0 op_sel_hi:[1,1,0]
	v_pk_fma_f32 v[136:137], v[26:27], v[136:137], 0 op_sel_hi:[1,1,0]
	v_pk_fma_f32 v[134:135], v[24:25], v[134:135], 0 op_sel_hi:[1,1,0]
	global_store_dwordx4 v[166:167], v[138:141], off nt
	global_store_dwordx4 v[166:167], v[134:137], off offset:1024 nt
	global_store_dwordx4 v[166:167], v[130:133], off offset:2048 nt
	global_store_dwordx4 v[166:167], v[126:129], off offset:3072 nt
	v_pk_mul_f32 v[16:17], v[16:17], v[164:165] op_sel_hi:[1,0]
	v_pk_mul_f32 v[18:19], v[18:19], v[164:165] op_sel_hi:[1,0]
	v_lshl_add_u64 v[126:127], v[60:61], 0, s[2:3]
	v_pk_mul_f32 v[12:13], v[12:13], v[164:165] op_sel_hi:[1,0]
	v_pk_mul_f32 v[14:15], v[14:15], v[164:165] op_sel_hi:[1,0]
	v_pk_mul_f32 v[8:9], v[8:9], v[164:165] op_sel_hi:[1,0]
	v_pk_mul_f32 v[10:11], v[10:11], v[164:165] op_sel_hi:[1,0]
	v_pk_fma_f32 v[6:7], v[22:23], v[6:7], 0 op_sel_hi:[1,1,0]
	v_pk_fma_f32 v[4:5], v[20:21], v[4:5], 0 op_sel_hi:[1,1,0]
	v_pk_fma_f32 v[18:19], v[42:43], v[18:19], 0 op_sel_hi:[1,1,0]
	v_pk_fma_f32 v[16:17], v[40:41], v[16:17], 0 op_sel_hi:[1,1,0]
	v_pk_fma_f32 v[14:15], v[38:39], v[14:15], 0 op_sel_hi:[1,1,0]
	v_pk_fma_f32 v[12:13], v[36:37], v[12:13], 0 op_sel_hi:[1,1,0]
	v_pk_fma_f32 v[10:11], v[26:27], v[10:11], 0 op_sel_hi:[1,1,0]
	v_pk_fma_f32 v[8:9], v[24:25], v[8:9], 0 op_sel_hi:[1,1,0]
	global_store_dwordx4 v[126:127], v[4:7], off nt
	global_store_dwordx4 v[126:127], v[8:11], off offset:1024 nt
	global_store_dwordx4 v[126:127], v[12:15], off offset:2048 nt
	global_store_dwordx4 v[126:127], v[16:19], off offset:3072 nt
